# proj A/B/out epilogues: all gate/residual loads issued ahead with counted waits; MoE unit loops: ballot expert search, bias rows loaded before the K-loop
# speedup vs baseline: 1.0172x; 1.0172x over previous
.LBB0_1132:
	v_lshl_add_u32 v150, s26, 8, v158
	v_lshl_or_b32 v148, s51, 8, v163
	v_mov_b64_e32 v[152:153], s[96:97]
	v_ashrrev_i32_e32 v149, 31, v148
	v_lshlrev_b64 v[146:147], 1, v[148:149]
	v_or_b32_e32 v148, 0x80, v148
	v_ashrrev_i32_e32 v149, 31, v148
	v_lshlrev_b64 v[148:149], 1, v[148:149]
	v_mov_b32_e32 v168, v150
	v_mad_i64_i32 v[172:173], s[0:1], v168, s50, v[152:153]
	v_lshl_add_u64 v[172:173], v[172:173], 0, s[16:17]
	v_lshl_add_u64 v[174:175], v[172:173], 0, v[146:147]
	global_load_dwordx4 v[176:179], v[174:175], off
	v_lshl_add_u64 v[174:175], v[172:173], 0, v[148:149]
	global_load_dwordx4 v[180:183], v[174:175], off
	v_or_b32_e32 v168, 16, v150
	v_mad_i64_i32 v[172:173], s[0:1], v168, s50, v[152:153]
	v_lshl_add_u64 v[172:173], v[172:173], 0, s[16:17]
	v_lshl_add_u64 v[174:175], v[172:173], 0, v[146:147]
	global_load_dwordx4 v[184:187], v[174:175], off
	v_lshl_add_u64 v[174:175], v[172:173], 0, v[148:149]
	global_load_dwordx4 v[188:191], v[174:175], off
	v_or_b32_e32 v168, 32, v150
	v_mad_i64_i32 v[172:173], s[0:1], v168, s50, v[152:153]
	v_lshl_add_u64 v[172:173], v[172:173], 0, s[16:17]
	v_lshl_add_u64 v[174:175], v[172:173], 0, v[146:147]
	global_load_dwordx4 v[192:195], v[174:175], off
	v_lshl_add_u64 v[174:175], v[172:173], 0, v[148:149]
	global_load_dwordx4 v[196:199], v[174:175], off
	v_or_b32_e32 v168, 48, v150
	v_mad_i64_i32 v[172:173], s[0:1], v168, s50, v[152:153]
	v_lshl_add_u64 v[172:173], v[172:173], 0, s[16:17]
	v_lshl_add_u64 v[174:175], v[172:173], 0, v[146:147]
	global_load_dwordx4 v[200:203], v[174:175], off
	v_lshl_add_u64 v[174:175], v[172:173], 0, v[148:149]
	global_load_dwordx4 v[204:207], v[174:175], off
	v_or_b32_e32 v168, 128, v150
	v_mad_i64_i32 v[172:173], s[0:1], v168, s50, v[152:153]
	v_lshl_add_u64 v[172:173], v[172:173], 0, s[16:17]
	v_lshl_add_u64 v[174:175], v[172:173], 0, v[146:147]
	global_load_dwordx4 v[208:211], v[174:175], off
	v_lshl_add_u64 v[174:175], v[172:173], 0, v[148:149]
	global_load_dwordx4 v[212:215], v[174:175], off
	v_or_b32_e32 v168, 144, v150
	v_mad_i64_i32 v[172:173], s[0:1], v168, s50, v[152:153]
	v_lshl_add_u64 v[172:173], v[172:173], 0, s[16:17]
	v_lshl_add_u64 v[174:175], v[172:173], 0, v[146:147]
	global_load_dwordx4 v[216:219], v[174:175], off
	v_lshl_add_u64 v[174:175], v[172:173], 0, v[148:149]
	global_load_dwordx4 v[220:223], v[174:175], off
	v_or_b32_e32 v168, 160, v150
	v_mad_i64_i32 v[172:173], s[0:1], v168, s50, v[152:153]
	v_lshl_add_u64 v[172:173], v[172:173], 0, s[16:17]
	v_lshl_add_u64 v[174:175], v[172:173], 0, v[146:147]
	global_load_dwordx4 v[224:227], v[174:175], off
	v_lshl_add_u64 v[174:175], v[172:173], 0, v[148:149]
	global_load_dwordx4 v[228:231], v[174:175], off
	v_or_b32_e32 v168, 176, v150
	v_mad_i64_i32 v[172:173], s[0:1], v168, s50, v[152:153]
	v_lshl_add_u64 v[172:173], v[172:173], 0, s[16:17]
	v_lshl_add_u64 v[174:175], v[172:173], 0, v[146:147]
	global_load_dwordx4 v[232:235], v[174:175], off
	v_lshl_add_u64 v[174:175], v[172:173], 0, v[148:149]
	global_load_dwordx4 v[236:239], v[174:175], off
	s_waitcnt vmcnt(15)
	v_lshlrev_b32_e32 v0, 16, v176
	v_and_b32_e32 v151, 0xffff0000, v176
	v_lshlrev_b32_e32 v167, 16, v177
	v_and_b32_e32 v169, 0xffff0000, v177
	v_lshlrev_b32_e32 v170, 16, v178
	v_and_b32_e32 v171, 0xffff0000, v178
	v_lshlrev_b32_e32 v174, 16, v179
	v_and_b32_e32 v175, 0xffff0000, v179
	v_mul_f32_e32 v0, 0xbfb8aa3b, v0
	v_mul_f32_e32 v151, 0xbfb8aa3b, v151
	v_mul_f32_e32 v167, 0xbfb8aa3b, v167
	v_mul_f32_e32 v169, 0xbfb8aa3b, v169
	v_mul_f32_e32 v170, 0xbfb8aa3b, v170
	v_mul_f32_e32 v171, 0xbfb8aa3b, v171
	v_mul_f32_e32 v174, 0xbfb8aa3b, v174
	v_mul_f32_e32 v175, 0xbfb8aa3b, v175
	v_exp_f32_e32 v0, v0
	v_exp_f32_e32 v151, v151
	v_exp_f32_e32 v167, v167
	v_exp_f32_e32 v169, v169
	v_exp_f32_e32 v170, v170
	v_exp_f32_e32 v171, v171
	v_exp_f32_e32 v174, v174
	v_exp_f32_e32 v175, v175
	v_add_f32_e32 v0, 1.0, v0
	v_add_f32_e32 v151, 1.0, v151
	v_add_f32_e32 v167, 1.0, v167
	v_add_f32_e32 v169, 1.0, v169
	v_add_f32_e32 v170, 1.0, v170
	v_add_f32_e32 v171, 1.0, v171
	v_add_f32_e32 v174, 1.0, v174
	v_add_f32_e32 v175, 1.0, v175
	v_rcp_f32_e32 v0, v0
	v_rcp_f32_e32 v151, v151
	v_rcp_f32_e32 v167, v167
	v_rcp_f32_e32 v169, v169
	v_rcp_f32_e32 v170, v170
	v_rcp_f32_e32 v171, v171
	v_rcp_f32_e32 v174, v174
	v_rcp_f32_e32 v175, v175
	v_mul_f32_e32 v0, v126, v0
	v_mul_f32_e32 v151, v127, v151
	v_mul_f32_e32 v167, v128, v167
	v_mul_f32_e32 v169, v129, v169
	v_mul_f32_e32 v170, v122, v170
	v_mul_f32_e32 v171, v123, v171
	v_mul_f32_e32 v174, v124, v174
	v_mul_f32_e32 v175, v125, v175
	v_cvt_pk_bf16_f32 v126, v0, v151
	v_cvt_pk_bf16_f32 v127, v167, v169
	v_cvt_pk_bf16_f32 v128, v170, v171
	v_cvt_pk_bf16_f32 v129, v174, v175
	v_mov_b32_e32 v172, v150
	v_mov_b32_e32 v173, 0
	v_lshlrev_b64 v[172:173], 12, v[172:173]
	v_lshl_add_u64 v[172:173], s[6:7], 0, v[172:173]
	v_lshl_add_u64 v[172:173], v[172:173], 0, v[146:147]
	global_store_dwordx4 v[172:173], v[126:129], off
	s_waitcnt vmcnt(15)
	v_lshlrev_b32_e32 v0, 16, v180
	v_and_b32_e32 v151, 0xffff0000, v180
	v_lshlrev_b32_e32 v167, 16, v181
	v_and_b32_e32 v169, 0xffff0000, v181
	v_lshlrev_b32_e32 v170, 16, v182
	v_and_b32_e32 v171, 0xffff0000, v182
	v_lshlrev_b32_e32 v174, 16, v183
	v_and_b32_e32 v175, 0xffff0000, v183
	v_mul_f32_e32 v0, 0xbfb8aa3b, v0
	v_mul_f32_e32 v151, 0xbfb8aa3b, v151
	v_mul_f32_e32 v167, 0xbfb8aa3b, v167
	v_mul_f32_e32 v169, 0xbfb8aa3b, v169
	v_mul_f32_e32 v170, 0xbfb8aa3b, v170
	v_mul_f32_e32 v171, 0xbfb8aa3b, v171
	v_mul_f32_e32 v174, 0xbfb8aa3b, v174
	v_mul_f32_e32 v175, 0xbfb8aa3b, v175
	v_exp_f32_e32 v0, v0
	v_exp_f32_e32 v151, v151
	v_exp_f32_e32 v167, v167
	v_exp_f32_e32 v169, v169
	v_exp_f32_e32 v170, v170
	v_exp_f32_e32 v171, v171
	v_exp_f32_e32 v174, v174
	v_exp_f32_e32 v175, v175
	v_add_f32_e32 v0, 1.0, v0
	v_add_f32_e32 v151, 1.0, v151
	v_add_f32_e32 v167, 1.0, v167
	v_add_f32_e32 v169, 1.0, v169
	v_add_f32_e32 v170, 1.0, v170
	v_add_f32_e32 v171, 1.0, v171
	v_add_f32_e32 v174, 1.0, v174
	v_add_f32_e32 v175, 1.0, v175
	v_rcp_f32_e32 v0, v0
	v_rcp_f32_e32 v151, v151
	v_rcp_f32_e32 v167, v167
	v_rcp_f32_e32 v169, v169
	v_rcp_f32_e32 v170, v170
	v_rcp_f32_e32 v171, v171
	v_rcp_f32_e32 v174, v174
	v_rcp_f32_e32 v175, v175
	v_mul_f32_e32 v0, v118, v0
	v_mul_f32_e32 v151, v119, v151
	v_mul_f32_e32 v167, v120, v167
	v_mul_f32_e32 v169, v121, v169
	v_mul_f32_e32 v170, v114, v170
	v_mul_f32_e32 v171, v115, v171
	v_mul_f32_e32 v174, v116, v174
	v_mul_f32_e32 v175, v117, v175
	v_cvt_pk_bf16_f32 v118, v0, v151
	v_cvt_pk_bf16_f32 v119, v167, v169
	v_cvt_pk_bf16_f32 v120, v170, v171
	v_cvt_pk_bf16_f32 v121, v174, v175
	global_store_dwordx4 v[172:173], v[118:121], off offset:256
	s_waitcnt vmcnt(15)
	v_lshlrev_b32_e32 v0, 16, v184
	v_and_b32_e32 v151, 0xffff0000, v184
	v_lshlrev_b32_e32 v167, 16, v185
	v_and_b32_e32 v169, 0xffff0000, v185
	v_lshlrev_b32_e32 v170, 16, v186
	v_and_b32_e32 v171, 0xffff0000, v186
	v_lshlrev_b32_e32 v174, 16, v187
	v_and_b32_e32 v175, 0xffff0000, v187
	v_mul_f32_e32 v0, 0xbfb8aa3b, v0
	v_mul_f32_e32 v151, 0xbfb8aa3b, v151
	v_mul_f32_e32 v167, 0xbfb8aa3b, v167
	v_mul_f32_e32 v169, 0xbfb8aa3b, v169
	v_mul_f32_e32 v170, 0xbfb8aa3b, v170
	v_mul_f32_e32 v171, 0xbfb8aa3b, v171
	v_mul_f32_e32 v174, 0xbfb8aa3b, v174
	v_mul_f32_e32 v175, 0xbfb8aa3b, v175
	v_exp_f32_e32 v0, v0
	v_exp_f32_e32 v151, v151
	v_exp_f32_e32 v167, v167
	v_exp_f32_e32 v169, v169
	v_exp_f32_e32 v170, v170
	v_exp_f32_e32 v171, v171
	v_exp_f32_e32 v174, v174
	v_exp_f32_e32 v175, v175
	v_add_f32_e32 v0, 1.0, v0
	v_add_f32_e32 v151, 1.0, v151
	v_add_f32_e32 v167, 1.0, v167
	v_add_f32_e32 v169, 1.0, v169
	v_add_f32_e32 v170, 1.0, v170
	v_add_f32_e32 v171, 1.0, v171
	v_add_f32_e32 v174, 1.0, v174
	v_add_f32_e32 v175, 1.0, v175
	v_rcp_f32_e32 v0, v0
	v_rcp_f32_e32 v151, v151
	v_rcp_f32_e32 v167, v167
	v_rcp_f32_e32 v169, v169
	v_rcp_f32_e32 v170, v170
	v_rcp_f32_e32 v171, v171
	v_rcp_f32_e32 v174, v174
	v_rcp_f32_e32 v175, v175
	v_mul_f32_e32 v0, v110, v0
	v_mul_f32_e32 v151, v111, v151
	v_mul_f32_e32 v167, v112, v167
	v_mul_f32_e32 v169, v113, v169
	v_mul_f32_e32 v170, v106, v170
	v_mul_f32_e32 v171, v107, v171
	v_mul_f32_e32 v174, v108, v174
	v_mul_f32_e32 v175, v109, v175
	v_cvt_pk_bf16_f32 v110, v0, v151
	v_cvt_pk_bf16_f32 v111, v167, v169
	v_cvt_pk_bf16_f32 v112, v170, v171
	v_cvt_pk_bf16_f32 v113, v174, v175
	v_or_b32_e32 v172, 16, v150
	v_mov_b32_e32 v173, 0
	v_lshlrev_b64 v[172:173], 12, v[172:173]
	v_lshl_add_u64 v[172:173], s[6:7], 0, v[172:173]
	v_lshl_add_u64 v[172:173], v[172:173], 0, v[146:147]
	global_store_dwordx4 v[172:173], v[110:113], off
	s_waitcnt vmcnt(15)
	v_lshlrev_b32_e32 v0, 16, v188
	v_and_b32_e32 v151, 0xffff0000, v188
	v_lshlrev_b32_e32 v167, 16, v189
	v_and_b32_e32 v169, 0xffff0000, v189
	v_lshlrev_b32_e32 v170, 16, v190
	v_and_b32_e32 v171, 0xffff0000, v190
	v_lshlrev_b32_e32 v174, 16, v191
	v_and_b32_e32 v175, 0xffff0000, v191
	v_mul_f32_e32 v0, 0xbfb8aa3b, v0
	v_mul_f32_e32 v151, 0xbfb8aa3b, v151
	v_mul_f32_e32 v167, 0xbfb8aa3b, v167
	v_mul_f32_e32 v169, 0xbfb8aa3b, v169
	v_mul_f32_e32 v170, 0xbfb8aa3b, v170
	v_mul_f32_e32 v171, 0xbfb8aa3b, v171
	v_mul_f32_e32 v174, 0xbfb8aa3b, v174
	v_mul_f32_e32 v175, 0xbfb8aa3b, v175
	v_exp_f32_e32 v0, v0
	v_exp_f32_e32 v151, v151
	v_exp_f32_e32 v167, v167
	v_exp_f32_e32 v169, v169
	v_exp_f32_e32 v170, v170
	v_exp_f32_e32 v171, v171
	v_exp_f32_e32 v174, v174
	v_exp_f32_e32 v175, v175
	v_add_f32_e32 v0, 1.0, v0
	v_add_f32_e32 v151, 1.0, v151
	v_add_f32_e32 v167, 1.0, v167
	v_add_f32_e32 v169, 1.0, v169
	v_add_f32_e32 v170, 1.0, v170
	v_add_f32_e32 v171, 1.0, v171
	v_add_f32_e32 v174, 1.0, v174
	v_add_f32_e32 v175, 1.0, v175
	v_rcp_f32_e32 v0, v0
	v_rcp_f32_e32 v151, v151
	v_rcp_f32_e32 v167, v167
	v_rcp_f32_e32 v169, v169
	v_rcp_f32_e32 v170, v170
	v_rcp_f32_e32 v171, v171
	v_rcp_f32_e32 v174, v174
	v_rcp_f32_e32 v175, v175
	v_mul_f32_e32 v0, v102, v0
	v_mul_f32_e32 v151, v103, v151
	v_mul_f32_e32 v167, v104, v167
	v_mul_f32_e32 v169, v105, v169
	v_mul_f32_e32 v170, v98, v170
	v_mul_f32_e32 v171, v99, v171
	v_mul_f32_e32 v174, v100, v174
	v_mul_f32_e32 v175, v101, v175
	v_cvt_pk_bf16_f32 v102, v0, v151
	v_cvt_pk_bf16_f32 v103, v167, v169
	v_cvt_pk_bf16_f32 v104, v170, v171
	v_cvt_pk_bf16_f32 v105, v174, v175
	global_store_dwordx4 v[172:173], v[102:105], off offset:256
	s_waitcnt vmcnt(15)
	v_lshlrev_b32_e32 v0, 16, v192
	v_and_b32_e32 v151, 0xffff0000, v192
	v_lshlrev_b32_e32 v167, 16, v193
	v_and_b32_e32 v169, 0xffff0000, v193
	v_lshlrev_b32_e32 v170, 16, v194
	v_and_b32_e32 v171, 0xffff0000, v194
	v_lshlrev_b32_e32 v174, 16, v195
	v_and_b32_e32 v175, 0xffff0000, v195
	v_mul_f32_e32 v0, 0xbfb8aa3b, v0
	v_mul_f32_e32 v151, 0xbfb8aa3b, v151
	v_mul_f32_e32 v167, 0xbfb8aa3b, v167
	v_mul_f32_e32 v169, 0xbfb8aa3b, v169
	v_mul_f32_e32 v170, 0xbfb8aa3b, v170
	v_mul_f32_e32 v171, 0xbfb8aa3b, v171
	v_mul_f32_e32 v174, 0xbfb8aa3b, v174
	v_mul_f32_e32 v175, 0xbfb8aa3b, v175
	v_exp_f32_e32 v0, v0
	v_exp_f32_e32 v151, v151
	v_exp_f32_e32 v167, v167
	v_exp_f32_e32 v169, v169
	v_exp_f32_e32 v170, v170
	v_exp_f32_e32 v171, v171
	v_exp_f32_e32 v174, v174
	v_exp_f32_e32 v175, v175
	v_add_f32_e32 v0, 1.0, v0
	v_add_f32_e32 v151, 1.0, v151
	v_add_f32_e32 v167, 1.0, v167
	v_add_f32_e32 v169, 1.0, v169
	v_add_f32_e32 v170, 1.0, v170
	v_add_f32_e32 v171, 1.0, v171
	v_add_f32_e32 v174, 1.0, v174
	v_add_f32_e32 v175, 1.0, v175
	v_rcp_f32_e32 v0, v0
	v_rcp_f32_e32 v151, v151
	v_rcp_f32_e32 v167, v167
	v_rcp_f32_e32 v169, v169
	v_rcp_f32_e32 v170, v170
	v_rcp_f32_e32 v171, v171
	v_rcp_f32_e32 v174, v174
	v_rcp_f32_e32 v175, v175
	v_mul_f32_e32 v0, v94, v0
	v_mul_f32_e32 v151, v95, v151
	v_mul_f32_e32 v167, v96, v167
	v_mul_f32_e32 v169, v97, v169
	v_mul_f32_e32 v170, v90, v170
	v_mul_f32_e32 v171, v91, v171
	v_mul_f32_e32 v174, v92, v174
	v_mul_f32_e32 v175, v93, v175
	v_cvt_pk_bf16_f32 v94, v0, v151
	v_cvt_pk_bf16_f32 v95, v167, v169
	v_cvt_pk_bf16_f32 v96, v170, v171
	v_cvt_pk_bf16_f32 v97, v174, v175
	v_or_b32_e32 v172, 32, v150
	v_mov_b32_e32 v173, 0
	v_lshlrev_b64 v[172:173], 12, v[172:173]
	v_lshl_add_u64 v[172:173], s[6:7], 0, v[172:173]
	v_lshl_add_u64 v[172:173], v[172:173], 0, v[146:147]
	global_store_dwordx4 v[172:173], v[94:97], off
	s_waitcnt vmcnt(15)
	v_lshlrev_b32_e32 v0, 16, v196
	v_and_b32_e32 v151, 0xffff0000, v196
	v_lshlrev_b32_e32 v167, 16, v197
	v_and_b32_e32 v169, 0xffff0000, v197
	v_lshlrev_b32_e32 v170, 16, v198
	v_and_b32_e32 v171, 0xffff0000, v198
	v_lshlrev_b32_e32 v174, 16, v199
	v_and_b32_e32 v175, 0xffff0000, v199
	v_mul_f32_e32 v0, 0xbfb8aa3b, v0
	v_mul_f32_e32 v151, 0xbfb8aa3b, v151
	v_mul_f32_e32 v167, 0xbfb8aa3b, v167
	v_mul_f32_e32 v169, 0xbfb8aa3b, v169
	v_mul_f32_e32 v170, 0xbfb8aa3b, v170
	v_mul_f32_e32 v171, 0xbfb8aa3b, v171
	v_mul_f32_e32 v174, 0xbfb8aa3b, v174
	v_mul_f32_e32 v175, 0xbfb8aa3b, v175
	v_exp_f32_e32 v0, v0
	v_exp_f32_e32 v151, v151
	v_exp_f32_e32 v167, v167
	v_exp_f32_e32 v169, v169
	v_exp_f32_e32 v170, v170
	v_exp_f32_e32 v171, v171
	v_exp_f32_e32 v174, v174
	v_exp_f32_e32 v175, v175
	v_add_f32_e32 v0, 1.0, v0
	v_add_f32_e32 v151, 1.0, v151
	v_add_f32_e32 v167, 1.0, v167
	v_add_f32_e32 v169, 1.0, v169
	v_add_f32_e32 v170, 1.0, v170
	v_add_f32_e32 v171, 1.0, v171
	v_add_f32_e32 v174, 1.0, v174
	v_add_f32_e32 v175, 1.0, v175
	v_rcp_f32_e32 v0, v0
	v_rcp_f32_e32 v151, v151
	v_rcp_f32_e32 v167, v167
	v_rcp_f32_e32 v169, v169
	v_rcp_f32_e32 v170, v170
	v_rcp_f32_e32 v171, v171
	v_rcp_f32_e32 v174, v174
	v_rcp_f32_e32 v175, v175
	v_mul_f32_e32 v0, v86, v0
	v_mul_f32_e32 v151, v87, v151
	v_mul_f32_e32 v167, v88, v167
	v_mul_f32_e32 v169, v89, v169
	v_mul_f32_e32 v170, v82, v170
	v_mul_f32_e32 v171, v83, v171
	v_mul_f32_e32 v174, v84, v174
	v_mul_f32_e32 v175, v85, v175
	v_cvt_pk_bf16_f32 v86, v0, v151
	v_cvt_pk_bf16_f32 v87, v167, v169
	v_cvt_pk_bf16_f32 v88, v170, v171
	v_cvt_pk_bf16_f32 v89, v174, v175
	global_store_dwordx4 v[172:173], v[86:89], off offset:256
	s_waitcnt vmcnt(15)
	v_lshlrev_b32_e32 v0, 16, v200
	v_and_b32_e32 v151, 0xffff0000, v200
	v_lshlrev_b32_e32 v167, 16, v201
	v_and_b32_e32 v169, 0xffff0000, v201
	v_lshlrev_b32_e32 v170, 16, v202
	v_and_b32_e32 v171, 0xffff0000, v202
	v_lshlrev_b32_e32 v174, 16, v203
	v_and_b32_e32 v175, 0xffff0000, v203
	v_mul_f32_e32 v0, 0xbfb8aa3b, v0
	v_mul_f32_e32 v151, 0xbfb8aa3b, v151
	v_mul_f32_e32 v167, 0xbfb8aa3b, v167
	v_mul_f32_e32 v169, 0xbfb8aa3b, v169
	v_mul_f32_e32 v170, 0xbfb8aa3b, v170
	v_mul_f32_e32 v171, 0xbfb8aa3b, v171
	v_mul_f32_e32 v174, 0xbfb8aa3b, v174
	v_mul_f32_e32 v175, 0xbfb8aa3b, v175
	v_exp_f32_e32 v0, v0
	v_exp_f32_e32 v151, v151
	v_exp_f32_e32 v167, v167
	v_exp_f32_e32 v169, v169
	v_exp_f32_e32 v170, v170
	v_exp_f32_e32 v171, v171
	v_exp_f32_e32 v174, v174
	v_exp_f32_e32 v175, v175
	v_add_f32_e32 v0, 1.0, v0
	v_add_f32_e32 v151, 1.0, v151
	v_add_f32_e32 v167, 1.0, v167
	v_add_f32_e32 v169, 1.0, v169
	v_add_f32_e32 v170, 1.0, v170
	v_add_f32_e32 v171, 1.0, v171
	v_add_f32_e32 v174, 1.0, v174
	v_add_f32_e32 v175, 1.0, v175
	v_rcp_f32_e32 v0, v0
	v_rcp_f32_e32 v151, v151
	v_rcp_f32_e32 v167, v167
	v_rcp_f32_e32 v169, v169
	v_rcp_f32_e32 v170, v170
	v_rcp_f32_e32 v171, v171
	v_rcp_f32_e32 v174, v174
	v_rcp_f32_e32 v175, v175
	v_mul_f32_e32 v0, v78, v0
	v_mul_f32_e32 v151, v79, v151
	v_mul_f32_e32 v167, v80, v167
	v_mul_f32_e32 v169, v81, v169
	v_mul_f32_e32 v170, v74, v170
	v_mul_f32_e32 v171, v75, v171
	v_mul_f32_e32 v174, v76, v174
	v_mul_f32_e32 v175, v77, v175
	v_cvt_pk_bf16_f32 v78, v0, v151
	v_cvt_pk_bf16_f32 v79, v167, v169
	v_cvt_pk_bf16_f32 v80, v170, v171
	v_cvt_pk_bf16_f32 v81, v174, v175
	v_or_b32_e32 v172, 48, v150
	v_mov_b32_e32 v173, 0
	v_lshlrev_b64 v[172:173], 12, v[172:173]
	v_lshl_add_u64 v[172:173], s[6:7], 0, v[172:173]
	v_lshl_add_u64 v[172:173], v[172:173], 0, v[146:147]
	global_store_dwordx4 v[172:173], v[78:81], off
	s_waitcnt vmcnt(15)
	v_lshlrev_b32_e32 v0, 16, v204
	v_and_b32_e32 v151, 0xffff0000, v204
	v_lshlrev_b32_e32 v167, 16, v205
	v_and_b32_e32 v169, 0xffff0000, v205
	v_lshlrev_b32_e32 v170, 16, v206
	v_and_b32_e32 v171, 0xffff0000, v206
	v_lshlrev_b32_e32 v174, 16, v207
	v_and_b32_e32 v175, 0xffff0000, v207
	v_mul_f32_e32 v0, 0xbfb8aa3b, v0
	v_mul_f32_e32 v151, 0xbfb8aa3b, v151
	v_mul_f32_e32 v167, 0xbfb8aa3b, v167
	v_mul_f32_e32 v169, 0xbfb8aa3b, v169
	v_mul_f32_e32 v170, 0xbfb8aa3b, v170
	v_mul_f32_e32 v171, 0xbfb8aa3b, v171
	v_mul_f32_e32 v174, 0xbfb8aa3b, v174
	v_mul_f32_e32 v175, 0xbfb8aa3b, v175
	v_exp_f32_e32 v0, v0
	v_exp_f32_e32 v151, v151
	v_exp_f32_e32 v167, v167
	v_exp_f32_e32 v169, v169
	v_exp_f32_e32 v170, v170
	v_exp_f32_e32 v171, v171
	v_exp_f32_e32 v174, v174
	v_exp_f32_e32 v175, v175
	v_add_f32_e32 v0, 1.0, v0
	v_add_f32_e32 v151, 1.0, v151
	v_add_f32_e32 v167, 1.0, v167
	v_add_f32_e32 v169, 1.0, v169
	v_add_f32_e32 v170, 1.0, v170
	v_add_f32_e32 v171, 1.0, v171
	v_add_f32_e32 v174, 1.0, v174
	v_add_f32_e32 v175, 1.0, v175
	v_rcp_f32_e32 v0, v0
	v_rcp_f32_e32 v151, v151
	v_rcp_f32_e32 v167, v167
	v_rcp_f32_e32 v169, v169
	v_rcp_f32_e32 v170, v170
	v_rcp_f32_e32 v171, v171
	v_rcp_f32_e32 v174, v174
	v_rcp_f32_e32 v175, v175
	v_mul_f32_e32 v0, v70, v0
	v_mul_f32_e32 v151, v71, v151
	v_mul_f32_e32 v167, v72, v167
	v_mul_f32_e32 v169, v73, v169
	v_mul_f32_e32 v170, v66, v170
	v_mul_f32_e32 v171, v67, v171
	v_mul_f32_e32 v174, v68, v174
	v_mul_f32_e32 v175, v69, v175
	v_cvt_pk_bf16_f32 v70, v0, v151
	v_cvt_pk_bf16_f32 v71, v167, v169
	v_cvt_pk_bf16_f32 v72, v170, v171
	v_cvt_pk_bf16_f32 v73, v174, v175
	global_store_dwordx4 v[172:173], v[70:73], off offset:256
	s_waitcnt vmcnt(15)
	v_lshlrev_b32_e32 v0, 16, v208
	v_and_b32_e32 v151, 0xffff0000, v208
	v_lshlrev_b32_e32 v167, 16, v209
	v_and_b32_e32 v169, 0xffff0000, v209
	v_lshlrev_b32_e32 v170, 16, v210
	v_and_b32_e32 v171, 0xffff0000, v210
	v_lshlrev_b32_e32 v174, 16, v211
	v_and_b32_e32 v175, 0xffff0000, v211
	v_mul_f32_e32 v0, 0xbfb8aa3b, v0
	v_mul_f32_e32 v151, 0xbfb8aa3b, v151
	v_mul_f32_e32 v167, 0xbfb8aa3b, v167
	v_mul_f32_e32 v169, 0xbfb8aa3b, v169
	v_mul_f32_e32 v170, 0xbfb8aa3b, v170
	v_mul_f32_e32 v171, 0xbfb8aa3b, v171
	v_mul_f32_e32 v174, 0xbfb8aa3b, v174
	v_mul_f32_e32 v175, 0xbfb8aa3b, v175
	v_exp_f32_e32 v0, v0
	v_exp_f32_e32 v151, v151
	v_exp_f32_e32 v167, v167
	v_exp_f32_e32 v169, v169
	v_exp_f32_e32 v170, v170
	v_exp_f32_e32 v171, v171
	v_exp_f32_e32 v174, v174
	v_exp_f32_e32 v175, v175
	v_add_f32_e32 v0, 1.0, v0
	v_add_f32_e32 v151, 1.0, v151
	v_add_f32_e32 v167, 1.0, v167
	v_add_f32_e32 v169, 1.0, v169
	v_add_f32_e32 v170, 1.0, v170
	v_add_f32_e32 v171, 1.0, v171
	v_add_f32_e32 v174, 1.0, v174
	v_add_f32_e32 v175, 1.0, v175
	v_rcp_f32_e32 v0, v0
	v_rcp_f32_e32 v151, v151
	v_rcp_f32_e32 v167, v167
	v_rcp_f32_e32 v169, v169
	v_rcp_f32_e32 v170, v170
	v_rcp_f32_e32 v171, v171
	v_rcp_f32_e32 v174, v174
	v_rcp_f32_e32 v175, v175
	v_mul_f32_e32 v0, v62, v0
	v_mul_f32_e32 v151, v63, v151
	v_mul_f32_e32 v167, v64, v167
	v_mul_f32_e32 v169, v65, v169
	v_mul_f32_e32 v170, v58, v170
	v_mul_f32_e32 v171, v59, v171
	v_mul_f32_e32 v174, v60, v174
	v_mul_f32_e32 v175, v61, v175
	v_cvt_pk_bf16_f32 v62, v0, v151
	v_cvt_pk_bf16_f32 v63, v167, v169
	v_cvt_pk_bf16_f32 v64, v170, v171
	v_cvt_pk_bf16_f32 v65, v174, v175
	v_or_b32_e32 v172, 128, v150
	v_mov_b32_e32 v173, 0
	v_lshlrev_b64 v[172:173], 12, v[172:173]
	v_lshl_add_u64 v[172:173], s[6:7], 0, v[172:173]
	v_lshl_add_u64 v[172:173], v[172:173], 0, v[146:147]
	global_store_dwordx4 v[172:173], v[62:65], off
	s_waitcnt vmcnt(15)
	v_lshlrev_b32_e32 v0, 16, v212
	v_and_b32_e32 v151, 0xffff0000, v212
	v_lshlrev_b32_e32 v167, 16, v213
	v_and_b32_e32 v169, 0xffff0000, v213
	v_lshlrev_b32_e32 v170, 16, v214
	v_and_b32_e32 v171, 0xffff0000, v214
	v_lshlrev_b32_e32 v174, 16, v215
	v_and_b32_e32 v175, 0xffff0000, v215
	v_mul_f32_e32 v0, 0xbfb8aa3b, v0
	v_mul_f32_e32 v151, 0xbfb8aa3b, v151
	v_mul_f32_e32 v167, 0xbfb8aa3b, v167
	v_mul_f32_e32 v169, 0xbfb8aa3b, v169
	v_mul_f32_e32 v170, 0xbfb8aa3b, v170
	v_mul_f32_e32 v171, 0xbfb8aa3b, v171
	v_mul_f32_e32 v174, 0xbfb8aa3b, v174
	v_mul_f32_e32 v175, 0xbfb8aa3b, v175
	v_exp_f32_e32 v0, v0
	v_exp_f32_e32 v151, v151
	v_exp_f32_e32 v167, v167
	v_exp_f32_e32 v169, v169
	v_exp_f32_e32 v170, v170
	v_exp_f32_e32 v171, v171
	v_exp_f32_e32 v174, v174
	v_exp_f32_e32 v175, v175
	v_add_f32_e32 v0, 1.0, v0
	v_add_f32_e32 v151, 1.0, v151
	v_add_f32_e32 v167, 1.0, v167
	v_add_f32_e32 v169, 1.0, v169
	v_add_f32_e32 v170, 1.0, v170
	v_add_f32_e32 v171, 1.0, v171
	v_add_f32_e32 v174, 1.0, v174
	v_add_f32_e32 v175, 1.0, v175
	v_rcp_f32_e32 v0, v0
	v_rcp_f32_e32 v151, v151
	v_rcp_f32_e32 v167, v167
	v_rcp_f32_e32 v169, v169
	v_rcp_f32_e32 v170, v170
	v_rcp_f32_e32 v171, v171
	v_rcp_f32_e32 v174, v174
	v_rcp_f32_e32 v175, v175
	v_mul_f32_e32 v0, v54, v0
	v_mul_f32_e32 v151, v55, v151
	v_mul_f32_e32 v167, v56, v167
	v_mul_f32_e32 v169, v57, v169
	v_mul_f32_e32 v170, v50, v170
	v_mul_f32_e32 v171, v51, v171
	v_mul_f32_e32 v174, v52, v174
	v_mul_f32_e32 v175, v53, v175
	v_cvt_pk_bf16_f32 v54, v0, v151
	v_cvt_pk_bf16_f32 v55, v167, v169
	v_cvt_pk_bf16_f32 v56, v170, v171
	v_cvt_pk_bf16_f32 v57, v174, v175
	global_store_dwordx4 v[172:173], v[54:57], off offset:256
	s_waitcnt vmcnt(15)
	v_lshlrev_b32_e32 v0, 16, v216
	v_and_b32_e32 v151, 0xffff0000, v216
	v_lshlrev_b32_e32 v167, 16, v217
	v_and_b32_e32 v169, 0xffff0000, v217
	v_lshlrev_b32_e32 v170, 16, v218
	v_and_b32_e32 v171, 0xffff0000, v218
	v_lshlrev_b32_e32 v174, 16, v219
	v_and_b32_e32 v175, 0xffff0000, v219
	v_mul_f32_e32 v0, 0xbfb8aa3b, v0
	v_mul_f32_e32 v151, 0xbfb8aa3b, v151
	v_mul_f32_e32 v167, 0xbfb8aa3b, v167
	v_mul_f32_e32 v169, 0xbfb8aa3b, v169
	v_mul_f32_e32 v170, 0xbfb8aa3b, v170
	v_mul_f32_e32 v171, 0xbfb8aa3b, v171
	v_mul_f32_e32 v174, 0xbfb8aa3b, v174
	v_mul_f32_e32 v175, 0xbfb8aa3b, v175
	v_exp_f32_e32 v0, v0
	v_exp_f32_e32 v151, v151
	v_exp_f32_e32 v167, v167
	v_exp_f32_e32 v169, v169
	v_exp_f32_e32 v170, v170
	v_exp_f32_e32 v171, v171
	v_exp_f32_e32 v174, v174
	v_exp_f32_e32 v175, v175
	v_add_f32_e32 v0, 1.0, v0
	v_add_f32_e32 v151, 1.0, v151
	v_add_f32_e32 v167, 1.0, v167
	v_add_f32_e32 v169, 1.0, v169
	v_add_f32_e32 v170, 1.0, v170
	v_add_f32_e32 v171, 1.0, v171
	v_add_f32_e32 v174, 1.0, v174
	v_add_f32_e32 v175, 1.0, v175
	v_rcp_f32_e32 v0, v0
	v_rcp_f32_e32 v151, v151
	v_rcp_f32_e32 v167, v167
	v_rcp_f32_e32 v169, v169
	v_rcp_f32_e32 v170, v170
	v_rcp_f32_e32 v171, v171
	v_rcp_f32_e32 v174, v174
	v_rcp_f32_e32 v175, v175
	v_mul_f32_e32 v0, v46, v0
	v_mul_f32_e32 v151, v47, v151
	v_mul_f32_e32 v167, v48, v167
	v_mul_f32_e32 v169, v49, v169
	v_mul_f32_e32 v170, v42, v170
	v_mul_f32_e32 v171, v43, v171
	v_mul_f32_e32 v174, v44, v174
	v_mul_f32_e32 v175, v45, v175
	v_cvt_pk_bf16_f32 v46, v0, v151
	v_cvt_pk_bf16_f32 v47, v167, v169
	v_cvt_pk_bf16_f32 v48, v170, v171
	v_cvt_pk_bf16_f32 v49, v174, v175
	v_or_b32_e32 v172, 144, v150
	v_mov_b32_e32 v173, 0
	v_lshlrev_b64 v[172:173], 12, v[172:173]
	v_lshl_add_u64 v[172:173], s[6:7], 0, v[172:173]
	v_lshl_add_u64 v[172:173], v[172:173], 0, v[146:147]
	global_store_dwordx4 v[172:173], v[46:49], off
	s_waitcnt vmcnt(15)
	v_lshlrev_b32_e32 v0, 16, v220
	v_and_b32_e32 v151, 0xffff0000, v220
	v_lshlrev_b32_e32 v167, 16, v221
	v_and_b32_e32 v169, 0xffff0000, v221
	v_lshlrev_b32_e32 v170, 16, v222
	v_and_b32_e32 v171, 0xffff0000, v222
	v_lshlrev_b32_e32 v174, 16, v223
	v_and_b32_e32 v175, 0xffff0000, v223
	v_mul_f32_e32 v0, 0xbfb8aa3b, v0
	v_mul_f32_e32 v151, 0xbfb8aa3b, v151
	v_mul_f32_e32 v167, 0xbfb8aa3b, v167
	v_mul_f32_e32 v169, 0xbfb8aa3b, v169
	v_mul_f32_e32 v170, 0xbfb8aa3b, v170
	v_mul_f32_e32 v171, 0xbfb8aa3b, v171
	v_mul_f32_e32 v174, 0xbfb8aa3b, v174
	v_mul_f32_e32 v175, 0xbfb8aa3b, v175
	v_exp_f32_e32 v0, v0
	v_exp_f32_e32 v151, v151
	v_exp_f32_e32 v167, v167
	v_exp_f32_e32 v169, v169
	v_exp_f32_e32 v170, v170
	v_exp_f32_e32 v171, v171
	v_exp_f32_e32 v174, v174
	v_exp_f32_e32 v175, v175
	v_add_f32_e32 v0, 1.0, v0
	v_add_f32_e32 v151, 1.0, v151
	v_add_f32_e32 v167, 1.0, v167
	v_add_f32_e32 v169, 1.0, v169
	v_add_f32_e32 v170, 1.0, v170
	v_add_f32_e32 v171, 1.0, v171
	v_add_f32_e32 v174, 1.0, v174
	v_add_f32_e32 v175, 1.0, v175
	v_rcp_f32_e32 v0, v0
	v_rcp_f32_e32 v151, v151
	v_rcp_f32_e32 v167, v167
	v_rcp_f32_e32 v169, v169
	v_rcp_f32_e32 v170, v170
	v_rcp_f32_e32 v171, v171
	v_rcp_f32_e32 v174, v174
	v_rcp_f32_e32 v175, v175
	v_mul_f32_e32 v0, v38, v0
	v_mul_f32_e32 v151, v39, v151
	v_mul_f32_e32 v167, v40, v167
	v_mul_f32_e32 v169, v41, v169
	v_mul_f32_e32 v170, v34, v170
	v_mul_f32_e32 v171, v35, v171
	v_mul_f32_e32 v174, v36, v174
	v_mul_f32_e32 v175, v37, v175
	v_cvt_pk_bf16_f32 v38, v0, v151
	v_cvt_pk_bf16_f32 v39, v167, v169
	v_cvt_pk_bf16_f32 v40, v170, v171
	v_cvt_pk_bf16_f32 v41, v174, v175
	global_store_dwordx4 v[172:173], v[38:41], off offset:256
	s_waitcnt vmcnt(15)
	v_lshlrev_b32_e32 v0, 16, v224
	v_and_b32_e32 v151, 0xffff0000, v224
	v_lshlrev_b32_e32 v167, 16, v225
	v_and_b32_e32 v169, 0xffff0000, v225
	v_lshlrev_b32_e32 v170, 16, v226
	v_and_b32_e32 v171, 0xffff0000, v226
	v_lshlrev_b32_e32 v174, 16, v227
	v_and_b32_e32 v175, 0xffff0000, v227
	v_mul_f32_e32 v0, 0xbfb8aa3b, v0
	v_mul_f32_e32 v151, 0xbfb8aa3b, v151
	v_mul_f32_e32 v167, 0xbfb8aa3b, v167
	v_mul_f32_e32 v169, 0xbfb8aa3b, v169
	v_mul_f32_e32 v170, 0xbfb8aa3b, v170
	v_mul_f32_e32 v171, 0xbfb8aa3b, v171
	v_mul_f32_e32 v174, 0xbfb8aa3b, v174
	v_mul_f32_e32 v175, 0xbfb8aa3b, v175
	v_exp_f32_e32 v0, v0
	v_exp_f32_e32 v151, v151
	v_exp_f32_e32 v167, v167
	v_exp_f32_e32 v169, v169
	v_exp_f32_e32 v170, v170
	v_exp_f32_e32 v171, v171
	v_exp_f32_e32 v174, v174
	v_exp_f32_e32 v175, v175
	v_add_f32_e32 v0, 1.0, v0
	v_add_f32_e32 v151, 1.0, v151
	v_add_f32_e32 v167, 1.0, v167
	v_add_f32_e32 v169, 1.0, v169
	v_add_f32_e32 v170, 1.0, v170
	v_add_f32_e32 v171, 1.0, v171
	v_add_f32_e32 v174, 1.0, v174
	v_add_f32_e32 v175, 1.0, v175
	v_rcp_f32_e32 v0, v0
	v_rcp_f32_e32 v151, v151
	v_rcp_f32_e32 v167, v167
	v_rcp_f32_e32 v169, v169
	v_rcp_f32_e32 v170, v170
	v_rcp_f32_e32 v171, v171
	v_rcp_f32_e32 v174, v174
	v_rcp_f32_e32 v175, v175
	v_mul_f32_e32 v0, v30, v0
	v_mul_f32_e32 v151, v31, v151
	v_mul_f32_e32 v167, v32, v167
	v_mul_f32_e32 v169, v33, v169
	v_mul_f32_e32 v170, v26, v170
	v_mul_f32_e32 v171, v27, v171
	v_mul_f32_e32 v174, v28, v174
	v_mul_f32_e32 v175, v29, v175
	v_cvt_pk_bf16_f32 v30, v0, v151
	v_cvt_pk_bf16_f32 v31, v167, v169
	v_cvt_pk_bf16_f32 v32, v170, v171
	v_cvt_pk_bf16_f32 v33, v174, v175
	v_or_b32_e32 v172, 160, v150
	v_mov_b32_e32 v173, 0
	v_lshlrev_b64 v[172:173], 12, v[172:173]
	v_lshl_add_u64 v[172:173], s[6:7], 0, v[172:173]
	v_lshl_add_u64 v[172:173], v[172:173], 0, v[146:147]
	global_store_dwordx4 v[172:173], v[30:33], off
	s_waitcnt vmcnt(15)
	v_lshlrev_b32_e32 v0, 16, v228
	v_and_b32_e32 v151, 0xffff0000, v228
	v_lshlrev_b32_e32 v167, 16, v229
	v_and_b32_e32 v169, 0xffff0000, v229
	v_lshlrev_b32_e32 v170, 16, v230
	v_and_b32_e32 v171, 0xffff0000, v230
	v_lshlrev_b32_e32 v174, 16, v231
	v_and_b32_e32 v175, 0xffff0000, v231
	v_mul_f32_e32 v0, 0xbfb8aa3b, v0
	v_mul_f32_e32 v151, 0xbfb8aa3b, v151
	v_mul_f32_e32 v167, 0xbfb8aa3b, v167
	v_mul_f32_e32 v169, 0xbfb8aa3b, v169
	v_mul_f32_e32 v170, 0xbfb8aa3b, v170
	v_mul_f32_e32 v171, 0xbfb8aa3b, v171
	v_mul_f32_e32 v174, 0xbfb8aa3b, v174
	v_mul_f32_e32 v175, 0xbfb8aa3b, v175
	v_exp_f32_e32 v0, v0
	v_exp_f32_e32 v151, v151
	v_exp_f32_e32 v167, v167
	v_exp_f32_e32 v169, v169
	v_exp_f32_e32 v170, v170
	v_exp_f32_e32 v171, v171
	v_exp_f32_e32 v174, v174
	v_exp_f32_e32 v175, v175
	v_add_f32_e32 v0, 1.0, v0
	v_add_f32_e32 v151, 1.0, v151
	v_add_f32_e32 v167, 1.0, v167
	v_add_f32_e32 v169, 1.0, v169
	v_add_f32_e32 v170, 1.0, v170
	v_add_f32_e32 v171, 1.0, v171
	v_add_f32_e32 v174, 1.0, v174
	v_add_f32_e32 v175, 1.0, v175
	v_rcp_f32_e32 v0, v0
	v_rcp_f32_e32 v151, v151
	v_rcp_f32_e32 v167, v167
	v_rcp_f32_e32 v169, v169
	v_rcp_f32_e32 v170, v170
	v_rcp_f32_e32 v171, v171
	v_rcp_f32_e32 v174, v174
	v_rcp_f32_e32 v175, v175
	v_mul_f32_e32 v0, v22, v0
	v_mul_f32_e32 v151, v23, v151
	v_mul_f32_e32 v167, v24, v167
	v_mul_f32_e32 v169, v25, v169
	v_mul_f32_e32 v170, v18, v170
	v_mul_f32_e32 v171, v19, v171
	v_mul_f32_e32 v174, v20, v174
	v_mul_f32_e32 v175, v21, v175
	v_cvt_pk_bf16_f32 v22, v0, v151
	v_cvt_pk_bf16_f32 v23, v167, v169
	v_cvt_pk_bf16_f32 v24, v170, v171
	v_cvt_pk_bf16_f32 v25, v174, v175
	global_store_dwordx4 v[172:173], v[22:25], off offset:256
	s_waitcnt vmcnt(15)
	v_lshlrev_b32_e32 v0, 16, v232
	v_and_b32_e32 v151, 0xffff0000, v232
	v_lshlrev_b32_e32 v167, 16, v233
	v_and_b32_e32 v169, 0xffff0000, v233
	v_lshlrev_b32_e32 v170, 16, v234
	v_and_b32_e32 v171, 0xffff0000, v234
	v_lshlrev_b32_e32 v174, 16, v235
	v_and_b32_e32 v175, 0xffff0000, v235
	v_mul_f32_e32 v0, 0xbfb8aa3b, v0
	v_mul_f32_e32 v151, 0xbfb8aa3b, v151
	v_mul_f32_e32 v167, 0xbfb8aa3b, v167
	v_mul_f32_e32 v169, 0xbfb8aa3b, v169
	v_mul_f32_e32 v170, 0xbfb8aa3b, v170
	v_mul_f32_e32 v171, 0xbfb8aa3b, v171
	v_mul_f32_e32 v174, 0xbfb8aa3b, v174
	v_mul_f32_e32 v175, 0xbfb8aa3b, v175
	v_exp_f32_e32 v0, v0
	v_exp_f32_e32 v151, v151
	v_exp_f32_e32 v167, v167
	v_exp_f32_e32 v169, v169
	v_exp_f32_e32 v170, v170
	v_exp_f32_e32 v171, v171
	v_exp_f32_e32 v174, v174
	v_exp_f32_e32 v175, v175
	v_add_f32_e32 v0, 1.0, v0
	v_add_f32_e32 v151, 1.0, v151
	v_add_f32_e32 v167, 1.0, v167
	v_add_f32_e32 v169, 1.0, v169
	v_add_f32_e32 v170, 1.0, v170
	v_add_f32_e32 v171, 1.0, v171
	v_add_f32_e32 v174, 1.0, v174
	v_add_f32_e32 v175, 1.0, v175
	v_rcp_f32_e32 v0, v0
	v_rcp_f32_e32 v151, v151
	v_rcp_f32_e32 v167, v167
	v_rcp_f32_e32 v169, v169
	v_rcp_f32_e32 v170, v170
	v_rcp_f32_e32 v171, v171
	v_rcp_f32_e32 v174, v174
	v_rcp_f32_e32 v175, v175
	v_mul_f32_e32 v0, v14, v0
	v_mul_f32_e32 v151, v15, v151
	v_mul_f32_e32 v167, v16, v167
	v_mul_f32_e32 v169, v17, v169
	v_mul_f32_e32 v170, v10, v170
	v_mul_f32_e32 v171, v11, v171
	v_mul_f32_e32 v174, v12, v174
	v_mul_f32_e32 v175, v13, v175
	v_cvt_pk_bf16_f32 v14, v0, v151
	v_cvt_pk_bf16_f32 v15, v167, v169
	v_cvt_pk_bf16_f32 v16, v170, v171
	v_cvt_pk_bf16_f32 v17, v174, v175
	v_or_b32_e32 v172, 176, v150
	v_mov_b32_e32 v173, 0
	v_lshlrev_b64 v[172:173], 12, v[172:173]
	v_lshl_add_u64 v[172:173], s[6:7], 0, v[172:173]
	v_lshl_add_u64 v[172:173], v[172:173], 0, v[146:147]
	global_store_dwordx4 v[172:173], v[14:17], off
	s_waitcnt vmcnt(15)
	v_lshlrev_b32_e32 v0, 16, v236
	v_and_b32_e32 v151, 0xffff0000, v236
	v_lshlrev_b32_e32 v167, 16, v237
	v_and_b32_e32 v169, 0xffff0000, v237
	v_lshlrev_b32_e32 v170, 16, v238
	v_and_b32_e32 v171, 0xffff0000, v238
	v_lshlrev_b32_e32 v174, 16, v239
	v_and_b32_e32 v175, 0xffff0000, v239
	v_mul_f32_e32 v0, 0xbfb8aa3b, v0
	v_mul_f32_e32 v151, 0xbfb8aa3b, v151
	v_mul_f32_e32 v167, 0xbfb8aa3b, v167
	v_mul_f32_e32 v169, 0xbfb8aa3b, v169
	v_mul_f32_e32 v170, 0xbfb8aa3b, v170
	v_mul_f32_e32 v171, 0xbfb8aa3b, v171
	v_mul_f32_e32 v174, 0xbfb8aa3b, v174
	v_mul_f32_e32 v175, 0xbfb8aa3b, v175
	v_exp_f32_e32 v0, v0
	v_exp_f32_e32 v151, v151
	v_exp_f32_e32 v167, v167
	v_exp_f32_e32 v169, v169
	v_exp_f32_e32 v170, v170
	v_exp_f32_e32 v171, v171
	v_exp_f32_e32 v174, v174
	v_exp_f32_e32 v175, v175
	v_add_f32_e32 v0, 1.0, v0
	v_add_f32_e32 v151, 1.0, v151
	v_add_f32_e32 v167, 1.0, v167
	v_add_f32_e32 v169, 1.0, v169
	v_add_f32_e32 v170, 1.0, v170
	v_add_f32_e32 v171, 1.0, v171
	v_add_f32_e32 v174, 1.0, v174
	v_add_f32_e32 v175, 1.0, v175
	v_rcp_f32_e32 v0, v0
	v_rcp_f32_e32 v151, v151
	v_rcp_f32_e32 v167, v167
	v_rcp_f32_e32 v169, v169
	v_rcp_f32_e32 v170, v170
	v_rcp_f32_e32 v171, v171
	v_rcp_f32_e32 v174, v174
	v_rcp_f32_e32 v175, v175
	v_mul_f32_e32 v0, v6, v0
	v_mul_f32_e32 v151, v7, v151
	v_mul_f32_e32 v167, v8, v167
	v_mul_f32_e32 v169, v9, v169
	v_mul_f32_e32 v170, v2, v170
	v_mul_f32_e32 v171, v3, v171
	v_mul_f32_e32 v174, v4, v174
	v_mul_f32_e32 v175, v5, v175
	v_cvt_pk_bf16_f32 v6, v0, v151
	v_cvt_pk_bf16_f32 v7, v167, v169
	v_cvt_pk_bf16_f32 v8, v170, v171
	v_cvt_pk_bf16_f32 v9, v174, v175
	global_store_dwordx4 v[172:173], v[6:9], off offset:256
	s_andn2_b64 vcc, exec, s[4:5]
	s_mov_b64 s[4:5], -1
	s_cbranch_vccnz .LBB0_1121
	s_andn2_b64 vcc, exec, s[10:11]
	s_cbranch_vccnz .LBB0_1120
	s_barrier
	s_branch .LBB0_1120

.LBB0_1156:
	v_lshl_add_u32 v150, s26, 8, v158
	v_lshl_or_b32 v148, s51, 8, v157
	v_mov_b64_e32 v[152:153], s[96:97]
	v_ashrrev_i32_e32 v149, 31, v148
	v_lshlrev_b64 v[146:147], 1, v[148:149]
	v_or_b32_e32 v148, 0x80, v148
	v_ashrrev_i32_e32 v149, 31, v148
	v_lshlrev_b64 v[148:149], 1, v[148:149]
	v_mov_b32_e32 v168, v150
	v_mad_i64_i32 v[172:173], s[0:1], v168, s50, v[152:153]
	v_lshl_add_u64 v[172:173], v[172:173], 0, s[16:17]
	v_mov_b32_e32 v169, 0
	v_lshlrev_b64 v[174:175], 12, v[168:169]
	v_lshl_add_u64 v[174:175], s[6:7], 0, v[174:175]
	v_lshl_add_u64 v[174:175], v[174:175], 0, v[146:147]
	v_lshl_add_u64 v[178:179], v[172:173], 0, v[146:147]
	global_load_dwordx4 v[180:183], v[178:179], off
	global_load_dwordx4 v[184:187], v[174:175], off
	v_lshl_add_u64 v[178:179], v[172:173], 0, v[148:149]
	global_load_dwordx4 v[188:191], v[178:179], off
	global_load_dwordx4 v[192:195], v[174:175], off offset:256
	v_or_b32_e32 v168, 16, v150
	v_mad_i64_i32 v[172:173], s[0:1], v168, s50, v[152:153]
	v_lshl_add_u64 v[172:173], v[172:173], 0, s[16:17]
	v_mov_b32_e32 v169, 0
	v_lshlrev_b64 v[174:175], 12, v[168:169]
	v_lshl_add_u64 v[174:175], s[6:7], 0, v[174:175]
	v_lshl_add_u64 v[174:175], v[174:175], 0, v[146:147]
	v_lshl_add_u64 v[178:179], v[172:173], 0, v[146:147]
	global_load_dwordx4 v[196:199], v[178:179], off
	global_load_dwordx4 v[200:203], v[174:175], off
	v_lshl_add_u64 v[178:179], v[172:173], 0, v[148:149]
	global_load_dwordx4 v[204:207], v[178:179], off
	global_load_dwordx4 v[208:211], v[174:175], off offset:256
	v_or_b32_e32 v168, 32, v150
	v_mad_i64_i32 v[172:173], s[0:1], v168, s50, v[152:153]
	v_lshl_add_u64 v[172:173], v[172:173], 0, s[16:17]
	v_mov_b32_e32 v169, 0
	v_lshlrev_b64 v[174:175], 12, v[168:169]
	v_lshl_add_u64 v[174:175], s[6:7], 0, v[174:175]
	v_lshl_add_u64 v[174:175], v[174:175], 0, v[146:147]
	v_lshl_add_u64 v[178:179], v[172:173], 0, v[146:147]
	global_load_dwordx4 v[212:215], v[178:179], off
	global_load_dwordx4 v[222:225], v[174:175], off
	v_lshl_add_u64 v[178:179], v[172:173], 0, v[148:149]
	global_load_dwordx4 v[226:229], v[178:179], off
	global_load_dwordx4 v[230:233], v[174:175], off offset:256
	v_or_b32_e32 v168, 48, v150
	v_mad_i64_i32 v[172:173], s[0:1], v168, s50, v[152:153]
	v_lshl_add_u64 v[172:173], v[172:173], 0, s[16:17]
	v_mov_b32_e32 v169, 0
	v_lshlrev_b64 v[174:175], 12, v[168:169]
	v_lshl_add_u64 v[174:175], s[6:7], 0, v[174:175]
	v_lshl_add_u64 v[174:175], v[174:175], 0, v[146:147]
	v_lshl_add_u64 v[178:179], v[172:173], 0, v[146:147]
	global_load_dwordx4 v[234:237], v[178:179], off
	global_load_dwordx4 v[238:241], v[174:175], off
	v_lshl_add_u64 v[178:179], v[172:173], 0, v[148:149]
	global_load_dwordx4 v[242:245], v[178:179], off
	global_load_dwordx4 v[246:249], v[174:175], off offset:256
	s_waitcnt vmcnt(14)
	v_lshlrev_b32_e32 v0, 16, v180
	v_and_b32_e32 v151, 0xffff0000, v180
	v_lshlrev_b32_e32 v160, 16, v181
	v_and_b32_e32 v161, 0xffff0000, v181
	v_lshlrev_b32_e32 v162, 16, v182
	v_and_b32_e32 v163, 0xffff0000, v182
	v_lshlrev_b32_e32 v164, 16, v183
	v_and_b32_e32 v165, 0xffff0000, v183
	v_mul_f32_e32 v0, 0xbfb8aa3b, v0
	v_mul_f32_e32 v151, 0xbfb8aa3b, v151
	v_mul_f32_e32 v160, 0xbfb8aa3b, v160
	v_mul_f32_e32 v161, 0xbfb8aa3b, v161
	v_mul_f32_e32 v162, 0xbfb8aa3b, v162
	v_mul_f32_e32 v163, 0xbfb8aa3b, v163
	v_mul_f32_e32 v164, 0xbfb8aa3b, v164
	v_mul_f32_e32 v165, 0xbfb8aa3b, v165
	v_exp_f32_e32 v0, v0
	v_exp_f32_e32 v151, v151
	v_exp_f32_e32 v160, v160
	v_exp_f32_e32 v161, v161
	v_exp_f32_e32 v162, v162
	v_exp_f32_e32 v163, v163
	v_exp_f32_e32 v164, v164
	v_exp_f32_e32 v165, v165
	v_add_f32_e32 v0, 1.0, v0
	v_add_f32_e32 v151, 1.0, v151
	v_add_f32_e32 v160, 1.0, v160
	v_add_f32_e32 v161, 1.0, v161
	v_add_f32_e32 v162, 1.0, v162
	v_add_f32_e32 v163, 1.0, v163
	v_add_f32_e32 v164, 1.0, v164
	v_add_f32_e32 v165, 1.0, v165
	v_rcp_f32_e32 v0, v0
	v_rcp_f32_e32 v151, v151
	v_rcp_f32_e32 v160, v160
	v_rcp_f32_e32 v161, v161
	v_rcp_f32_e32 v162, v162
	v_rcp_f32_e32 v163, v163
	v_rcp_f32_e32 v164, v164
	v_rcp_f32_e32 v165, v165
	v_lshlrev_b32_e32 v166, 16, v184
	v_and_b32_e32 v184, 0xffff0000, v184
	v_lshlrev_b32_e32 v167, 16, v185
	v_and_b32_e32 v185, 0xffff0000, v185
	v_lshlrev_b32_e32 v170, 16, v186
	v_and_b32_e32 v186, 0xffff0000, v186
	v_lshlrev_b32_e32 v171, 16, v187
	v_and_b32_e32 v187, 0xffff0000, v187
	v_fmac_f32_e32 v166, v126, v0
	v_fmac_f32_e32 v184, v127, v151
	v_fmac_f32_e32 v167, v128, v160
	v_fmac_f32_e32 v185, v129, v161
	v_fmac_f32_e32 v170, v122, v162
	v_fmac_f32_e32 v186, v123, v163
	v_fmac_f32_e32 v171, v124, v164
	v_fmac_f32_e32 v187, v125, v165
	v_cvt_pk_bf16_f32 v184, v166, v184
	v_cvt_pk_bf16_f32 v185, v167, v185
	v_cvt_pk_bf16_f32 v186, v170, v186
	v_cvt_pk_bf16_f32 v187, v171, v187
	v_mov_b32_e32 v176, v150
	v_mov_b32_e32 v177, 0
	v_lshlrev_b64 v[176:177], 12, v[176:177]
	v_lshl_add_u64 v[176:177], s[10:11], 0, v[176:177]
	v_lshl_add_u64 v[176:177], v[176:177], 0, v[146:147]
	global_store_dwordx4 v[176:177], v[184:187], off
	v_or_b32_e32 v168, 128, v150
	v_mad_i64_i32 v[172:173], s[0:1], v168, s50, v[152:153]
	v_lshl_add_u64 v[172:173], v[172:173], 0, s[16:17]
	v_mov_b32_e32 v169, 0
	v_lshlrev_b64 v[174:175], 12, v[168:169]
	v_lshl_add_u64 v[174:175], s[6:7], 0, v[174:175]
	v_lshl_add_u64 v[174:175], v[174:175], 0, v[146:147]
	v_lshl_add_u64 v[178:179], v[172:173], 0, v[146:147]
	global_load_dwordx4 v[122:125], v[178:179], off
	global_load_dwordx4 v[126:129], v[174:175], off
	s_waitcnt vmcnt(15)
	v_lshlrev_b32_e32 v0, 16, v188
	v_and_b32_e32 v151, 0xffff0000, v188
	v_lshlrev_b32_e32 v160, 16, v189
	v_and_b32_e32 v161, 0xffff0000, v189
	v_lshlrev_b32_e32 v162, 16, v190
	v_and_b32_e32 v163, 0xffff0000, v190
	v_lshlrev_b32_e32 v164, 16, v191
	v_and_b32_e32 v165, 0xffff0000, v191
	v_mul_f32_e32 v0, 0xbfb8aa3b, v0
	v_mul_f32_e32 v151, 0xbfb8aa3b, v151
	v_mul_f32_e32 v160, 0xbfb8aa3b, v160
	v_mul_f32_e32 v161, 0xbfb8aa3b, v161
	v_mul_f32_e32 v162, 0xbfb8aa3b, v162
	v_mul_f32_e32 v163, 0xbfb8aa3b, v163
	v_mul_f32_e32 v164, 0xbfb8aa3b, v164
	v_mul_f32_e32 v165, 0xbfb8aa3b, v165
	v_exp_f32_e32 v0, v0
	v_exp_f32_e32 v151, v151
	v_exp_f32_e32 v160, v160
	v_exp_f32_e32 v161, v161
	v_exp_f32_e32 v162, v162
	v_exp_f32_e32 v163, v163
	v_exp_f32_e32 v164, v164
	v_exp_f32_e32 v165, v165
	v_add_f32_e32 v0, 1.0, v0
	v_add_f32_e32 v151, 1.0, v151
	v_add_f32_e32 v160, 1.0, v160
	v_add_f32_e32 v161, 1.0, v161
	v_add_f32_e32 v162, 1.0, v162
	v_add_f32_e32 v163, 1.0, v163
	v_add_f32_e32 v164, 1.0, v164
	v_add_f32_e32 v165, 1.0, v165
	v_rcp_f32_e32 v0, v0
	v_rcp_f32_e32 v151, v151
	v_rcp_f32_e32 v160, v160
	v_rcp_f32_e32 v161, v161
	v_rcp_f32_e32 v162, v162
	v_rcp_f32_e32 v163, v163
	v_rcp_f32_e32 v164, v164
	v_rcp_f32_e32 v165, v165
	v_lshlrev_b32_e32 v166, 16, v192
	v_and_b32_e32 v192, 0xffff0000, v192
	v_lshlrev_b32_e32 v167, 16, v193
	v_and_b32_e32 v193, 0xffff0000, v193
	v_lshlrev_b32_e32 v170, 16, v194
	v_and_b32_e32 v194, 0xffff0000, v194
	v_lshlrev_b32_e32 v171, 16, v195
	v_and_b32_e32 v195, 0xffff0000, v195
	v_fmac_f32_e32 v166, v118, v0
	v_fmac_f32_e32 v192, v119, v151
	v_fmac_f32_e32 v167, v120, v160
	v_fmac_f32_e32 v193, v121, v161
	v_fmac_f32_e32 v170, v114, v162
	v_fmac_f32_e32 v194, v115, v163
	v_fmac_f32_e32 v171, v116, v164
	v_fmac_f32_e32 v195, v117, v165
	v_cvt_pk_bf16_f32 v192, v166, v192
	v_cvt_pk_bf16_f32 v193, v167, v193
	v_cvt_pk_bf16_f32 v194, v170, v194
	v_cvt_pk_bf16_f32 v195, v171, v195
	global_store_dwordx4 v[176:177], v[192:195], off offset:256
	v_lshl_add_u64 v[178:179], v[172:173], 0, v[148:149]
	global_load_dwordx4 v[114:117], v[178:179], off
	global_load_dwordx4 v[118:121], v[174:175], off offset:256
	s_waitcnt vmcnt(16)
	v_lshlrev_b32_e32 v0, 16, v196
	v_and_b32_e32 v151, 0xffff0000, v196
	v_lshlrev_b32_e32 v160, 16, v197
	v_and_b32_e32 v161, 0xffff0000, v197
	v_lshlrev_b32_e32 v162, 16, v198
	v_and_b32_e32 v163, 0xffff0000, v198
	v_lshlrev_b32_e32 v164, 16, v199
	v_and_b32_e32 v165, 0xffff0000, v199
	v_mul_f32_e32 v0, 0xbfb8aa3b, v0
	v_mul_f32_e32 v151, 0xbfb8aa3b, v151
	v_mul_f32_e32 v160, 0xbfb8aa3b, v160
	v_mul_f32_e32 v161, 0xbfb8aa3b, v161
	v_mul_f32_e32 v162, 0xbfb8aa3b, v162
	v_mul_f32_e32 v163, 0xbfb8aa3b, v163
	v_mul_f32_e32 v164, 0xbfb8aa3b, v164
	v_mul_f32_e32 v165, 0xbfb8aa3b, v165
	v_exp_f32_e32 v0, v0
	v_exp_f32_e32 v151, v151
	v_exp_f32_e32 v160, v160
	v_exp_f32_e32 v161, v161
	v_exp_f32_e32 v162, v162
	v_exp_f32_e32 v163, v163
	v_exp_f32_e32 v164, v164
	v_exp_f32_e32 v165, v165
	v_add_f32_e32 v0, 1.0, v0
	v_add_f32_e32 v151, 1.0, v151
	v_add_f32_e32 v160, 1.0, v160
	v_add_f32_e32 v161, 1.0, v161
	v_add_f32_e32 v162, 1.0, v162
	v_add_f32_e32 v163, 1.0, v163
	v_add_f32_e32 v164, 1.0, v164
	v_add_f32_e32 v165, 1.0, v165
	v_rcp_f32_e32 v0, v0
	v_rcp_f32_e32 v151, v151
	v_rcp_f32_e32 v160, v160
	v_rcp_f32_e32 v161, v161
	v_rcp_f32_e32 v162, v162
	v_rcp_f32_e32 v163, v163
	v_rcp_f32_e32 v164, v164
	v_rcp_f32_e32 v165, v165
	v_lshlrev_b32_e32 v166, 16, v200
	v_and_b32_e32 v200, 0xffff0000, v200
	v_lshlrev_b32_e32 v167, 16, v201
	v_and_b32_e32 v201, 0xffff0000, v201
	v_lshlrev_b32_e32 v170, 16, v202
	v_and_b32_e32 v202, 0xffff0000, v202
	v_lshlrev_b32_e32 v171, 16, v203
	v_and_b32_e32 v203, 0xffff0000, v203
	v_fmac_f32_e32 v166, v110, v0
	v_fmac_f32_e32 v200, v111, v151
	v_fmac_f32_e32 v167, v112, v160
	v_fmac_f32_e32 v201, v113, v161
	v_fmac_f32_e32 v170, v106, v162
	v_fmac_f32_e32 v202, v107, v163
	v_fmac_f32_e32 v171, v108, v164
	v_fmac_f32_e32 v203, v109, v165
	v_cvt_pk_bf16_f32 v200, v166, v200
	v_cvt_pk_bf16_f32 v201, v167, v201
	v_cvt_pk_bf16_f32 v202, v170, v202
	v_cvt_pk_bf16_f32 v203, v171, v203
	v_or_b32_e32 v176, 16, v150
	v_mov_b32_e32 v177, 0
	v_lshlrev_b64 v[176:177], 12, v[176:177]
	v_lshl_add_u64 v[176:177], s[10:11], 0, v[176:177]
	v_lshl_add_u64 v[176:177], v[176:177], 0, v[146:147]
	global_store_dwordx4 v[176:177], v[200:203], off
	v_or_b32_e32 v168, 144, v150
	v_mad_i64_i32 v[172:173], s[0:1], v168, s50, v[152:153]
	v_lshl_add_u64 v[172:173], v[172:173], 0, s[16:17]
	v_mov_b32_e32 v169, 0
	v_lshlrev_b64 v[174:175], 12, v[168:169]
	v_lshl_add_u64 v[174:175], s[6:7], 0, v[174:175]
	v_lshl_add_u64 v[174:175], v[174:175], 0, v[146:147]
	v_lshl_add_u64 v[178:179], v[172:173], 0, v[146:147]
	global_load_dwordx4 v[106:109], v[178:179], off
	global_load_dwordx4 v[110:113], v[174:175], off
	s_waitcnt vmcnt(17)
	v_lshlrev_b32_e32 v0, 16, v204
	v_and_b32_e32 v151, 0xffff0000, v204
	v_lshlrev_b32_e32 v160, 16, v205
	v_and_b32_e32 v161, 0xffff0000, v205
	v_lshlrev_b32_e32 v162, 16, v206
	v_and_b32_e32 v163, 0xffff0000, v206
	v_lshlrev_b32_e32 v164, 16, v207
	v_and_b32_e32 v165, 0xffff0000, v207
	v_mul_f32_e32 v0, 0xbfb8aa3b, v0
	v_mul_f32_e32 v151, 0xbfb8aa3b, v151
	v_mul_f32_e32 v160, 0xbfb8aa3b, v160
	v_mul_f32_e32 v161, 0xbfb8aa3b, v161
	v_mul_f32_e32 v162, 0xbfb8aa3b, v162
	v_mul_f32_e32 v163, 0xbfb8aa3b, v163
	v_mul_f32_e32 v164, 0xbfb8aa3b, v164
	v_mul_f32_e32 v165, 0xbfb8aa3b, v165
	v_exp_f32_e32 v0, v0
	v_exp_f32_e32 v151, v151
	v_exp_f32_e32 v160, v160
	v_exp_f32_e32 v161, v161
	v_exp_f32_e32 v162, v162
	v_exp_f32_e32 v163, v163
	v_exp_f32_e32 v164, v164
	v_exp_f32_e32 v165, v165
	v_add_f32_e32 v0, 1.0, v0
	v_add_f32_e32 v151, 1.0, v151
	v_add_f32_e32 v160, 1.0, v160
	v_add_f32_e32 v161, 1.0, v161
	v_add_f32_e32 v162, 1.0, v162
	v_add_f32_e32 v163, 1.0, v163
	v_add_f32_e32 v164, 1.0, v164
	v_add_f32_e32 v165, 1.0, v165
	v_rcp_f32_e32 v0, v0
	v_rcp_f32_e32 v151, v151
	v_rcp_f32_e32 v160, v160
	v_rcp_f32_e32 v161, v161
	v_rcp_f32_e32 v162, v162
	v_rcp_f32_e32 v163, v163
	v_rcp_f32_e32 v164, v164
	v_rcp_f32_e32 v165, v165
	v_lshlrev_b32_e32 v166, 16, v208
	v_and_b32_e32 v208, 0xffff0000, v208
	v_lshlrev_b32_e32 v167, 16, v209
	v_and_b32_e32 v209, 0xffff0000, v209
	v_lshlrev_b32_e32 v170, 16, v210
	v_and_b32_e32 v210, 0xffff0000, v210
	v_lshlrev_b32_e32 v171, 16, v211
	v_and_b32_e32 v211, 0xffff0000, v211
	v_fmac_f32_e32 v166, v102, v0
	v_fmac_f32_e32 v208, v103, v151
	v_fmac_f32_e32 v167, v104, v160
	v_fmac_f32_e32 v209, v105, v161
	v_fmac_f32_e32 v170, v98, v162
	v_fmac_f32_e32 v210, v99, v163
	v_fmac_f32_e32 v171, v100, v164
	v_fmac_f32_e32 v211, v101, v165
	v_cvt_pk_bf16_f32 v208, v166, v208
	v_cvt_pk_bf16_f32 v209, v167, v209
	v_cvt_pk_bf16_f32 v210, v170, v210
	v_cvt_pk_bf16_f32 v211, v171, v211
	global_store_dwordx4 v[176:177], v[208:211], off offset:256
	v_lshl_add_u64 v[178:179], v[172:173], 0, v[148:149]
	global_load_dwordx4 v[98:101], v[178:179], off
	global_load_dwordx4 v[102:105], v[174:175], off offset:256
	s_waitcnt vmcnt(18)
	v_lshlrev_b32_e32 v0, 16, v212
	v_and_b32_e32 v151, 0xffff0000, v212
	v_lshlrev_b32_e32 v160, 16, v213
	v_and_b32_e32 v161, 0xffff0000, v213
	v_lshlrev_b32_e32 v162, 16, v214
	v_and_b32_e32 v163, 0xffff0000, v214
	v_lshlrev_b32_e32 v164, 16, v215
	v_and_b32_e32 v165, 0xffff0000, v215
	v_mul_f32_e32 v0, 0xbfb8aa3b, v0
	v_mul_f32_e32 v151, 0xbfb8aa3b, v151
	v_mul_f32_e32 v160, 0xbfb8aa3b, v160
	v_mul_f32_e32 v161, 0xbfb8aa3b, v161
	v_mul_f32_e32 v162, 0xbfb8aa3b, v162
	v_mul_f32_e32 v163, 0xbfb8aa3b, v163
	v_mul_f32_e32 v164, 0xbfb8aa3b, v164
	v_mul_f32_e32 v165, 0xbfb8aa3b, v165
	v_exp_f32_e32 v0, v0
	v_exp_f32_e32 v151, v151
	v_exp_f32_e32 v160, v160
	v_exp_f32_e32 v161, v161
	v_exp_f32_e32 v162, v162
	v_exp_f32_e32 v163, v163
	v_exp_f32_e32 v164, v164
	v_exp_f32_e32 v165, v165
	v_add_f32_e32 v0, 1.0, v0
	v_add_f32_e32 v151, 1.0, v151
	v_add_f32_e32 v160, 1.0, v160
	v_add_f32_e32 v161, 1.0, v161
	v_add_f32_e32 v162, 1.0, v162
	v_add_f32_e32 v163, 1.0, v163
	v_add_f32_e32 v164, 1.0, v164
	v_add_f32_e32 v165, 1.0, v165
	v_rcp_f32_e32 v0, v0
	v_rcp_f32_e32 v151, v151
	v_rcp_f32_e32 v160, v160
	v_rcp_f32_e32 v161, v161
	v_rcp_f32_e32 v162, v162
	v_rcp_f32_e32 v163, v163
	v_rcp_f32_e32 v164, v164
	v_rcp_f32_e32 v165, v165
	v_lshlrev_b32_e32 v166, 16, v222
	v_and_b32_e32 v222, 0xffff0000, v222
	v_lshlrev_b32_e32 v167, 16, v223
	v_and_b32_e32 v223, 0xffff0000, v223
	v_lshlrev_b32_e32 v170, 16, v224
	v_and_b32_e32 v224, 0xffff0000, v224
	v_lshlrev_b32_e32 v171, 16, v225
	v_and_b32_e32 v225, 0xffff0000, v225
	v_fmac_f32_e32 v166, v94, v0
	v_fmac_f32_e32 v222, v95, v151
	v_fmac_f32_e32 v167, v96, v160
	v_fmac_f32_e32 v223, v97, v161
	v_fmac_f32_e32 v170, v90, v162
	v_fmac_f32_e32 v224, v91, v163
	v_fmac_f32_e32 v171, v92, v164
	v_fmac_f32_e32 v225, v93, v165
	v_cvt_pk_bf16_f32 v222, v166, v222
	v_cvt_pk_bf16_f32 v223, v167, v223
	v_cvt_pk_bf16_f32 v224, v170, v224
	v_cvt_pk_bf16_f32 v225, v171, v225
	v_or_b32_e32 v176, 32, v150
	v_mov_b32_e32 v177, 0
	v_lshlrev_b64 v[176:177], 12, v[176:177]
	v_lshl_add_u64 v[176:177], s[10:11], 0, v[176:177]
	v_lshl_add_u64 v[176:177], v[176:177], 0, v[146:147]
	global_store_dwordx4 v[176:177], v[222:225], off
	v_or_b32_e32 v168, 160, v150
	v_mad_i64_i32 v[172:173], s[0:1], v168, s50, v[152:153]
	v_lshl_add_u64 v[172:173], v[172:173], 0, s[16:17]
	v_mov_b32_e32 v169, 0
	v_lshlrev_b64 v[174:175], 12, v[168:169]
	v_lshl_add_u64 v[174:175], s[6:7], 0, v[174:175]
	v_lshl_add_u64 v[174:175], v[174:175], 0, v[146:147]
	v_lshl_add_u64 v[178:179], v[172:173], 0, v[146:147]
	global_load_dwordx4 v[90:93], v[178:179], off
	global_load_dwordx4 v[94:97], v[174:175], off
	s_waitcnt vmcnt(19)
	v_lshlrev_b32_e32 v0, 16, v226
	v_and_b32_e32 v151, 0xffff0000, v226
	v_lshlrev_b32_e32 v160, 16, v227
	v_and_b32_e32 v161, 0xffff0000, v227
	v_lshlrev_b32_e32 v162, 16, v228
	v_and_b32_e32 v163, 0xffff0000, v228
	v_lshlrev_b32_e32 v164, 16, v229
	v_and_b32_e32 v165, 0xffff0000, v229
	v_mul_f32_e32 v0, 0xbfb8aa3b, v0
	v_mul_f32_e32 v151, 0xbfb8aa3b, v151
	v_mul_f32_e32 v160, 0xbfb8aa3b, v160
	v_mul_f32_e32 v161, 0xbfb8aa3b, v161
	v_mul_f32_e32 v162, 0xbfb8aa3b, v162
	v_mul_f32_e32 v163, 0xbfb8aa3b, v163
	v_mul_f32_e32 v164, 0xbfb8aa3b, v164
	v_mul_f32_e32 v165, 0xbfb8aa3b, v165
	v_exp_f32_e32 v0, v0
	v_exp_f32_e32 v151, v151
	v_exp_f32_e32 v160, v160
	v_exp_f32_e32 v161, v161
	v_exp_f32_e32 v162, v162
	v_exp_f32_e32 v163, v163
	v_exp_f32_e32 v164, v164
	v_exp_f32_e32 v165, v165
	v_add_f32_e32 v0, 1.0, v0
	v_add_f32_e32 v151, 1.0, v151
	v_add_f32_e32 v160, 1.0, v160
	v_add_f32_e32 v161, 1.0, v161
	v_add_f32_e32 v162, 1.0, v162
	v_add_f32_e32 v163, 1.0, v163
	v_add_f32_e32 v164, 1.0, v164
	v_add_f32_e32 v165, 1.0, v165
	v_rcp_f32_e32 v0, v0
	v_rcp_f32_e32 v151, v151
	v_rcp_f32_e32 v160, v160
	v_rcp_f32_e32 v161, v161
	v_rcp_f32_e32 v162, v162
	v_rcp_f32_e32 v163, v163
	v_rcp_f32_e32 v164, v164
	v_rcp_f32_e32 v165, v165
	v_lshlrev_b32_e32 v166, 16, v230
	v_and_b32_e32 v230, 0xffff0000, v230
	v_lshlrev_b32_e32 v167, 16, v231
	v_and_b32_e32 v231, 0xffff0000, v231
	v_lshlrev_b32_e32 v170, 16, v232
	v_and_b32_e32 v232, 0xffff0000, v232
	v_lshlrev_b32_e32 v171, 16, v233
	v_and_b32_e32 v233, 0xffff0000, v233
	v_fmac_f32_e32 v166, v86, v0
	v_fmac_f32_e32 v230, v87, v151
	v_fmac_f32_e32 v167, v88, v160
	v_fmac_f32_e32 v231, v89, v161
	v_fmac_f32_e32 v170, v82, v162
	v_fmac_f32_e32 v232, v83, v163
	v_fmac_f32_e32 v171, v84, v164
	v_fmac_f32_e32 v233, v85, v165
	v_cvt_pk_bf16_f32 v230, v166, v230
	v_cvt_pk_bf16_f32 v231, v167, v231
	v_cvt_pk_bf16_f32 v232, v170, v232
	v_cvt_pk_bf16_f32 v233, v171, v233
	global_store_dwordx4 v[176:177], v[230:233], off offset:256
	v_lshl_add_u64 v[178:179], v[172:173], 0, v[148:149]
	global_load_dwordx4 v[82:85], v[178:179], off
	global_load_dwordx4 v[86:89], v[174:175], off offset:256
	s_waitcnt vmcnt(20)
	v_lshlrev_b32_e32 v0, 16, v234
	v_and_b32_e32 v151, 0xffff0000, v234
	v_lshlrev_b32_e32 v160, 16, v235
	v_and_b32_e32 v161, 0xffff0000, v235
	v_lshlrev_b32_e32 v162, 16, v236
	v_and_b32_e32 v163, 0xffff0000, v236
	v_lshlrev_b32_e32 v164, 16, v237
	v_and_b32_e32 v165, 0xffff0000, v237
	v_mul_f32_e32 v0, 0xbfb8aa3b, v0
	v_mul_f32_e32 v151, 0xbfb8aa3b, v151
	v_mul_f32_e32 v160, 0xbfb8aa3b, v160
	v_mul_f32_e32 v161, 0xbfb8aa3b, v161
	v_mul_f32_e32 v162, 0xbfb8aa3b, v162
	v_mul_f32_e32 v163, 0xbfb8aa3b, v163
	v_mul_f32_e32 v164, 0xbfb8aa3b, v164
	v_mul_f32_e32 v165, 0xbfb8aa3b, v165
	v_exp_f32_e32 v0, v0
	v_exp_f32_e32 v151, v151
	v_exp_f32_e32 v160, v160
	v_exp_f32_e32 v161, v161
	v_exp_f32_e32 v162, v162
	v_exp_f32_e32 v163, v163
	v_exp_f32_e32 v164, v164
	v_exp_f32_e32 v165, v165
	v_add_f32_e32 v0, 1.0, v0
	v_add_f32_e32 v151, 1.0, v151
	v_add_f32_e32 v160, 1.0, v160
	v_add_f32_e32 v161, 1.0, v161
	v_add_f32_e32 v162, 1.0, v162
	v_add_f32_e32 v163, 1.0, v163
	v_add_f32_e32 v164, 1.0, v164
	v_add_f32_e32 v165, 1.0, v165
	v_rcp_f32_e32 v0, v0
	v_rcp_f32_e32 v151, v151
	v_rcp_f32_e32 v160, v160
	v_rcp_f32_e32 v161, v161
	v_rcp_f32_e32 v162, v162
	v_rcp_f32_e32 v163, v163
	v_rcp_f32_e32 v164, v164
	v_rcp_f32_e32 v165, v165
	v_lshlrev_b32_e32 v166, 16, v238
	v_and_b32_e32 v238, 0xffff0000, v238
	v_lshlrev_b32_e32 v167, 16, v239
	v_and_b32_e32 v239, 0xffff0000, v239
	v_lshlrev_b32_e32 v170, 16, v240
	v_and_b32_e32 v240, 0xffff0000, v240
	v_lshlrev_b32_e32 v171, 16, v241
	v_and_b32_e32 v241, 0xffff0000, v241
	v_fmac_f32_e32 v166, v78, v0
	v_fmac_f32_e32 v238, v79, v151
	v_fmac_f32_e32 v167, v80, v160
	v_fmac_f32_e32 v239, v81, v161
	v_fmac_f32_e32 v170, v74, v162
	v_fmac_f32_e32 v240, v75, v163
	v_fmac_f32_e32 v171, v76, v164
	v_fmac_f32_e32 v241, v77, v165
	v_cvt_pk_bf16_f32 v238, v166, v238
	v_cvt_pk_bf16_f32 v239, v167, v239
	v_cvt_pk_bf16_f32 v240, v170, v240
	v_cvt_pk_bf16_f32 v241, v171, v241
	v_or_b32_e32 v176, 48, v150
	v_mov_b32_e32 v177, 0
	v_lshlrev_b64 v[176:177], 12, v[176:177]
	v_lshl_add_u64 v[176:177], s[10:11], 0, v[176:177]
	v_lshl_add_u64 v[176:177], v[176:177], 0, v[146:147]
	global_store_dwordx4 v[176:177], v[238:241], off
	v_or_b32_e32 v168, 176, v150
	v_mad_i64_i32 v[172:173], s[0:1], v168, s50, v[152:153]
	v_lshl_add_u64 v[172:173], v[172:173], 0, s[16:17]
	v_mov_b32_e32 v169, 0
	v_lshlrev_b64 v[174:175], 12, v[168:169]
	v_lshl_add_u64 v[174:175], s[6:7], 0, v[174:175]
	v_lshl_add_u64 v[174:175], v[174:175], 0, v[146:147]
	v_lshl_add_u64 v[178:179], v[172:173], 0, v[146:147]
	global_load_dwordx4 v[74:77], v[178:179], off
	global_load_dwordx4 v[78:81], v[174:175], off
	s_waitcnt vmcnt(21)
	v_lshlrev_b32_e32 v0, 16, v242
	v_and_b32_e32 v151, 0xffff0000, v242
	v_lshlrev_b32_e32 v160, 16, v243
	v_and_b32_e32 v161, 0xffff0000, v243
	v_lshlrev_b32_e32 v162, 16, v244
	v_and_b32_e32 v163, 0xffff0000, v244
	v_lshlrev_b32_e32 v164, 16, v245
	v_and_b32_e32 v165, 0xffff0000, v245
	v_mul_f32_e32 v0, 0xbfb8aa3b, v0
	v_mul_f32_e32 v151, 0xbfb8aa3b, v151
	v_mul_f32_e32 v160, 0xbfb8aa3b, v160
	v_mul_f32_e32 v161, 0xbfb8aa3b, v161
	v_mul_f32_e32 v162, 0xbfb8aa3b, v162
	v_mul_f32_e32 v163, 0xbfb8aa3b, v163
	v_mul_f32_e32 v164, 0xbfb8aa3b, v164
	v_mul_f32_e32 v165, 0xbfb8aa3b, v165
	v_exp_f32_e32 v0, v0
	v_exp_f32_e32 v151, v151
	v_exp_f32_e32 v160, v160
	v_exp_f32_e32 v161, v161
	v_exp_f32_e32 v162, v162
	v_exp_f32_e32 v163, v163
	v_exp_f32_e32 v164, v164
	v_exp_f32_e32 v165, v165
	v_add_f32_e32 v0, 1.0, v0
	v_add_f32_e32 v151, 1.0, v151
	v_add_f32_e32 v160, 1.0, v160
	v_add_f32_e32 v161, 1.0, v161
	v_add_f32_e32 v162, 1.0, v162
	v_add_f32_e32 v163, 1.0, v163
	v_add_f32_e32 v164, 1.0, v164
	v_add_f32_e32 v165, 1.0, v165
	v_rcp_f32_e32 v0, v0
	v_rcp_f32_e32 v151, v151
	v_rcp_f32_e32 v160, v160
	v_rcp_f32_e32 v161, v161
	v_rcp_f32_e32 v162, v162
	v_rcp_f32_e32 v163, v163
	v_rcp_f32_e32 v164, v164
	v_rcp_f32_e32 v165, v165
	v_lshlrev_b32_e32 v166, 16, v246
	v_and_b32_e32 v246, 0xffff0000, v246
	v_lshlrev_b32_e32 v167, 16, v247
	v_and_b32_e32 v247, 0xffff0000, v247
	v_lshlrev_b32_e32 v170, 16, v248
	v_and_b32_e32 v248, 0xffff0000, v248
	v_lshlrev_b32_e32 v171, 16, v249
	v_and_b32_e32 v249, 0xffff0000, v249
	v_fmac_f32_e32 v166, v70, v0
	v_fmac_f32_e32 v246, v71, v151
	v_fmac_f32_e32 v167, v72, v160
	v_fmac_f32_e32 v247, v73, v161
	v_fmac_f32_e32 v170, v66, v162
	v_fmac_f32_e32 v248, v67, v163
	v_fmac_f32_e32 v171, v68, v164
	v_fmac_f32_e32 v249, v69, v165
	v_cvt_pk_bf16_f32 v246, v166, v246
	v_cvt_pk_bf16_f32 v247, v167, v247
	v_cvt_pk_bf16_f32 v248, v170, v248
	v_cvt_pk_bf16_f32 v249, v171, v249
	global_store_dwordx4 v[176:177], v[246:249], off offset:256
	v_lshl_add_u64 v[178:179], v[172:173], 0, v[148:149]
	global_load_dwordx4 v[66:69], v[178:179], off
	global_load_dwordx4 v[70:73], v[174:175], off offset:256
	s_waitcnt vmcnt(21)
	v_lshlrev_b32_e32 v0, 16, v122
	v_and_b32_e32 v151, 0xffff0000, v122
	v_lshlrev_b32_e32 v160, 16, v123
	v_and_b32_e32 v161, 0xffff0000, v123
	v_lshlrev_b32_e32 v162, 16, v124
	v_and_b32_e32 v163, 0xffff0000, v124
	v_lshlrev_b32_e32 v164, 16, v125
	v_and_b32_e32 v165, 0xffff0000, v125
	v_mul_f32_e32 v0, 0xbfb8aa3b, v0
	v_mul_f32_e32 v151, 0xbfb8aa3b, v151
	v_mul_f32_e32 v160, 0xbfb8aa3b, v160
	v_mul_f32_e32 v161, 0xbfb8aa3b, v161
	v_mul_f32_e32 v162, 0xbfb8aa3b, v162
	v_mul_f32_e32 v163, 0xbfb8aa3b, v163
	v_mul_f32_e32 v164, 0xbfb8aa3b, v164
	v_mul_f32_e32 v165, 0xbfb8aa3b, v165
	v_exp_f32_e32 v0, v0
	v_exp_f32_e32 v151, v151
	v_exp_f32_e32 v160, v160
	v_exp_f32_e32 v161, v161
	v_exp_f32_e32 v162, v162
	v_exp_f32_e32 v163, v163
	v_exp_f32_e32 v164, v164
	v_exp_f32_e32 v165, v165
	v_add_f32_e32 v0, 1.0, v0
	v_add_f32_e32 v151, 1.0, v151
	v_add_f32_e32 v160, 1.0, v160
	v_add_f32_e32 v161, 1.0, v161
	v_add_f32_e32 v162, 1.0, v162
	v_add_f32_e32 v163, 1.0, v163
	v_add_f32_e32 v164, 1.0, v164
	v_add_f32_e32 v165, 1.0, v165
	v_rcp_f32_e32 v0, v0
	v_rcp_f32_e32 v151, v151
	v_rcp_f32_e32 v160, v160
	v_rcp_f32_e32 v161, v161
	v_rcp_f32_e32 v162, v162
	v_rcp_f32_e32 v163, v163
	v_rcp_f32_e32 v164, v164
	v_rcp_f32_e32 v165, v165
	v_lshlrev_b32_e32 v166, 16, v126
	v_and_b32_e32 v126, 0xffff0000, v126
	v_lshlrev_b32_e32 v167, 16, v127
	v_and_b32_e32 v127, 0xffff0000, v127
	v_lshlrev_b32_e32 v170, 16, v128
	v_and_b32_e32 v128, 0xffff0000, v128
	v_lshlrev_b32_e32 v171, 16, v129
	v_and_b32_e32 v129, 0xffff0000, v129
	v_fmac_f32_e32 v166, v62, v0
	v_fmac_f32_e32 v126, v63, v151
	v_fmac_f32_e32 v167, v64, v160
	v_fmac_f32_e32 v127, v65, v161
	v_fmac_f32_e32 v170, v58, v162
	v_fmac_f32_e32 v128, v59, v163
	v_fmac_f32_e32 v171, v60, v164
	v_fmac_f32_e32 v129, v61, v165
	v_cvt_pk_bf16_f32 v126, v166, v126
	v_cvt_pk_bf16_f32 v127, v167, v127
	v_cvt_pk_bf16_f32 v128, v170, v128
	v_cvt_pk_bf16_f32 v129, v171, v129
	v_or_b32_e32 v176, 128, v150
	v_mov_b32_e32 v177, 0
	v_lshlrev_b64 v[176:177], 12, v[176:177]
	v_lshl_add_u64 v[176:177], s[10:11], 0, v[176:177]
	v_lshl_add_u64 v[176:177], v[176:177], 0, v[146:147]
	global_store_dwordx4 v[176:177], v[126:129], off
	s_waitcnt vmcnt(19)
	v_lshlrev_b32_e32 v0, 16, v114
	v_and_b32_e32 v151, 0xffff0000, v114
	v_lshlrev_b32_e32 v160, 16, v115
	v_and_b32_e32 v161, 0xffff0000, v115
	v_lshlrev_b32_e32 v162, 16, v116
	v_and_b32_e32 v163, 0xffff0000, v116
	v_lshlrev_b32_e32 v164, 16, v117
	v_and_b32_e32 v165, 0xffff0000, v117
	v_mul_f32_e32 v0, 0xbfb8aa3b, v0
	v_mul_f32_e32 v151, 0xbfb8aa3b, v151
	v_mul_f32_e32 v160, 0xbfb8aa3b, v160
	v_mul_f32_e32 v161, 0xbfb8aa3b, v161
	v_mul_f32_e32 v162, 0xbfb8aa3b, v162
	v_mul_f32_e32 v163, 0xbfb8aa3b, v163
	v_mul_f32_e32 v164, 0xbfb8aa3b, v164
	v_mul_f32_e32 v165, 0xbfb8aa3b, v165
	v_exp_f32_e32 v0, v0
	v_exp_f32_e32 v151, v151
	v_exp_f32_e32 v160, v160
	v_exp_f32_e32 v161, v161
	v_exp_f32_e32 v162, v162
	v_exp_f32_e32 v163, v163
	v_exp_f32_e32 v164, v164
	v_exp_f32_e32 v165, v165
	v_add_f32_e32 v0, 1.0, v0
	v_add_f32_e32 v151, 1.0, v151
	v_add_f32_e32 v160, 1.0, v160
	v_add_f32_e32 v161, 1.0, v161
	v_add_f32_e32 v162, 1.0, v162
	v_add_f32_e32 v163, 1.0, v163
	v_add_f32_e32 v164, 1.0, v164
	v_add_f32_e32 v165, 1.0, v165
	v_rcp_f32_e32 v0, v0
	v_rcp_f32_e32 v151, v151
	v_rcp_f32_e32 v160, v160
	v_rcp_f32_e32 v161, v161
	v_rcp_f32_e32 v162, v162
	v_rcp_f32_e32 v163, v163
	v_rcp_f32_e32 v164, v164
	v_rcp_f32_e32 v165, v165
	v_lshlrev_b32_e32 v166, 16, v118
	v_and_b32_e32 v118, 0xffff0000, v118
	v_lshlrev_b32_e32 v167, 16, v119
	v_and_b32_e32 v119, 0xffff0000, v119
	v_lshlrev_b32_e32 v170, 16, v120
	v_and_b32_e32 v120, 0xffff0000, v120
	v_lshlrev_b32_e32 v171, 16, v121
	v_and_b32_e32 v121, 0xffff0000, v121
	v_fmac_f32_e32 v166, v54, v0
	v_fmac_f32_e32 v118, v55, v151
	v_fmac_f32_e32 v167, v56, v160
	v_fmac_f32_e32 v119, v57, v161
	v_fmac_f32_e32 v170, v50, v162
	v_fmac_f32_e32 v120, v51, v163
	v_fmac_f32_e32 v171, v52, v164
	v_fmac_f32_e32 v121, v53, v165
	v_cvt_pk_bf16_f32 v118, v166, v118
	v_cvt_pk_bf16_f32 v119, v167, v119
	v_cvt_pk_bf16_f32 v120, v170, v120
	v_cvt_pk_bf16_f32 v121, v171, v121
	global_store_dwordx4 v[176:177], v[118:121], off offset:256
	s_waitcnt vmcnt(17)
	v_lshlrev_b32_e32 v0, 16, v106
	v_and_b32_e32 v151, 0xffff0000, v106
	v_lshlrev_b32_e32 v160, 16, v107
	v_and_b32_e32 v161, 0xffff0000, v107
	v_lshlrev_b32_e32 v162, 16, v108
	v_and_b32_e32 v163, 0xffff0000, v108
	v_lshlrev_b32_e32 v164, 16, v109
	v_and_b32_e32 v165, 0xffff0000, v109
	v_mul_f32_e32 v0, 0xbfb8aa3b, v0
	v_mul_f32_e32 v151, 0xbfb8aa3b, v151
	v_mul_f32_e32 v160, 0xbfb8aa3b, v160
	v_mul_f32_e32 v161, 0xbfb8aa3b, v161
	v_mul_f32_e32 v162, 0xbfb8aa3b, v162
	v_mul_f32_e32 v163, 0xbfb8aa3b, v163
	v_mul_f32_e32 v164, 0xbfb8aa3b, v164
	v_mul_f32_e32 v165, 0xbfb8aa3b, v165
	v_exp_f32_e32 v0, v0
	v_exp_f32_e32 v151, v151
	v_exp_f32_e32 v160, v160
	v_exp_f32_e32 v161, v161
	v_exp_f32_e32 v162, v162
	v_exp_f32_e32 v163, v163
	v_exp_f32_e32 v164, v164
	v_exp_f32_e32 v165, v165
	v_add_f32_e32 v0, 1.0, v0
	v_add_f32_e32 v151, 1.0, v151
	v_add_f32_e32 v160, 1.0, v160
	v_add_f32_e32 v161, 1.0, v161
	v_add_f32_e32 v162, 1.0, v162
	v_add_f32_e32 v163, 1.0, v163
	v_add_f32_e32 v164, 1.0, v164
	v_add_f32_e32 v165, 1.0, v165
	v_rcp_f32_e32 v0, v0
	v_rcp_f32_e32 v151, v151
	v_rcp_f32_e32 v160, v160
	v_rcp_f32_e32 v161, v161
	v_rcp_f32_e32 v162, v162
	v_rcp_f32_e32 v163, v163
	v_rcp_f32_e32 v164, v164
	v_rcp_f32_e32 v165, v165
	v_lshlrev_b32_e32 v166, 16, v110
	v_and_b32_e32 v110, 0xffff0000, v110
	v_lshlrev_b32_e32 v167, 16, v111
	v_and_b32_e32 v111, 0xffff0000, v111
	v_lshlrev_b32_e32 v170, 16, v112
	v_and_b32_e32 v112, 0xffff0000, v112
	v_lshlrev_b32_e32 v171, 16, v113
	v_and_b32_e32 v113, 0xffff0000, v113
	v_fmac_f32_e32 v166, v46, v0
	v_fmac_f32_e32 v110, v47, v151
	v_fmac_f32_e32 v167, v48, v160
	v_fmac_f32_e32 v111, v49, v161
	v_fmac_f32_e32 v170, v42, v162
	v_fmac_f32_e32 v112, v43, v163
	v_fmac_f32_e32 v171, v44, v164
	v_fmac_f32_e32 v113, v45, v165
	v_cvt_pk_bf16_f32 v110, v166, v110
	v_cvt_pk_bf16_f32 v111, v167, v111
	v_cvt_pk_bf16_f32 v112, v170, v112
	v_cvt_pk_bf16_f32 v113, v171, v113
	v_or_b32_e32 v176, 144, v150
	v_mov_b32_e32 v177, 0
	v_lshlrev_b64 v[176:177], 12, v[176:177]
	v_lshl_add_u64 v[176:177], s[10:11], 0, v[176:177]
	v_lshl_add_u64 v[176:177], v[176:177], 0, v[146:147]
	global_store_dwordx4 v[176:177], v[110:113], off
	s_waitcnt vmcnt(15)
	v_lshlrev_b32_e32 v0, 16, v98
	v_and_b32_e32 v151, 0xffff0000, v98
	v_lshlrev_b32_e32 v160, 16, v99
	v_and_b32_e32 v161, 0xffff0000, v99
	v_lshlrev_b32_e32 v162, 16, v100
	v_and_b32_e32 v163, 0xffff0000, v100
	v_lshlrev_b32_e32 v164, 16, v101
	v_and_b32_e32 v165, 0xffff0000, v101
	v_mul_f32_e32 v0, 0xbfb8aa3b, v0
	v_mul_f32_e32 v151, 0xbfb8aa3b, v151
	v_mul_f32_e32 v160, 0xbfb8aa3b, v160
	v_mul_f32_e32 v161, 0xbfb8aa3b, v161
	v_mul_f32_e32 v162, 0xbfb8aa3b, v162
	v_mul_f32_e32 v163, 0xbfb8aa3b, v163
	v_mul_f32_e32 v164, 0xbfb8aa3b, v164
	v_mul_f32_e32 v165, 0xbfb8aa3b, v165
	v_exp_f32_e32 v0, v0
	v_exp_f32_e32 v151, v151
	v_exp_f32_e32 v160, v160
	v_exp_f32_e32 v161, v161
	v_exp_f32_e32 v162, v162
	v_exp_f32_e32 v163, v163
	v_exp_f32_e32 v164, v164
	v_exp_f32_e32 v165, v165
	v_add_f32_e32 v0, 1.0, v0
	v_add_f32_e32 v151, 1.0, v151
	v_add_f32_e32 v160, 1.0, v160
	v_add_f32_e32 v161, 1.0, v161
	v_add_f32_e32 v162, 1.0, v162
	v_add_f32_e32 v163, 1.0, v163
	v_add_f32_e32 v164, 1.0, v164
	v_add_f32_e32 v165, 1.0, v165
	v_rcp_f32_e32 v0, v0
	v_rcp_f32_e32 v151, v151
	v_rcp_f32_e32 v160, v160
	v_rcp_f32_e32 v161, v161
	v_rcp_f32_e32 v162, v162
	v_rcp_f32_e32 v163, v163
	v_rcp_f32_e32 v164, v164
	v_rcp_f32_e32 v165, v165
	v_lshlrev_b32_e32 v166, 16, v102
	v_and_b32_e32 v102, 0xffff0000, v102
	v_lshlrev_b32_e32 v167, 16, v103
	v_and_b32_e32 v103, 0xffff0000, v103
	v_lshlrev_b32_e32 v170, 16, v104
	v_and_b32_e32 v104, 0xffff0000, v104
	v_lshlrev_b32_e32 v171, 16, v105
	v_and_b32_e32 v105, 0xffff0000, v105
	v_fmac_f32_e32 v166, v38, v0
	v_fmac_f32_e32 v102, v39, v151
	v_fmac_f32_e32 v167, v40, v160
	v_fmac_f32_e32 v103, v41, v161
	v_fmac_f32_e32 v170, v34, v162
	v_fmac_f32_e32 v104, v35, v163
	v_fmac_f32_e32 v171, v36, v164
	v_fmac_f32_e32 v105, v37, v165
	v_cvt_pk_bf16_f32 v102, v166, v102
	v_cvt_pk_bf16_f32 v103, v167, v103
	v_cvt_pk_bf16_f32 v104, v170, v104
	v_cvt_pk_bf16_f32 v105, v171, v105
	global_store_dwordx4 v[176:177], v[102:105], off offset:256
	s_waitcnt vmcnt(13)
	v_lshlrev_b32_e32 v0, 16, v90
	v_and_b32_e32 v151, 0xffff0000, v90
	v_lshlrev_b32_e32 v160, 16, v91
	v_and_b32_e32 v161, 0xffff0000, v91
	v_lshlrev_b32_e32 v162, 16, v92
	v_and_b32_e32 v163, 0xffff0000, v92
	v_lshlrev_b32_e32 v164, 16, v93
	v_and_b32_e32 v165, 0xffff0000, v93
	v_mul_f32_e32 v0, 0xbfb8aa3b, v0
	v_mul_f32_e32 v151, 0xbfb8aa3b, v151
	v_mul_f32_e32 v160, 0xbfb8aa3b, v160
	v_mul_f32_e32 v161, 0xbfb8aa3b, v161
	v_mul_f32_e32 v162, 0xbfb8aa3b, v162
	v_mul_f32_e32 v163, 0xbfb8aa3b, v163
	v_mul_f32_e32 v164, 0xbfb8aa3b, v164
	v_mul_f32_e32 v165, 0xbfb8aa3b, v165
	v_exp_f32_e32 v0, v0
	v_exp_f32_e32 v151, v151
	v_exp_f32_e32 v160, v160
	v_exp_f32_e32 v161, v161
	v_exp_f32_e32 v162, v162
	v_exp_f32_e32 v163, v163
	v_exp_f32_e32 v164, v164
	v_exp_f32_e32 v165, v165
	v_add_f32_e32 v0, 1.0, v0
	v_add_f32_e32 v151, 1.0, v151
	v_add_f32_e32 v160, 1.0, v160
	v_add_f32_e32 v161, 1.0, v161
	v_add_f32_e32 v162, 1.0, v162
	v_add_f32_e32 v163, 1.0, v163
	v_add_f32_e32 v164, 1.0, v164
	v_add_f32_e32 v165, 1.0, v165
	v_rcp_f32_e32 v0, v0
	v_rcp_f32_e32 v151, v151
	v_rcp_f32_e32 v160, v160
	v_rcp_f32_e32 v161, v161
	v_rcp_f32_e32 v162, v162
	v_rcp_f32_e32 v163, v163
	v_rcp_f32_e32 v164, v164
	v_rcp_f32_e32 v165, v165
	v_lshlrev_b32_e32 v166, 16, v94
	v_and_b32_e32 v94, 0xffff0000, v94
	v_lshlrev_b32_e32 v167, 16, v95
	v_and_b32_e32 v95, 0xffff0000, v95
	v_lshlrev_b32_e32 v170, 16, v96
	v_and_b32_e32 v96, 0xffff0000, v96
	v_lshlrev_b32_e32 v171, 16, v97
	v_and_b32_e32 v97, 0xffff0000, v97
	v_fmac_f32_e32 v166, v30, v0
	v_fmac_f32_e32 v94, v31, v151
	v_fmac_f32_e32 v167, v32, v160
	v_fmac_f32_e32 v95, v33, v161
	v_fmac_f32_e32 v170, v26, v162
	v_fmac_f32_e32 v96, v27, v163
	v_fmac_f32_e32 v171, v28, v164
	v_fmac_f32_e32 v97, v29, v165
	v_cvt_pk_bf16_f32 v94, v166, v94
	v_cvt_pk_bf16_f32 v95, v167, v95
	v_cvt_pk_bf16_f32 v96, v170, v96
	v_cvt_pk_bf16_f32 v97, v171, v97
	v_or_b32_e32 v176, 160, v150
	v_mov_b32_e32 v177, 0
	v_lshlrev_b64 v[176:177], 12, v[176:177]
	v_lshl_add_u64 v[176:177], s[10:11], 0, v[176:177]
	v_lshl_add_u64 v[176:177], v[176:177], 0, v[146:147]
	global_store_dwordx4 v[176:177], v[94:97], off
	s_waitcnt vmcnt(11)
	v_lshlrev_b32_e32 v0, 16, v82
	v_and_b32_e32 v151, 0xffff0000, v82
	v_lshlrev_b32_e32 v160, 16, v83
	v_and_b32_e32 v161, 0xffff0000, v83
	v_lshlrev_b32_e32 v162, 16, v84
	v_and_b32_e32 v163, 0xffff0000, v84
	v_lshlrev_b32_e32 v164, 16, v85
	v_and_b32_e32 v165, 0xffff0000, v85
	v_mul_f32_e32 v0, 0xbfb8aa3b, v0
	v_mul_f32_e32 v151, 0xbfb8aa3b, v151
	v_mul_f32_e32 v160, 0xbfb8aa3b, v160
	v_mul_f32_e32 v161, 0xbfb8aa3b, v161
	v_mul_f32_e32 v162, 0xbfb8aa3b, v162
	v_mul_f32_e32 v163, 0xbfb8aa3b, v163
	v_mul_f32_e32 v164, 0xbfb8aa3b, v164
	v_mul_f32_e32 v165, 0xbfb8aa3b, v165
	v_exp_f32_e32 v0, v0
	v_exp_f32_e32 v151, v151
	v_exp_f32_e32 v160, v160
	v_exp_f32_e32 v161, v161
	v_exp_f32_e32 v162, v162
	v_exp_f32_e32 v163, v163
	v_exp_f32_e32 v164, v164
	v_exp_f32_e32 v165, v165
	v_add_f32_e32 v0, 1.0, v0
	v_add_f32_e32 v151, 1.0, v151
	v_add_f32_e32 v160, 1.0, v160
	v_add_f32_e32 v161, 1.0, v161
	v_add_f32_e32 v162, 1.0, v162
	v_add_f32_e32 v163, 1.0, v163
	v_add_f32_e32 v164, 1.0, v164
	v_add_f32_e32 v165, 1.0, v165
	v_rcp_f32_e32 v0, v0
	v_rcp_f32_e32 v151, v151
	v_rcp_f32_e32 v160, v160
	v_rcp_f32_e32 v161, v161
	v_rcp_f32_e32 v162, v162
	v_rcp_f32_e32 v163, v163
	v_rcp_f32_e32 v164, v164
	v_rcp_f32_e32 v165, v165
	v_lshlrev_b32_e32 v166, 16, v86
	v_and_b32_e32 v86, 0xffff0000, v86
	v_lshlrev_b32_e32 v167, 16, v87
	v_and_b32_e32 v87, 0xffff0000, v87
	v_lshlrev_b32_e32 v170, 16, v88
	v_and_b32_e32 v88, 0xffff0000, v88
	v_lshlrev_b32_e32 v171, 16, v89
	v_and_b32_e32 v89, 0xffff0000, v89
	v_fmac_f32_e32 v166, v22, v0
	v_fmac_f32_e32 v86, v23, v151
	v_fmac_f32_e32 v167, v24, v160
	v_fmac_f32_e32 v87, v25, v161
	v_fmac_f32_e32 v170, v18, v162
	v_fmac_f32_e32 v88, v19, v163
	v_fmac_f32_e32 v171, v20, v164
	v_fmac_f32_e32 v89, v21, v165
	v_cvt_pk_bf16_f32 v86, v166, v86
	v_cvt_pk_bf16_f32 v87, v167, v87
	v_cvt_pk_bf16_f32 v88, v170, v88
	v_cvt_pk_bf16_f32 v89, v171, v89
	global_store_dwordx4 v[176:177], v[86:89], off offset:256
	s_waitcnt vmcnt(9)
	v_lshlrev_b32_e32 v0, 16, v74
	v_and_b32_e32 v151, 0xffff0000, v74
	v_lshlrev_b32_e32 v160, 16, v75
	v_and_b32_e32 v161, 0xffff0000, v75
	v_lshlrev_b32_e32 v162, 16, v76
	v_and_b32_e32 v163, 0xffff0000, v76
	v_lshlrev_b32_e32 v164, 16, v77
	v_and_b32_e32 v165, 0xffff0000, v77
	v_mul_f32_e32 v0, 0xbfb8aa3b, v0
	v_mul_f32_e32 v151, 0xbfb8aa3b, v151
	v_mul_f32_e32 v160, 0xbfb8aa3b, v160
	v_mul_f32_e32 v161, 0xbfb8aa3b, v161
	v_mul_f32_e32 v162, 0xbfb8aa3b, v162
	v_mul_f32_e32 v163, 0xbfb8aa3b, v163
	v_mul_f32_e32 v164, 0xbfb8aa3b, v164
	v_mul_f32_e32 v165, 0xbfb8aa3b, v165
	v_exp_f32_e32 v0, v0
	v_exp_f32_e32 v151, v151
	v_exp_f32_e32 v160, v160
	v_exp_f32_e32 v161, v161
	v_exp_f32_e32 v162, v162
	v_exp_f32_e32 v163, v163
	v_exp_f32_e32 v164, v164
	v_exp_f32_e32 v165, v165
	v_add_f32_e32 v0, 1.0, v0
	v_add_f32_e32 v151, 1.0, v151
	v_add_f32_e32 v160, 1.0, v160
	v_add_f32_e32 v161, 1.0, v161
	v_add_f32_e32 v162, 1.0, v162
	v_add_f32_e32 v163, 1.0, v163
	v_add_f32_e32 v164, 1.0, v164
	v_add_f32_e32 v165, 1.0, v165
	v_rcp_f32_e32 v0, v0
	v_rcp_f32_e32 v151, v151
	v_rcp_f32_e32 v160, v160
	v_rcp_f32_e32 v161, v161
	v_rcp_f32_e32 v162, v162
	v_rcp_f32_e32 v163, v163
	v_rcp_f32_e32 v164, v164
	v_rcp_f32_e32 v165, v165
	v_lshlrev_b32_e32 v166, 16, v78
	v_and_b32_e32 v78, 0xffff0000, v78
	v_lshlrev_b32_e32 v167, 16, v79
	v_and_b32_e32 v79, 0xffff0000, v79
	v_lshlrev_b32_e32 v170, 16, v80
	v_and_b32_e32 v80, 0xffff0000, v80
	v_lshlrev_b32_e32 v171, 16, v81
	v_and_b32_e32 v81, 0xffff0000, v81
	v_fmac_f32_e32 v166, v14, v0
	v_fmac_f32_e32 v78, v15, v151
	v_fmac_f32_e32 v167, v16, v160
	v_fmac_f32_e32 v79, v17, v161
	v_fmac_f32_e32 v170, v10, v162
	v_fmac_f32_e32 v80, v11, v163
	v_fmac_f32_e32 v171, v12, v164
	v_fmac_f32_e32 v81, v13, v165
	v_cvt_pk_bf16_f32 v78, v166, v78
	v_cvt_pk_bf16_f32 v79, v167, v79
	v_cvt_pk_bf16_f32 v80, v170, v80
	v_cvt_pk_bf16_f32 v81, v171, v81
	v_or_b32_e32 v176, 176, v150
	v_mov_b32_e32 v177, 0
	v_lshlrev_b64 v[176:177], 12, v[176:177]
	v_lshl_add_u64 v[176:177], s[10:11], 0, v[176:177]
	v_lshl_add_u64 v[176:177], v[176:177], 0, v[146:147]
	global_store_dwordx4 v[176:177], v[78:81], off
	s_waitcnt vmcnt(7)
	v_lshlrev_b32_e32 v0, 16, v66
	v_and_b32_e32 v151, 0xffff0000, v66
	v_lshlrev_b32_e32 v160, 16, v67
	v_and_b32_e32 v161, 0xffff0000, v67
	v_lshlrev_b32_e32 v162, 16, v68
	v_and_b32_e32 v163, 0xffff0000, v68
	v_lshlrev_b32_e32 v164, 16, v69
	v_and_b32_e32 v165, 0xffff0000, v69
	v_mul_f32_e32 v0, 0xbfb8aa3b, v0
	v_mul_f32_e32 v151, 0xbfb8aa3b, v151
	v_mul_f32_e32 v160, 0xbfb8aa3b, v160
	v_mul_f32_e32 v161, 0xbfb8aa3b, v161
	v_mul_f32_e32 v162, 0xbfb8aa3b, v162
	v_mul_f32_e32 v163, 0xbfb8aa3b, v163
	v_mul_f32_e32 v164, 0xbfb8aa3b, v164
	v_mul_f32_e32 v165, 0xbfb8aa3b, v165
	v_exp_f32_e32 v0, v0
	v_exp_f32_e32 v151, v151
	v_exp_f32_e32 v160, v160
	v_exp_f32_e32 v161, v161
	v_exp_f32_e32 v162, v162
	v_exp_f32_e32 v163, v163
	v_exp_f32_e32 v164, v164
	v_exp_f32_e32 v165, v165
	v_add_f32_e32 v0, 1.0, v0
	v_add_f32_e32 v151, 1.0, v151
	v_add_f32_e32 v160, 1.0, v160
	v_add_f32_e32 v161, 1.0, v161
	v_add_f32_e32 v162, 1.0, v162
	v_add_f32_e32 v163, 1.0, v163
	v_add_f32_e32 v164, 1.0, v164
	v_add_f32_e32 v165, 1.0, v165
	v_rcp_f32_e32 v0, v0
	v_rcp_f32_e32 v151, v151
	v_rcp_f32_e32 v160, v160
	v_rcp_f32_e32 v161, v161
	v_rcp_f32_e32 v162, v162
	v_rcp_f32_e32 v163, v163
	v_rcp_f32_e32 v164, v164
	v_rcp_f32_e32 v165, v165
	v_lshlrev_b32_e32 v166, 16, v70
	v_and_b32_e32 v70, 0xffff0000, v70
	v_lshlrev_b32_e32 v167, 16, v71
	v_and_b32_e32 v71, 0xffff0000, v71
	v_lshlrev_b32_e32 v170, 16, v72
	v_and_b32_e32 v72, 0xffff0000, v72
	v_lshlrev_b32_e32 v171, 16, v73
	v_and_b32_e32 v73, 0xffff0000, v73
	v_fmac_f32_e32 v166, v6, v0
	v_fmac_f32_e32 v70, v7, v151
	v_fmac_f32_e32 v167, v8, v160
	v_fmac_f32_e32 v71, v9, v161
	v_fmac_f32_e32 v170, v2, v162
	v_fmac_f32_e32 v72, v3, v163
	v_fmac_f32_e32 v171, v4, v164
	v_fmac_f32_e32 v73, v5, v165
	v_cvt_pk_bf16_f32 v70, v166, v70
	v_cvt_pk_bf16_f32 v71, v167, v71
	v_cvt_pk_bf16_f32 v72, v170, v72
	v_cvt_pk_bf16_f32 v73, v171, v73
	global_store_dwordx4 v[176:177], v[70:73], off offset:256
	s_andn2_b64 vcc, exec, s[4:5]
	s_mov_b64 s[4:5], -1
	s_cbranch_vccnz .LBB0_1145
	s_andn2_b64 vcc, exec, s[8:9]
	s_cbranch_vccnz .LBB0_1144
	s_barrier
	s_branch .LBB0_1144

.LBB0_1231:
	v_lshl_add_u32 v150, s34, 8, v1
	v_lshl_or_b32 v148, s56, 8, v153
	v_ashrrev_i32_e32 v149, 31, v148
	v_mov_b32_e32 v146, v150
	v_mov_b32_e32 v147, 0
	v_lshlrev_b64 v[146:147], 11, v[146:147]
	v_lshl_add_u64 v[146:147], v[146:147], 0, v[148:149]
	v_lshl_add_u64 v[158:159], v[146:147], 2, s[6:7]
	global_load_dwordx4 v[170:173], v[158:159], off
	global_load_dwordx4 v[174:177], v[158:159], off offset:16
	global_load_dwordx4 v[178:181], v[158:159], off offset:512
	global_load_dwordx4 v[182:185], v[158:159], off offset:528
	v_or_b32_e32 v146, 16, v150
	v_mov_b32_e32 v147, 0
	v_lshlrev_b64 v[146:147], 11, v[146:147]
	v_lshl_add_u64 v[146:147], v[146:147], 0, v[148:149]
	v_lshl_add_u64 v[158:159], v[146:147], 2, s[6:7]
	global_load_dwordx4 v[186:189], v[158:159], off
	global_load_dwordx4 v[190:193], v[158:159], off offset:16
	global_load_dwordx4 v[194:197], v[158:159], off offset:512
	global_load_dwordx4 v[198:201], v[158:159], off offset:528
	v_or_b32_e32 v146, 32, v150
	v_mov_b32_e32 v147, 0
	v_lshlrev_b64 v[146:147], 11, v[146:147]
	v_lshl_add_u64 v[146:147], v[146:147], 0, v[148:149]
	v_lshl_add_u64 v[158:159], v[146:147], 2, s[6:7]
	global_load_dwordx4 v[202:205], v[158:159], off
	global_load_dwordx4 v[206:209], v[158:159], off offset:16
	global_load_dwordx4 v[210:213], v[158:159], off offset:512
	global_load_dwordx4 v[214:217], v[158:159], off offset:528
	v_or_b32_e32 v146, 48, v150
	v_mov_b32_e32 v147, 0
	v_lshlrev_b64 v[146:147], 11, v[146:147]
	v_lshl_add_u64 v[146:147], v[146:147], 0, v[148:149]
	v_lshl_add_u64 v[158:159], v[146:147], 2, s[6:7]
	global_load_dwordx4 v[222:225], v[158:159], off
	global_load_dwordx4 v[226:229], v[158:159], off offset:16
	global_load_dwordx4 v[230:233], v[158:159], off offset:512
	global_load_dwordx4 v[234:237], v[158:159], off offset:528
	s_waitcnt vmcnt(14)
	v_pk_add_f32 v[126:127], v[126:127], v[170:171]
	v_pk_add_f32 v[128:129], v[128:129], v[172:173]
	v_pk_add_f32 v[122:123], v[122:123], v[174:175]
	v_pk_add_f32 v[124:125], v[124:125], v[176:177]
	v_cvt_pk_bf16_f32 v170, v126, v127
	v_cvt_pk_bf16_f32 v171, v128, v129
	v_cvt_pk_bf16_f32 v172, v122, v123
	v_cvt_pk_bf16_f32 v173, v124, v125
	v_mov_b32_e32 v160, v150
	v_mov_b32_e32 v161, 0
	v_lshlrev_b64 v[160:161], 11, v[160:161]
	v_lshl_add_u64 v[160:161], v[160:161], 0, v[148:149]
	v_lshl_add_u64 v[160:161], v[160:161], 1, s[10:11]
	global_store_dwordx4 v[160:161], v[170:173], off
	v_or_b32_e32 v146, 128, v150
	v_mov_b32_e32 v147, 0
	v_lshlrev_b64 v[146:147], 11, v[146:147]
	v_lshl_add_u64 v[146:147], v[146:147], 0, v[148:149]
	v_lshl_add_u64 v[158:159], v[146:147], 2, s[6:7]
	global_load_dwordx4 v[126:129], v[158:159], off
	global_load_dwordx4 v[122:125], v[158:159], off offset:16
	s_waitcnt vmcnt(15)
	v_pk_add_f32 v[118:119], v[118:119], v[178:179]
	v_pk_add_f32 v[120:121], v[120:121], v[180:181]
	v_pk_add_f32 v[114:115], v[114:115], v[182:183]
	v_pk_add_f32 v[116:117], v[116:117], v[184:185]
	v_cvt_pk_bf16_f32 v178, v118, v119
	v_cvt_pk_bf16_f32 v179, v120, v121
	v_cvt_pk_bf16_f32 v180, v114, v115
	v_cvt_pk_bf16_f32 v181, v116, v117
	global_store_dwordx4 v[160:161], v[178:181], off offset:256
	global_load_dwordx4 v[118:121], v[158:159], off offset:512
	global_load_dwordx4 v[114:117], v[158:159], off offset:528
	s_waitcnt vmcnt(16)
	v_pk_add_f32 v[110:111], v[110:111], v[186:187]
	v_pk_add_f32 v[112:113], v[112:113], v[188:189]
	v_pk_add_f32 v[106:107], v[106:107], v[190:191]
	v_pk_add_f32 v[108:109], v[108:109], v[192:193]
	v_cvt_pk_bf16_f32 v186, v110, v111
	v_cvt_pk_bf16_f32 v187, v112, v113
	v_cvt_pk_bf16_f32 v188, v106, v107
	v_cvt_pk_bf16_f32 v189, v108, v109
	v_or_b32_e32 v160, 16, v150
	v_mov_b32_e32 v161, 0
	v_lshlrev_b64 v[160:161], 11, v[160:161]
	v_lshl_add_u64 v[160:161], v[160:161], 0, v[148:149]
	v_lshl_add_u64 v[160:161], v[160:161], 1, s[10:11]
	global_store_dwordx4 v[160:161], v[186:189], off
	v_or_b32_e32 v146, 144, v150
	v_mov_b32_e32 v147, 0
	v_lshlrev_b64 v[146:147], 11, v[146:147]
	v_lshl_add_u64 v[146:147], v[146:147], 0, v[148:149]
	v_lshl_add_u64 v[158:159], v[146:147], 2, s[6:7]
	global_load_dwordx4 v[110:113], v[158:159], off
	global_load_dwordx4 v[106:109], v[158:159], off offset:16
	s_waitcnt vmcnt(17)
	v_pk_add_f32 v[102:103], v[102:103], v[194:195]
	v_pk_add_f32 v[104:105], v[104:105], v[196:197]
	v_pk_add_f32 v[98:99], v[98:99], v[198:199]
	v_pk_add_f32 v[100:101], v[100:101], v[200:201]
	v_cvt_pk_bf16_f32 v194, v102, v103
	v_cvt_pk_bf16_f32 v195, v104, v105
	v_cvt_pk_bf16_f32 v196, v98, v99
	v_cvt_pk_bf16_f32 v197, v100, v101
	global_store_dwordx4 v[160:161], v[194:197], off offset:256
	global_load_dwordx4 v[102:105], v[158:159], off offset:512
	global_load_dwordx4 v[98:101], v[158:159], off offset:528
	s_waitcnt vmcnt(18)
	v_pk_add_f32 v[94:95], v[94:95], v[202:203]
	v_pk_add_f32 v[96:97], v[96:97], v[204:205]
	v_pk_add_f32 v[90:91], v[90:91], v[206:207]
	v_pk_add_f32 v[92:93], v[92:93], v[208:209]
	v_cvt_pk_bf16_f32 v202, v94, v95
	v_cvt_pk_bf16_f32 v203, v96, v97
	v_cvt_pk_bf16_f32 v204, v90, v91
	v_cvt_pk_bf16_f32 v205, v92, v93
	v_or_b32_e32 v160, 32, v150
	v_mov_b32_e32 v161, 0
	v_lshlrev_b64 v[160:161], 11, v[160:161]
	v_lshl_add_u64 v[160:161], v[160:161], 0, v[148:149]
	v_lshl_add_u64 v[160:161], v[160:161], 1, s[10:11]
	global_store_dwordx4 v[160:161], v[202:205], off
	v_or_b32_e32 v146, 160, v150
	v_mov_b32_e32 v147, 0
	v_lshlrev_b64 v[146:147], 11, v[146:147]
	v_lshl_add_u64 v[146:147], v[146:147], 0, v[148:149]
	v_lshl_add_u64 v[158:159], v[146:147], 2, s[6:7]
	global_load_dwordx4 v[94:97], v[158:159], off
	global_load_dwordx4 v[90:93], v[158:159], off offset:16
	s_waitcnt vmcnt(19)
	v_pk_add_f32 v[86:87], v[86:87], v[210:211]
	v_pk_add_f32 v[88:89], v[88:89], v[212:213]
	v_pk_add_f32 v[82:83], v[82:83], v[214:215]
	v_pk_add_f32 v[84:85], v[84:85], v[216:217]
	v_cvt_pk_bf16_f32 v210, v86, v87
	v_cvt_pk_bf16_f32 v211, v88, v89
	v_cvt_pk_bf16_f32 v212, v82, v83
	v_cvt_pk_bf16_f32 v213, v84, v85
	global_store_dwordx4 v[160:161], v[210:213], off offset:256
	global_load_dwordx4 v[86:89], v[158:159], off offset:512
	global_load_dwordx4 v[82:85], v[158:159], off offset:528
	s_waitcnt vmcnt(20)
	v_pk_add_f32 v[78:79], v[78:79], v[222:223]
	v_pk_add_f32 v[80:81], v[80:81], v[224:225]
	v_pk_add_f32 v[74:75], v[74:75], v[226:227]
	v_pk_add_f32 v[76:77], v[76:77], v[228:229]
	v_cvt_pk_bf16_f32 v222, v78, v79
	v_cvt_pk_bf16_f32 v223, v80, v81
	v_cvt_pk_bf16_f32 v224, v74, v75
	v_cvt_pk_bf16_f32 v225, v76, v77
	v_or_b32_e32 v160, 48, v150
	v_mov_b32_e32 v161, 0
	v_lshlrev_b64 v[160:161], 11, v[160:161]
	v_lshl_add_u64 v[160:161], v[160:161], 0, v[148:149]
	v_lshl_add_u64 v[160:161], v[160:161], 1, s[10:11]
	global_store_dwordx4 v[160:161], v[222:225], off
	v_or_b32_e32 v146, 176, v150
	v_mov_b32_e32 v147, 0
	v_lshlrev_b64 v[146:147], 11, v[146:147]
	v_lshl_add_u64 v[146:147], v[146:147], 0, v[148:149]
	v_lshl_add_u64 v[158:159], v[146:147], 2, s[6:7]
	global_load_dwordx4 v[78:81], v[158:159], off
	global_load_dwordx4 v[74:77], v[158:159], off offset:16
	s_waitcnt vmcnt(21)
	v_pk_add_f32 v[70:71], v[70:71], v[230:231]
	v_pk_add_f32 v[72:73], v[72:73], v[232:233]
	v_pk_add_f32 v[66:67], v[66:67], v[234:235]
	v_pk_add_f32 v[68:69], v[68:69], v[236:237]
	v_cvt_pk_bf16_f32 v230, v70, v71
	v_cvt_pk_bf16_f32 v231, v72, v73
	v_cvt_pk_bf16_f32 v232, v66, v67
	v_cvt_pk_bf16_f32 v233, v68, v69
	global_store_dwordx4 v[160:161], v[230:233], off offset:256
	global_load_dwordx4 v[70:73], v[158:159], off offset:512
	global_load_dwordx4 v[66:69], v[158:159], off offset:528
	s_waitcnt vmcnt(21)
	v_pk_add_f32 v[62:63], v[62:63], v[126:127]
	v_pk_add_f32 v[64:65], v[64:65], v[128:129]
	v_pk_add_f32 v[58:59], v[58:59], v[122:123]
	v_pk_add_f32 v[60:61], v[60:61], v[124:125]
	v_cvt_pk_bf16_f32 v126, v62, v63
	v_cvt_pk_bf16_f32 v127, v64, v65
	v_cvt_pk_bf16_f32 v128, v58, v59
	v_cvt_pk_bf16_f32 v129, v60, v61
	v_or_b32_e32 v160, 128, v150
	v_mov_b32_e32 v161, 0
	v_lshlrev_b64 v[160:161], 11, v[160:161]
	v_lshl_add_u64 v[160:161], v[160:161], 0, v[148:149]
	v_lshl_add_u64 v[160:161], v[160:161], 1, s[10:11]
	global_store_dwordx4 v[160:161], v[126:129], off
	s_waitcnt vmcnt(19)
	v_pk_add_f32 v[54:55], v[54:55], v[118:119]
	v_pk_add_f32 v[56:57], v[56:57], v[120:121]
	v_pk_add_f32 v[50:51], v[50:51], v[114:115]
	v_pk_add_f32 v[52:53], v[52:53], v[116:117]
	v_cvt_pk_bf16_f32 v118, v54, v55
	v_cvt_pk_bf16_f32 v119, v56, v57
	v_cvt_pk_bf16_f32 v120, v50, v51
	v_cvt_pk_bf16_f32 v121, v52, v53
	global_store_dwordx4 v[160:161], v[118:121], off offset:256
	s_waitcnt vmcnt(17)
	v_pk_add_f32 v[46:47], v[46:47], v[110:111]
	v_pk_add_f32 v[48:49], v[48:49], v[112:113]
	v_pk_add_f32 v[42:43], v[42:43], v[106:107]
	v_pk_add_f32 v[44:45], v[44:45], v[108:109]
	v_cvt_pk_bf16_f32 v110, v46, v47
	v_cvt_pk_bf16_f32 v111, v48, v49
	v_cvt_pk_bf16_f32 v112, v42, v43
	v_cvt_pk_bf16_f32 v113, v44, v45
	v_or_b32_e32 v160, 144, v150
	v_mov_b32_e32 v161, 0
	v_lshlrev_b64 v[160:161], 11, v[160:161]
	v_lshl_add_u64 v[160:161], v[160:161], 0, v[148:149]
	v_lshl_add_u64 v[160:161], v[160:161], 1, s[10:11]
	global_store_dwordx4 v[160:161], v[110:113], off
	s_waitcnt vmcnt(15)
	v_pk_add_f32 v[38:39], v[38:39], v[102:103]
	v_pk_add_f32 v[40:41], v[40:41], v[104:105]
	v_pk_add_f32 v[34:35], v[34:35], v[98:99]
	v_pk_add_f32 v[36:37], v[36:37], v[100:101]
	v_cvt_pk_bf16_f32 v102, v38, v39
	v_cvt_pk_bf16_f32 v103, v40, v41
	v_cvt_pk_bf16_f32 v104, v34, v35
	v_cvt_pk_bf16_f32 v105, v36, v37
	global_store_dwordx4 v[160:161], v[102:105], off offset:256
	s_waitcnt vmcnt(13)
	v_pk_add_f32 v[30:31], v[30:31], v[94:95]
	v_pk_add_f32 v[32:33], v[32:33], v[96:97]
	v_pk_add_f32 v[26:27], v[26:27], v[90:91]
	v_pk_add_f32 v[28:29], v[28:29], v[92:93]
	v_cvt_pk_bf16_f32 v94, v30, v31
	v_cvt_pk_bf16_f32 v95, v32, v33
	v_cvt_pk_bf16_f32 v96, v26, v27
	v_cvt_pk_bf16_f32 v97, v28, v29
	v_or_b32_e32 v160, 160, v150
	v_mov_b32_e32 v161, 0
	v_lshlrev_b64 v[160:161], 11, v[160:161]
	v_lshl_add_u64 v[160:161], v[160:161], 0, v[148:149]
	v_lshl_add_u64 v[160:161], v[160:161], 1, s[10:11]
	global_store_dwordx4 v[160:161], v[94:97], off
	s_waitcnt vmcnt(11)
	v_pk_add_f32 v[22:23], v[22:23], v[86:87]
	v_pk_add_f32 v[24:25], v[24:25], v[88:89]
	v_pk_add_f32 v[18:19], v[18:19], v[82:83]
	v_pk_add_f32 v[20:21], v[20:21], v[84:85]
	v_cvt_pk_bf16_f32 v86, v22, v23
	v_cvt_pk_bf16_f32 v87, v24, v25
	v_cvt_pk_bf16_f32 v88, v18, v19
	v_cvt_pk_bf16_f32 v89, v20, v21
	global_store_dwordx4 v[160:161], v[86:89], off offset:256
	s_waitcnt vmcnt(9)
	v_pk_add_f32 v[14:15], v[14:15], v[78:79]
	v_pk_add_f32 v[16:17], v[16:17], v[80:81]
	v_pk_add_f32 v[10:11], v[10:11], v[74:75]
	v_pk_add_f32 v[12:13], v[12:13], v[76:77]
	v_cvt_pk_bf16_f32 v78, v14, v15
	v_cvt_pk_bf16_f32 v79, v16, v17
	v_cvt_pk_bf16_f32 v80, v10, v11
	v_cvt_pk_bf16_f32 v81, v12, v13
	v_or_b32_e32 v160, 176, v150
	v_mov_b32_e32 v161, 0
	v_lshlrev_b64 v[160:161], 11, v[160:161]
	v_lshl_add_u64 v[160:161], v[160:161], 0, v[148:149]
	v_lshl_add_u64 v[160:161], v[160:161], 1, s[10:11]
	global_store_dwordx4 v[160:161], v[78:81], off
	s_waitcnt vmcnt(7)
	v_pk_add_f32 v[6:7], v[6:7], v[70:71]
	v_pk_add_f32 v[8:9], v[8:9], v[72:73]
	v_pk_add_f32 v[2:3], v[2:3], v[66:67]
	v_pk_add_f32 v[4:5], v[4:5], v[68:69]
	v_cvt_pk_bf16_f32 v70, v6, v7
	v_cvt_pk_bf16_f32 v71, v8, v9
	v_cvt_pk_bf16_f32 v72, v2, v3
	v_cvt_pk_bf16_f32 v73, v4, v5
	global_store_dwordx4 v[160:161], v[70:73], off offset:256
	s_andn2_b64 vcc, exec, s[4:5]
	s_mov_b64 s[4:5], -1
	s_cbranch_vccnz .LBB0_1220
	s_andn2_b64 vcc, exec, s[8:9]
	s_cbranch_vccnz .LBB0_1219
	s_barrier
	s_branch .LBB0_1219

.LBB0_1476:
	s_ashr_i32 s0, s22, 3
	s_add_i32 s20, s24, s0
	v_and_b32_e32 v0, 63, v254
	v_lshlrev_b32_e32 v0, 2, v0
	v_add_u32_e32 v0, 0x23a00, v0
	ds_read_b32 v0, v0
	s_waitcnt lgkmcnt(0)
	v_cmp_ge_i32_e32 vcc, s20, v0
	s_nop 1
	s_and_b32 s0, vcc_lo, 0xfffffffe
	s_bcnt1_i32_b32 s21, s0
	s_lshl_b32 s0, s21, 2
	s_add_i32 s0, s0, 0
	s_add_i32 s0, s0, 0x23a00
	v_mov_b32_e32 v0, s0
	ds_read2st64_b32 v[2:3], v0 offset1:1
	ds_read_b32 v0, v0 offset:512
	s_waitcnt lgkmcnt(0)
	v_readfirstlane_b32 s0, v3
	s_abs_i32 s1, s0
	v_cvt_f32_u32_e32 v3, s1
	v_readfirstlane_b32 s2, v2
	v_readfirstlane_b32 s3, v0
	s_sub_i32 s23, 0, s1
	v_rcp_iflag_f32_e32 v2, v3
	s_sub_i32 s2, s20, s2
	s_abs_i32 s22, s2
	s_xor_b32 s20, s2, s0
	v_mul_f32_e32 v0, 0x4f7ffffe, v2
	v_cvt_u32_f32_e32 v0, v0
	s_ashr_i32 s20, s20, 31
	v_readfirstlane_b32 s24, v0
	s_mul_i32 s23, s23, s24
	s_mul_hi_u32 s23, s24, s23
	s_add_i32 s24, s24, s23
	s_mul_hi_u32 s23, s22, s24
	s_mul_i32 s24, s23, s1
	s_sub_i32 s22, s22, s24
	s_add_i32 s25, s23, 1
	s_sub_i32 s24, s22, s1
	s_cmp_ge_u32 s22, s1
	s_cselect_b32 s23, s25, s23
	s_cselect_b32 s22, s24, s22
	s_add_i32 s24, s23, 1
	s_cmp_ge_u32 s22, s1
	s_cselect_b32 s1, s24, s23
	s_xor_b32 s1, s1, s20
	s_sub_i32 s1, s1, s20
	s_mul_i32 s0, s1, s0
	s_lshl_b32 s21, s21, 4
	s_sub_i32 s0, s2, s0
	s_add_i32 s20, s0, s3
	s_add_i32 s22, s1, s21
.LBB0_1481:
	s_lshl_b32 s1, s30, 7
	s_ashr_i32 s0, s30, 4
	s_and_b32 s1, s1, 0x780
	v_or_b32_e32 v240, s1, v184
	s_ashr_i32 s1, s0, 31
	s_lshl_b64 s[0:1], s[0:1], 13
	s_add_u32 s2, s8, s0
	s_addc_u32 s3, s9, s1
	v_lshlrev_b32_e32 v240, 2, v240
	s_add_u32 s0, s10, s0
	s_addc_u32 s1, s11, s1
	global_load_dwordx4 v[224:227], v240, s[2:3]
	global_load_dwordx4 v[228:231], v240, s[2:3] offset:16
	global_load_dwordx4 v[232:235], v240, s[0:1]
	global_load_dwordx4 v[236:239], v240, s[0:1] offset:16
	s_ashr_i32 s21, s20, 31
	s_lshl_b64 s[0:1], s[20:21], 19
	s_add_u32 s24, s47, s0
	s_addc_u32 s25, s48, s1
	s_and_b64 s[0:1], s[4:5], exec
	s_cselect_b32 s21, s25, s37
	s_cselect_b32 s63, s24, s36
	s_ashr_i32 s23, s22, 31
	s_lshl_b64 s[0:1], s[22:23], 19
	s_add_u32 s26, s45, s0
	s_addc_u32 s27, s46, s1
	s_and_b64 s[0:1], s[4:5], exec
	s_cselect_b32 s23, s27, s35
	s_cselect_b32 s64, s26, s34
	s_add_u32 s65, s34, 0x4000
	s_addc_u32 s66, s35, 0
	s_add_u32 s34, s36, 0x40080
	v_mov_b32_e32 v34, 0
	s_addc_u32 s35, s37, 0
	s_mov_b32 s67, -2
	v_mov_b32_e32 v35, v34
	v_mov_b32_e32 v36, v34
	v_mov_b32_e32 v37, v34
	v_mov_b32_e32 v38, v34
	v_mov_b32_e32 v39, v34
	v_mov_b32_e32 v40, v34
	v_mov_b32_e32 v41, v34
	v_mov_b32_e32 v50, v34
	v_mov_b32_e32 v51, v34
	v_mov_b32_e32 v52, v34
	v_mov_b32_e32 v53, v34
	v_mov_b32_e32 v54, v34
	v_mov_b32_e32 v55, v34
	v_mov_b32_e32 v56, v34
	v_mov_b32_e32 v57, v34
	v_mov_b32_e32 v66, v34
	v_mov_b32_e32 v67, v34
	v_mov_b32_e32 v68, v34
	v_mov_b32_e32 v69, v34
	v_mov_b32_e32 v70, v34
	v_mov_b32_e32 v71, v34
	v_mov_b32_e32 v72, v34
	v_mov_b32_e32 v73, v34
	v_mov_b32_e32 v82, v34
	v_mov_b32_e32 v83, v34
	v_mov_b32_e32 v84, v34
	v_mov_b32_e32 v85, v34
	v_mov_b32_e32 v86, v34
	v_mov_b32_e32 v87, v34
	v_mov_b32_e32 v88, v34
	v_mov_b32_e32 v89, v34
	v_mov_b32_e32 v42, v34
	v_mov_b32_e32 v43, v34
	v_mov_b32_e32 v44, v34
	v_mov_b32_e32 v45, v34
	v_mov_b32_e32 v46, v34
	v_mov_b32_e32 v47, v34
	v_mov_b32_e32 v48, v34
	v_mov_b32_e32 v49, v34
	v_mov_b32_e32 v58, v34
	v_mov_b32_e32 v59, v34
	v_mov_b32_e32 v60, v34
	v_mov_b32_e32 v61, v34
	v_mov_b32_e32 v62, v34
	v_mov_b32_e32 v63, v34
	v_mov_b32_e32 v64, v34
	v_mov_b32_e32 v65, v34
	v_mov_b32_e32 v74, v34
	v_mov_b32_e32 v75, v34
	v_mov_b32_e32 v76, v34
	v_mov_b32_e32 v77, v34
	v_mov_b32_e32 v78, v34
	v_mov_b32_e32 v79, v34
	v_mov_b32_e32 v80, v34
	v_mov_b32_e32 v81, v34
	v_mov_b32_e32 v90, v34
	v_mov_b32_e32 v91, v34
	v_mov_b32_e32 v92, v34
	v_mov_b32_e32 v93, v34
	v_mov_b32_e32 v94, v34
	v_mov_b32_e32 v95, v34
	v_mov_b32_e32 v96, v34
	v_mov_b32_e32 v97, v34
	v_mov_b32_e32 v98, v34
	v_mov_b32_e32 v99, v34
	v_mov_b32_e32 v100, v34
	v_mov_b32_e32 v101, v34
	v_mov_b32_e32 v102, v34
	v_mov_b32_e32 v103, v34
	v_mov_b32_e32 v104, v34
	v_mov_b32_e32 v105, v34
	v_mov_b32_e32 v114, v34
	v_mov_b32_e32 v115, v34
	v_mov_b32_e32 v116, v34
	v_mov_b32_e32 v117, v34
	v_mov_b32_e32 v118, v34
	v_mov_b32_e32 v119, v34
	v_mov_b32_e32 v120, v34
	v_mov_b32_e32 v121, v34
	v_mov_b32_e32 v130, v34
	v_mov_b32_e32 v131, v34
	v_mov_b32_e32 v132, v34
	v_mov_b32_e32 v133, v34
	v_mov_b32_e32 v134, v34
	v_mov_b32_e32 v135, v34
	v_mov_b32_e32 v136, v34
	v_mov_b32_e32 v137, v34
	v_mov_b32_e32 v146, v34
	v_mov_b32_e32 v147, v34
	v_mov_b32_e32 v148, v34
	v_mov_b32_e32 v149, v34
	v_mov_b32_e32 v150, v34
	v_mov_b32_e32 v151, v34
	v_mov_b32_e32 v152, v34
	v_mov_b32_e32 v153, v34
	v_mov_b32_e32 v106, v34
	v_mov_b32_e32 v107, v34
	v_mov_b32_e32 v108, v34
	v_mov_b32_e32 v109, v34
	v_mov_b32_e32 v110, v34
	v_mov_b32_e32 v111, v34
	v_mov_b32_e32 v112, v34
	v_mov_b32_e32 v113, v34
	v_mov_b32_e32 v122, v34
	v_mov_b32_e32 v123, v34
	v_mov_b32_e32 v124, v34
	v_mov_b32_e32 v125, v34
	v_mov_b32_e32 v126, v34
	v_mov_b32_e32 v127, v34
	v_mov_b32_e32 v128, v34
	v_mov_b32_e32 v129, v34
	v_mov_b32_e32 v138, v34
	v_mov_b32_e32 v139, v34
	v_mov_b32_e32 v140, v34
	v_mov_b32_e32 v141, v34
	v_mov_b32_e32 v142, v34
	v_mov_b32_e32 v143, v34
	v_mov_b32_e32 v144, v34
	v_mov_b32_e32 v145, v34
	v_mov_b32_e32 v154, v34
	v_mov_b32_e32 v155, v34
	v_mov_b32_e32 v156, v34
	v_mov_b32_e32 v157, v34
	v_mov_b32_e32 v158, v34
	v_mov_b32_e32 v159, v34
	v_mov_b32_e32 v160, v34
	v_mov_b32_e32 v161, v34

.LBB0_1485:
	s_lshl_b32 s1, s30, 7
	s_ashr_i32 s0, s30, 4
	s_and_b32 s1, s1, 0x780
	v_or_b32_e32 v170, s1, v184
	s_nop 15
	s_nop 15
	s_nop 15
	s_nop 15
	s_nop 15
	v_lshl_add_u32 v20, s28, 8, v182
	v_fmamk_f32 v0, v158, 0x3a800000, v224
	v_fmamk_f32 v23, v156, 0x3a800000, v230
	v_fmamk_f32 v18, v154, 0x3a800000, v228
	v_min_f32_e32 v0, 0x40e00000, v0
	v_min_f32_e32 v23, 0x40e00000, v23
	v_min_f32_e32 v18, 0x40e00000, v18
	v_fmamk_f32 v26, v150, 0x3a800000, v232
	v_mul_f32_e32 v28, 0x3fd9db23, v0
	v_mul_f32_e32 v150, 0x3fd9db23, v23
	v_mul_f32_e32 v29, 0x3fd9db23, v18
	v_mul_f32_e32 v28, 0xbfb8aa3b, v28
	v_mul_f32_e32 v150, 0xbfb8aa3b, v150
	v_mul_f32_e32 v29, 0xbfb8aa3b, v29
	v_exp_f32_e32 v28, v28
	v_exp_f32_e32 v150, v150
	v_fmamk_f32 v31, v147, 0x3a800000, v237
	v_exp_f32_e32 v29, v29
	v_fmamk_f32 v21, v155, 0x3a800000, v229
	v_fmamk_f32 v27, v146, 0x3a800000, v236
	v_med3_f32 v26, v26, s59, v189
	v_med3_f32 v31, v31, s59, v189
	v_min_f32_e32 v21, 0x40e00000, v21
	v_med3_f32 v27, v27, s59, v189
	v_add_f32_e32 v26, 1.0, v26
	v_add_f32_e32 v31, 1.0, v31
	v_mul_f32_e32 v33, 0x3fd9db23, v21
	v_add_f32_e32 v27, 1.0, v27
	v_mul_f32_e32 v0, v0, v26
	v_mul_f32_e32 v21, v21, v31
	v_add_f32_e32 v26, 1.0, v28
	v_add_f32_e32 v31, 1.0, v150
	v_fmamk_f32 v147, v148, 0x3a800000, v238
	v_mul_f32_e32 v18, v18, v27
	v_add_f32_e32 v27, 1.0, v29
	v_rcp_f32_e32 v26, v26
	v_rcp_f32_e32 v31, v31
	v_fmamk_f32 v19, v159, 0x3a800000, v225
	v_fmamk_f32 v22, v160, 0x3a800000, v226
	v_fmamk_f32 v24, v161, 0x3a800000, v227
	v_med3_f32 v147, v147, s59, v189
	v_rcp_f32_e32 v27, v27
	v_min_f32_e32 v19, 0x40e00000, v19
	v_min_f32_e32 v22, 0x40e00000, v22
	v_min_f32_e32 v24, 0x40e00000, v24
	v_add_f32_e32 v147, 1.0, v147
	v_fmamk_f32 v25, v157, 0x3a800000, v231
	v_mul_f32_e32 v32, 0x3fd9db23, v19
	v_fmamk_f32 v146, v152, 0x3a800000, v234
	v_mul_f32_e32 v148, 0x3fd9db23, v22
	v_mul_f32_e32 v152, 0x3fd9db23, v24
	v_mul_f32_e32 v23, v23, v147
	v_min_f32_e32 v25, 0x40e00000, v25
	v_mul_f32_e32 v32, 0xbfb8aa3b, v32
	v_mul_f32_e32 v148, 0xbfb8aa3b, v148
	v_mul_f32_e32 v0, v0, v26
	v_mul_f32_e32 v26, v23, v31
	v_mul_f32_e32 v23, 0xbfb8aa3b, v152
	v_mul_f32_e32 v33, 0xbfb8aa3b, v33
	v_exp_f32_e32 v32, v32
	v_exp_f32_e32 v148, v148
	v_mul_f32_e32 v18, v18, v27
	v_exp_f32_e32 v23, v23
	v_mul_f32_e32 v27, 0x3fd9db23, v25
	v_fmamk_f32 v30, v151, 0x3a800000, v233
	v_exp_f32_e32 v33, v33
	v_mul_f32_e32 v27, 0xbfb8aa3b, v27
	v_med3_f32 v30, v30, s59, v189
	v_exp_f32_e32 v27, v27
	v_add_f32_e32 v30, 1.0, v30
	v_mul_f32_e32 v19, v19, v30
	v_add_f32_e32 v28, 1.0, v32
	v_add_f32_e32 v30, 1.0, v148
	v_add_f32_e32 v23, 1.0, v23
	v_fmamk_f32 v151, v153, 0x3a800000, v235
	v_add_f32_e32 v29, 1.0, v33
	v_rcp_f32_e32 v28, v28
	v_rcp_f32_e32 v30, v30
	v_rcp_f32_e32 v23, v23
	v_med3_f32 v146, v146, s59, v189
	v_med3_f32 v151, v151, s59, v189
	v_rcp_f32_e32 v29, v29
	v_add_f32_e32 v27, 1.0, v27
	v_fmamk_f32 v149, v149, 0x3a800000, v239
	v_add_f32_e32 v146, 1.0, v146
	v_add_f32_e32 v151, 1.0, v151
	v_rcp_f32_e32 v27, v27
	v_med3_f32 v149, v149, s59, v189
	v_mul_f32_e32 v22, v22, v146
	v_mul_f32_e32 v24, v24, v151
	v_mul_f32_e32 v19, v19, v28
	v_mul_f32_e32 v22, v22, v30
	v_mul_f32_e32 v23, v24, v23
	v_add_f32_e32 v24, 1.0, v149
	v_mul_f32_e32 v21, v21, v29
	v_mul_f32_e32 v24, v25, v24
	v_mul_f32_e32 v0, 4.0, v0
	v_mul_f32_e32 v19, 4.0, v19
	v_mul_f32_e32 v25, 4.0, v22
	v_mov_b32_e32 v22, v171
	v_mul_f32_e32 v24, v24, v27
	v_mul_f32_e32 v27, 4.0, v23
	v_cvt_pk_fp8_f32 v22, v0, v19
	v_mul_f32_e32 v0, 4.0, v18
	v_mul_f32_e32 v18, 4.0, v21
	v_mov_b32_e32 v23, v171
	v_cvt_pk_fp8_f32 v23, v0, v18
	v_mul_f32_e32 v0, 4.0, v26
	v_mul_f32_e32 v18, 4.0, v24
	v_ashrrev_i32_e32 v21, 31, v20
	v_cvt_pk_fp8_f32 v23, v0, v18 op_sel:[0,0,1]
	v_lshlrev_b64 v[18:19], 11, v[20:21]
	v_fmamk_f32 v21, v138, 0x3a800000, v228
	v_cvt_pk_fp8_f32 v22, v25, v27 op_sel:[0,0,1]
	v_min_f32_e32 v21, 0x40e00000, v21
	v_mul_f32_e32 v25, 0x3fd9db23, v21
	v_lshl_add_u64 v[18:19], s[14:15], 0, v[18:19]
	v_mul_f32_e32 v25, 0xbfb8aa3b, v25
	v_lshl_add_u64 v[18:19], v[18:19], 0, v[170:171]
	v_exp_f32_e32 v25, v25
	global_store_dwordx2 v[18:19], v[22:23], off
	v_fmamk_f32 v22, v134, 0x3a800000, v232
	v_fmamk_f32 v0, v142, 0x3a800000, v224
	v_med3_f32 v22, v22, s59, v189
	v_min_f32_e32 v0, 0x40e00000, v0
	v_add_f32_e32 v22, 1.0, v22
	v_mul_f32_e32 v24, 0x3fd9db23, v0
	v_mul_f32_e32 v0, v0, v22
	v_add_f32_e32 v22, 1.0, v25
	v_fmamk_f32 v23, v130, 0x3a800000, v236
	v_rcp_f32_e32 v22, v22
	v_med3_f32 v23, v23, s59, v189
	v_mul_f32_e32 v24, 0xbfb8aa3b, v24
	v_exp_f32_e32 v24, v24
	v_add_f32_e32 v23, 1.0, v23
	v_mul_f32_e32 v21, v21, v23
	v_mul_f32_e32 v21, v21, v22
	v_fmamk_f32 v22, v143, 0x3a800000, v225
	v_min_f32_e32 v22, 0x40e00000, v22
	v_add_f32_e32 v24, 1.0, v24
	v_fmamk_f32 v23, v139, 0x3a800000, v229
	v_mul_f32_e32 v26, 0x3fd9db23, v22
	v_rcp_f32_e32 v24, v24
	v_min_f32_e32 v23, 0x40e00000, v23
	v_mul_f32_e32 v26, 0xbfb8aa3b, v26
	v_exp_f32_e32 v26, v26
	v_mul_f32_e32 v27, 0x3fd9db23, v23
	v_mul_f32_e32 v27, 0xbfb8aa3b, v27
	v_exp_f32_e32 v27, v27
	v_mul_f32_e32 v0, v0, v24
	v_fmamk_f32 v24, v135, 0x3a800000, v233
	v_med3_f32 v24, v24, s59, v189
	v_add_f32_e32 v26, 1.0, v26
	v_add_f32_e32 v24, 1.0, v24
	v_rcp_f32_e32 v26, v26
	v_mul_f32_e32 v22, v22, v24
	v_add_f32_e32 v24, 1.0, v27
	v_fmamk_f32 v25, v131, 0x3a800000, v237
	v_rcp_f32_e32 v24, v24
	v_med3_f32 v25, v25, s59, v189
	v_mul_f32_e32 v26, v22, v26
	v_add_f32_e32 v22, 1.0, v25
	v_mul_f32_e32 v22, v23, v22
	v_mul_f32_e32 v23, v22, v24
	v_fmamk_f32 v22, v144, 0x3a800000, v226
	v_min_f32_e32 v22, 0x40e00000, v22
	v_fmamk_f32 v24, v140, 0x3a800000, v230
	v_mul_f32_e32 v28, 0x3fd9db23, v22
	v_min_f32_e32 v24, 0x40e00000, v24
	v_mul_f32_e32 v28, 0xbfb8aa3b, v28
	v_exp_f32_e32 v28, v28
	v_mul_f32_e32 v29, 0x3fd9db23, v24
	v_mul_f32_e32 v29, 0xbfb8aa3b, v29
	v_exp_f32_e32 v29, v29
	v_fmamk_f32 v25, v136, 0x3a800000, v234
	v_med3_f32 v25, v25, s59, v189
	v_add_f32_e32 v28, 1.0, v28
	v_add_f32_e32 v25, 1.0, v25
	v_rcp_f32_e32 v28, v28
	v_mul_f32_e32 v22, v22, v25
	v_add_f32_e32 v25, 1.0, v29
	v_fmamk_f32 v27, v132, 0x3a800000, v238
	v_rcp_f32_e32 v25, v25
	v_med3_f32 v27, v27, s59, v189
	v_mul_f32_e32 v28, v22, v28
	v_add_f32_e32 v22, 1.0, v27
	v_mul_f32_e32 v22, v24, v22
	v_mul_f32_e32 v27, v22, v25
	v_fmamk_f32 v22, v145, 0x3a800000, v227
	v_min_f32_e32 v22, 0x40e00000, v22
	v_fmamk_f32 v24, v141, 0x3a800000, v231
	v_mul_f32_e32 v30, 0x3fd9db23, v22
	v_min_f32_e32 v24, 0x40e00000, v24
	v_mul_f32_e32 v30, 0xbfb8aa3b, v30
	v_exp_f32_e32 v30, v30
	v_mul_f32_e32 v31, 0x3fd9db23, v24
	v_mul_f32_e32 v31, 0xbfb8aa3b, v31
	v_exp_f32_e32 v31, v31
	v_fmamk_f32 v25, v137, 0x3a800000, v235
	v_med3_f32 v25, v25, s59, v189
	v_add_f32_e32 v30, 1.0, v30
	v_add_f32_e32 v25, 1.0, v25
	v_rcp_f32_e32 v30, v30
	v_mul_f32_e32 v22, v22, v25
	v_add_f32_e32 v25, 1.0, v31
	v_fmamk_f32 v29, v133, 0x3a800000, v239
	v_rcp_f32_e32 v25, v25
	v_med3_f32 v29, v29, s59, v189
	v_mul_f32_e32 v30, v22, v30
	v_add_f32_e32 v22, 1.0, v29
	v_mul_f32_e32 v22, v24, v22
	v_mul_f32_e32 v29, v22, v25
	v_mul_f32_e32 v0, 4.0, v0
	v_mul_f32_e32 v25, 4.0, v26
	v_mov_b32_e32 v24, v171
	v_cvt_pk_fp8_f32 v24, v0, v25
	v_mul_f32_e32 v0, 4.0, v21
	v_mul_f32_e32 v21, 4.0, v23
	v_mov_b32_e32 v25, v171
	v_cvt_pk_fp8_f32 v25, v0, v21
	v_or_b32_e32 v22, 16, v20
	v_mul_f32_e32 v26, 4.0, v28
	v_mul_f32_e32 v28, 4.0, v30
	v_mul_f32_e32 v0, 4.0, v27
	v_mul_f32_e32 v21, 4.0, v29
	v_cvt_pk_fp8_f32 v24, v26, v28 op_sel:[0,0,1]
	v_cvt_pk_fp8_f32 v25, v0, v21 op_sel:[0,0,1]
	v_ashrrev_i32_e32 v23, 31, v22
	v_lshlrev_b64 v[22:23], 11, v[22:23]
	v_lshl_add_u64 v[22:23], s[14:15], 0, v[22:23]
	v_fmamk_f32 v21, v122, 0x3a800000, v228
	v_lshl_add_u64 v[22:23], v[22:23], 0, v[170:171]
	v_min_f32_e32 v21, 0x40e00000, v21
	global_store_dwordx2 v[22:23], v[24:25], off
	v_mul_f32_e32 v25, 0x3fd9db23, v21
	v_mul_f32_e32 v25, 0xbfb8aa3b, v25
	v_exp_f32_e32 v25, v25
	v_fmamk_f32 v22, v118, 0x3a800000, v232
	v_fmamk_f32 v0, v126, 0x3a800000, v224
	v_med3_f32 v22, v22, s59, v189
	v_min_f32_e32 v0, 0x40e00000, v0
	v_add_f32_e32 v22, 1.0, v22
	v_mul_f32_e32 v24, 0x3fd9db23, v0
	v_mul_f32_e32 v0, v0, v22
	v_add_f32_e32 v22, 1.0, v25
	v_fmamk_f32 v23, v114, 0x3a800000, v236
	v_rcp_f32_e32 v22, v22
	v_med3_f32 v23, v23, s59, v189
	v_mul_f32_e32 v24, 0xbfb8aa3b, v24
	v_exp_f32_e32 v24, v24
	v_add_f32_e32 v23, 1.0, v23
	v_mul_f32_e32 v21, v21, v23
	v_mul_f32_e32 v21, v21, v22
	v_fmamk_f32 v22, v127, 0x3a800000, v225
	v_min_f32_e32 v22, 0x40e00000, v22
	v_add_f32_e32 v24, 1.0, v24
	v_fmamk_f32 v23, v123, 0x3a800000, v229
	v_mul_f32_e32 v26, 0x3fd9db23, v22
	v_rcp_f32_e32 v24, v24
	v_min_f32_e32 v23, 0x40e00000, v23
	v_mul_f32_e32 v26, 0xbfb8aa3b, v26
	v_exp_f32_e32 v26, v26
	v_mul_f32_e32 v27, 0x3fd9db23, v23
	v_mul_f32_e32 v27, 0xbfb8aa3b, v27
	v_exp_f32_e32 v27, v27
	v_mul_f32_e32 v0, v0, v24
	v_fmamk_f32 v24, v119, 0x3a800000, v233
	v_med3_f32 v24, v24, s59, v189
	v_add_f32_e32 v26, 1.0, v26
	v_add_f32_e32 v24, 1.0, v24
	v_rcp_f32_e32 v26, v26
	v_mul_f32_e32 v22, v22, v24
	v_add_f32_e32 v24, 1.0, v27
	v_fmamk_f32 v25, v115, 0x3a800000, v237
	v_rcp_f32_e32 v24, v24
	v_med3_f32 v25, v25, s59, v189
	v_mul_f32_e32 v26, v22, v26
	v_add_f32_e32 v22, 1.0, v25
	v_mul_f32_e32 v22, v23, v22
	v_mul_f32_e32 v23, v22, v24
	v_fmamk_f32 v22, v128, 0x3a800000, v226
	v_min_f32_e32 v22, 0x40e00000, v22
	v_fmamk_f32 v24, v124, 0x3a800000, v230
	v_mul_f32_e32 v28, 0x3fd9db23, v22
	v_min_f32_e32 v24, 0x40e00000, v24
	v_mul_f32_e32 v28, 0xbfb8aa3b, v28
	v_exp_f32_e32 v28, v28
	v_mul_f32_e32 v29, 0x3fd9db23, v24
	v_mul_f32_e32 v29, 0xbfb8aa3b, v29
	v_exp_f32_e32 v29, v29
	v_fmamk_f32 v25, v120, 0x3a800000, v234
	v_med3_f32 v25, v25, s59, v189
	v_add_f32_e32 v28, 1.0, v28
	v_add_f32_e32 v25, 1.0, v25
	v_rcp_f32_e32 v28, v28
	v_mul_f32_e32 v22, v22, v25
	v_add_f32_e32 v25, 1.0, v29
	v_fmamk_f32 v27, v116, 0x3a800000, v238
	v_rcp_f32_e32 v25, v25
	v_med3_f32 v27, v27, s59, v189
	v_mul_f32_e32 v28, v22, v28
	v_add_f32_e32 v22, 1.0, v27
	v_mul_f32_e32 v22, v24, v22
	v_mul_f32_e32 v27, v22, v25
	v_fmamk_f32 v22, v129, 0x3a800000, v227
	v_min_f32_e32 v22, 0x40e00000, v22
	v_fmamk_f32 v24, v125, 0x3a800000, v231
	v_mul_f32_e32 v30, 0x3fd9db23, v22
	v_min_f32_e32 v24, 0x40e00000, v24
	v_mul_f32_e32 v30, 0xbfb8aa3b, v30
	v_exp_f32_e32 v30, v30
	v_mul_f32_e32 v31, 0x3fd9db23, v24
	v_mul_f32_e32 v31, 0xbfb8aa3b, v31
	v_exp_f32_e32 v31, v31
	v_fmamk_f32 v25, v121, 0x3a800000, v235
	v_med3_f32 v25, v25, s59, v189
	v_add_f32_e32 v30, 1.0, v30
	v_add_f32_e32 v25, 1.0, v25
	v_rcp_f32_e32 v30, v30
	v_mul_f32_e32 v22, v22, v25
	v_add_f32_e32 v25, 1.0, v31
	v_fmamk_f32 v29, v117, 0x3a800000, v239
	v_rcp_f32_e32 v25, v25
	v_med3_f32 v29, v29, s59, v189
	v_mul_f32_e32 v30, v22, v30
	v_add_f32_e32 v22, 1.0, v29
	v_mul_f32_e32 v22, v24, v22
	v_mul_f32_e32 v29, v22, v25
	v_mul_f32_e32 v0, 4.0, v0
	v_mul_f32_e32 v25, 4.0, v26
	v_mov_b32_e32 v24, v171
	v_cvt_pk_fp8_f32 v24, v0, v25
	v_mul_f32_e32 v0, 4.0, v21
	v_mul_f32_e32 v21, 4.0, v23
	v_mov_b32_e32 v25, v171
	v_cvt_pk_fp8_f32 v25, v0, v21
	v_or_b32_e32 v22, 32, v20
	v_mul_f32_e32 v26, 4.0, v28
	v_mul_f32_e32 v28, 4.0, v30
	v_mul_f32_e32 v0, 4.0, v27
	v_mul_f32_e32 v21, 4.0, v29
	v_cvt_pk_fp8_f32 v24, v26, v28 op_sel:[0,0,1]
	v_cvt_pk_fp8_f32 v25, v0, v21 op_sel:[0,0,1]
	v_ashrrev_i32_e32 v23, 31, v22
	v_lshlrev_b64 v[22:23], 11, v[22:23]
	v_lshl_add_u64 v[22:23], s[14:15], 0, v[22:23]
	v_fmamk_f32 v21, v106, 0x3a800000, v228
	v_lshl_add_u64 v[22:23], v[22:23], 0, v[170:171]
	v_fmamk_f32 v0, v110, 0x3a800000, v224
	v_min_f32_e32 v21, 0x40e00000, v21
	global_store_dwordx2 v[22:23], v[24:25], off
	v_min_f32_e32 v0, 0x40e00000, v0
	v_mul_f32_e32 v25, 0x3fd9db23, v21
	v_mul_f32_e32 v24, 0x3fd9db23, v0
	v_mul_f32_e32 v25, 0xbfb8aa3b, v25
	v_mul_f32_e32 v24, 0xbfb8aa3b, v24
	v_exp_f32_e32 v25, v25
	v_fmamk_f32 v22, v102, 0x3a800000, v232
	v_exp_f32_e32 v24, v24
	v_med3_f32 v22, v22, s59, v189
	v_fmamk_f32 v23, v98, 0x3a800000, v236
	v_med3_f32 v23, v23, s59, v189
	v_add_f32_e32 v22, 1.0, v22
	v_mul_f32_e32 v0, v0, v22
	v_add_f32_e32 v22, 1.0, v25
	v_add_f32_e32 v23, 1.0, v23
	v_add_f32_e32 v24, 1.0, v24
	v_rcp_f32_e32 v22, v22
	v_mul_f32_e32 v21, v21, v23
	v_fmamk_f32 v23, v107, 0x3a800000, v229
	v_rcp_f32_e32 v24, v24
	v_min_f32_e32 v23, 0x40e00000, v23
	v_mul_f32_e32 v27, 0x3fd9db23, v23
	v_mul_f32_e32 v27, 0xbfb8aa3b, v27
	v_mul_f32_e32 v21, v21, v22
	v_fmamk_f32 v22, v111, 0x3a800000, v225
	v_exp_f32_e32 v27, v27
	v_mul_f32_e32 v0, v0, v24
	v_min_f32_e32 v22, 0x40e00000, v22
	v_fmamk_f32 v24, v103, 0x3a800000, v233
	v_med3_f32 v24, v24, s59, v189
	v_mul_f32_e32 v26, 0x3fd9db23, v22
	v_add_f32_e32 v24, 1.0, v24
	v_mul_f32_e32 v26, 0xbfb8aa3b, v26
	v_exp_f32_e32 v26, v26
	v_mul_f32_e32 v22, v22, v24
	v_add_f32_e32 v24, 1.0, v27
	v_fmamk_f32 v25, v99, 0x3a800000, v237
	v_rcp_f32_e32 v24, v24
	v_med3_f32 v25, v25, s59, v189
	v_add_f32_e32 v25, 1.0, v25
	v_add_f32_e32 v26, 1.0, v26
	v_mul_f32_e32 v23, v23, v25
	v_fmamk_f32 v25, v108, 0x3a800000, v230
	v_rcp_f32_e32 v26, v26
	v_mul_f32_e32 v23, v23, v24
	v_fmamk_f32 v24, v112, 0x3a800000, v226
	v_min_f32_e32 v25, 0x40e00000, v25
	v_min_f32_e32 v24, 0x40e00000, v24
	v_mul_f32_e32 v29, 0x3fd9db23, v25
	v_mul_f32_e32 v28, 0x3fd9db23, v24
	v_mul_f32_e32 v29, 0xbfb8aa3b, v29
	v_mul_f32_e32 v28, 0xbfb8aa3b, v28
	v_exp_f32_e32 v29, v29
	v_mul_f32_e32 v22, v22, v26
	v_fmamk_f32 v26, v104, 0x3a800000, v234
	v_exp_f32_e32 v28, v28
	v_med3_f32 v26, v26, s59, v189
	v_fmamk_f32 v27, v100, 0x3a800000, v238
	v_med3_f32 v27, v27, s59, v189
	v_add_f32_e32 v26, 1.0, v26
	v_mul_f32_e32 v24, v24, v26
	v_add_f32_e32 v26, 1.0, v29
	v_add_f32_e32 v27, 1.0, v27
	v_add_f32_e32 v28, 1.0, v28
	v_rcp_f32_e32 v26, v26
	v_mul_f32_e32 v25, v25, v27
	v_fmamk_f32 v27, v109, 0x3a800000, v231
	v_rcp_f32_e32 v28, v28
	v_min_f32_e32 v27, 0x40e00000, v27
	v_mul_f32_e32 v31, 0x3fd9db23, v27
	v_mul_f32_e32 v31, 0xbfb8aa3b, v31
	v_mul_f32_e32 v25, v25, v26
	v_fmamk_f32 v26, v113, 0x3a800000, v227
	v_exp_f32_e32 v31, v31
	v_mul_f32_e32 v24, v24, v28
	v_min_f32_e32 v26, 0x40e00000, v26
	v_fmamk_f32 v28, v105, 0x3a800000, v235
	v_med3_f32 v28, v28, s59, v189
	v_mul_f32_e32 v30, 0x3fd9db23, v26
	v_add_f32_e32 v28, 1.0, v28
	v_mul_f32_e32 v30, 0xbfb8aa3b, v30
	v_exp_f32_e32 v30, v30
	v_mul_f32_e32 v26, v26, v28
	v_add_f32_e32 v28, 1.0, v31
	v_fmamk_f32 v29, v101, 0x3a800000, v239
	v_rcp_f32_e32 v28, v28
	v_med3_f32 v29, v29, s59, v189
	v_add_f32_e32 v29, 1.0, v29
	v_add_f32_e32 v30, 1.0, v30
	v_mul_f32_e32 v27, v27, v29
	v_rcp_f32_e32 v30, v30
	v_mul_f32_e32 v27, v27, v28
	v_mul_f32_e32 v0, 4.0, v0
	v_mul_f32_e32 v28, 4.0, v22
	v_mov_b32_e32 v22, v171
	v_cvt_pk_fp8_f32 v22, v0, v28
	v_mul_f32_e32 v0, 4.0, v21
	v_mul_f32_e32 v21, 4.0, v23
	v_mov_b32_e32 v23, v171
	v_cvt_pk_fp8_f32 v23, v0, v21
	v_mul_f32_e32 v26, v26, v30
	v_or_b32_e32 v20, 48, v20
	v_mul_f32_e32 v24, 4.0, v24
	v_mul_f32_e32 v26, 4.0, v26
	v_mul_f32_e32 v0, 4.0, v25
	v_mul_f32_e32 v21, 4.0, v27
	v_cvt_pk_fp8_f32 v22, v24, v26 op_sel:[0,0,1]
	v_cvt_pk_fp8_f32 v23, v0, v21 op_sel:[0,0,1]
	v_ashrrev_i32_e32 v21, 31, v20
	v_lshlrev_b64 v[20:21], 11, v[20:21]
	v_lshl_add_u64 v[20:21], s[14:15], 0, v[20:21]
	v_lshl_add_u64 v[20:21], v[20:21], 0, v[170:171]
	global_store_dwordx2 v[20:21], v[22:23], off
	v_fmamk_f32 v20, v90, 0x3a800000, v228
	v_fmamk_f32 v0, v94, 0x3a800000, v224
	v_min_f32_e32 v20, 0x40e00000, v20
	v_min_f32_e32 v0, 0x40e00000, v0
	v_mul_f32_e32 v24, 0x3fd9db23, v20
	v_mul_f32_e32 v23, 0x3fd9db23, v0
	v_mul_f32_e32 v24, 0xbfb8aa3b, v24
	v_mul_f32_e32 v23, 0xbfb8aa3b, v23
	v_exp_f32_e32 v24, v24
	v_fmamk_f32 v21, v86, 0x3a800000, v232
	v_exp_f32_e32 v23, v23
	v_med3_f32 v21, v21, s59, v189
	v_fmamk_f32 v22, v82, 0x3a800000, v236
	v_med3_f32 v22, v22, s59, v189
	v_add_f32_e32 v21, 1.0, v21
	v_mul_f32_e32 v0, v0, v21
	v_add_f32_e32 v21, 1.0, v24
	v_add_f32_e32 v22, 1.0, v22
	v_add_f32_e32 v23, 1.0, v23
	v_rcp_f32_e32 v21, v21
	v_mul_f32_e32 v20, v20, v22
	v_fmamk_f32 v22, v91, 0x3a800000, v229
	v_rcp_f32_e32 v23, v23
	v_min_f32_e32 v22, 0x40e00000, v22
	v_mul_f32_e32 v26, 0x3fd9db23, v22
	v_mul_f32_e32 v26, 0xbfb8aa3b, v26
	v_mul_f32_e32 v21, v20, v21
	v_fmamk_f32 v20, v95, 0x3a800000, v225
	v_exp_f32_e32 v26, v26
	v_mul_f32_e32 v0, v0, v23
	v_min_f32_e32 v20, 0x40e00000, v20
	v_fmamk_f32 v23, v87, 0x3a800000, v233
	v_med3_f32 v23, v23, s59, v189
	v_mul_f32_e32 v25, 0x3fd9db23, v20
	v_add_f32_e32 v23, 1.0, v23
	v_mul_f32_e32 v25, 0xbfb8aa3b, v25
	v_exp_f32_e32 v25, v25
	v_mul_f32_e32 v20, v20, v23
	v_add_f32_e32 v23, 1.0, v26
	v_fmamk_f32 v24, v83, 0x3a800000, v237
	v_rcp_f32_e32 v23, v23
	v_med3_f32 v24, v24, s59, v189
	v_add_f32_e32 v24, 1.0, v24
	v_add_f32_e32 v25, 1.0, v25
	v_mul_f32_e32 v22, v22, v24
	v_fmamk_f32 v24, v92, 0x3a800000, v230
	v_rcp_f32_e32 v25, v25
	v_mul_f32_e32 v22, v22, v23
	v_fmamk_f32 v23, v96, 0x3a800000, v226
	v_min_f32_e32 v24, 0x40e00000, v24
	v_min_f32_e32 v23, 0x40e00000, v23
	v_mul_f32_e32 v28, 0x3fd9db23, v24
	v_mul_f32_e32 v27, 0x3fd9db23, v23
	v_mul_f32_e32 v28, 0xbfb8aa3b, v28
	v_mul_f32_e32 v27, 0xbfb8aa3b, v27
	v_exp_f32_e32 v28, v28
	v_mul_f32_e32 v20, v20, v25
	v_fmamk_f32 v25, v88, 0x3a800000, v234
	v_exp_f32_e32 v27, v27
	v_med3_f32 v25, v25, s59, v189
	v_fmamk_f32 v26, v84, 0x3a800000, v238
	v_med3_f32 v26, v26, s59, v189
	v_add_f32_e32 v25, 1.0, v25
	v_mul_f32_e32 v23, v23, v25
	v_add_f32_e32 v25, 1.0, v28
	v_add_f32_e32 v26, 1.0, v26
	v_add_f32_e32 v27, 1.0, v27
	v_rcp_f32_e32 v25, v25
	v_mul_f32_e32 v24, v24, v26
	v_fmamk_f32 v26, v93, 0x3a800000, v231
	v_rcp_f32_e32 v27, v27
	v_min_f32_e32 v26, 0x40e00000, v26
	v_mul_f32_e32 v30, 0x3fd9db23, v26
	v_mul_f32_e32 v30, 0xbfb8aa3b, v30
	v_mul_f32_e32 v24, v24, v25
	v_fmamk_f32 v25, v97, 0x3a800000, v227
	v_exp_f32_e32 v30, v30
	v_mul_f32_e32 v23, v23, v27
	v_min_f32_e32 v25, 0x40e00000, v25
	v_fmamk_f32 v27, v89, 0x3a800000, v235
	v_med3_f32 v27, v27, s59, v189
	v_mul_f32_e32 v29, 0x3fd9db23, v25
	v_add_f32_e32 v27, 1.0, v27
	v_mul_f32_e32 v29, 0xbfb8aa3b, v29
	v_exp_f32_e32 v29, v29
	v_mul_f32_e32 v25, v25, v27
	v_add_f32_e32 v27, 1.0, v30
	v_fmamk_f32 v28, v85, 0x3a800000, v239
	v_rcp_f32_e32 v27, v27
	v_med3_f32 v28, v28, s59, v189
	v_add_f32_e32 v28, 1.0, v28
	v_add_f32_e32 v29, 1.0, v29
	v_mul_f32_e32 v26, v26, v28
	v_rcp_f32_e32 v29, v29
	v_mul_f32_e32 v26, v26, v27
	v_mul_f32_e32 v0, 4.0, v0
	v_mul_f32_e32 v27, 4.0, v20
	v_mov_b32_e32 v20, v171
	v_cvt_pk_fp8_f32 v20, v0, v27
	v_mul_f32_e32 v0, 4.0, v21
	v_mul_f32_e32 v22, 4.0, v22
	v_mov_b32_e32 v21, v171
	v_cvt_pk_fp8_f32 v21, v0, v22
	v_mul_f32_e32 v25, v25, v29
	v_mul_f32_e32 v23, 4.0, v23
	v_mul_f32_e32 v25, 4.0, v25
	v_mul_f32_e32 v0, 4.0, v24
	v_mul_f32_e32 v22, 4.0, v26
	v_cvt_pk_fp8_f32 v20, v23, v25 op_sel:[0,0,1]
	v_cvt_pk_fp8_f32 v21, v0, v22 op_sel:[0,0,1]
	v_add_co_u32_e32 v22, vcc, s60, v18
	v_fmamk_f32 v0, v78, 0x3a800000, v224
	s_nop 0
	v_addc_co_u32_e32 v23, vcc, 0, v19, vcc
	global_store_dwordx2 v[22:23], v[20:21], off
	v_fmamk_f32 v20, v74, 0x3a800000, v228
	v_min_f32_e32 v20, 0x40e00000, v20
	v_min_f32_e32 v0, 0x40e00000, v0
	v_mul_f32_e32 v24, 0x3fd9db23, v20
	v_mul_f32_e32 v23, 0x3fd9db23, v0
	v_mul_f32_e32 v24, 0xbfb8aa3b, v24
	v_mul_f32_e32 v23, 0xbfb8aa3b, v23
	v_exp_f32_e32 v24, v24
	v_fmamk_f32 v21, v70, 0x3a800000, v232
	v_exp_f32_e32 v23, v23
	v_med3_f32 v21, v21, s59, v189
	v_fmamk_f32 v22, v66, 0x3a800000, v236
	v_med3_f32 v22, v22, s59, v189
	v_add_f32_e32 v21, 1.0, v21
	v_mul_f32_e32 v0, v0, v21
	v_add_f32_e32 v21, 1.0, v24
	v_add_f32_e32 v22, 1.0, v22
	v_add_f32_e32 v23, 1.0, v23
	v_rcp_f32_e32 v21, v21
	v_mul_f32_e32 v20, v20, v22
	v_fmamk_f32 v22, v75, 0x3a800000, v229
	v_rcp_f32_e32 v23, v23
	v_min_f32_e32 v22, 0x40e00000, v22
	v_mul_f32_e32 v26, 0x3fd9db23, v22
	v_mul_f32_e32 v26, 0xbfb8aa3b, v26
	v_mul_f32_e32 v21, v20, v21
	v_fmamk_f32 v20, v79, 0x3a800000, v225
	v_exp_f32_e32 v26, v26
	v_mul_f32_e32 v0, v0, v23
	v_min_f32_e32 v20, 0x40e00000, v20
	v_fmamk_f32 v23, v71, 0x3a800000, v233
	v_med3_f32 v23, v23, s59, v189
	v_mul_f32_e32 v25, 0x3fd9db23, v20
	v_add_f32_e32 v23, 1.0, v23
	v_mul_f32_e32 v25, 0xbfb8aa3b, v25
	v_exp_f32_e32 v25, v25
	v_mul_f32_e32 v20, v20, v23
	v_add_f32_e32 v23, 1.0, v26
	v_fmamk_f32 v24, v67, 0x3a800000, v237
	v_rcp_f32_e32 v23, v23
	v_med3_f32 v24, v24, s59, v189
	v_add_f32_e32 v24, 1.0, v24
	v_add_f32_e32 v25, 1.0, v25
	v_mul_f32_e32 v22, v22, v24
	v_fmamk_f32 v24, v76, 0x3a800000, v230
	v_rcp_f32_e32 v25, v25
	v_mul_f32_e32 v22, v22, v23
	v_fmamk_f32 v23, v80, 0x3a800000, v226
	v_min_f32_e32 v24, 0x40e00000, v24
	v_min_f32_e32 v23, 0x40e00000, v23
	v_mul_f32_e32 v28, 0x3fd9db23, v24
	v_mul_f32_e32 v27, 0x3fd9db23, v23
	v_mul_f32_e32 v28, 0xbfb8aa3b, v28
	v_mul_f32_e32 v27, 0xbfb8aa3b, v27
	v_exp_f32_e32 v28, v28
	v_mul_f32_e32 v20, v20, v25
	v_fmamk_f32 v25, v72, 0x3a800000, v234
	v_exp_f32_e32 v27, v27
	v_med3_f32 v25, v25, s59, v189
	v_fmamk_f32 v26, v68, 0x3a800000, v238
	v_med3_f32 v26, v26, s59, v189
	v_add_f32_e32 v25, 1.0, v25
	v_mul_f32_e32 v23, v23, v25
	v_add_f32_e32 v25, 1.0, v28
	v_add_f32_e32 v26, 1.0, v26
	v_add_f32_e32 v27, 1.0, v27
	v_rcp_f32_e32 v25, v25
	v_mul_f32_e32 v24, v24, v26
	v_fmamk_f32 v26, v77, 0x3a800000, v231
	v_rcp_f32_e32 v27, v27
	v_min_f32_e32 v26, 0x40e00000, v26
	v_mul_f32_e32 v30, 0x3fd9db23, v26
	v_mul_f32_e32 v30, 0xbfb8aa3b, v30
	v_mul_f32_e32 v24, v24, v25
	v_fmamk_f32 v25, v81, 0x3a800000, v227
	v_exp_f32_e32 v30, v30
	v_mul_f32_e32 v23, v23, v27
	v_min_f32_e32 v25, 0x40e00000, v25
	v_fmamk_f32 v27, v73, 0x3a800000, v235
	v_med3_f32 v27, v27, s59, v189
	v_mul_f32_e32 v29, 0x3fd9db23, v25
	v_add_f32_e32 v27, 1.0, v27
	v_mul_f32_e32 v29, 0xbfb8aa3b, v29
	v_exp_f32_e32 v29, v29
	v_mul_f32_e32 v25, v25, v27
	v_add_f32_e32 v27, 1.0, v30
	v_fmamk_f32 v28, v69, 0x3a800000, v239
	v_rcp_f32_e32 v27, v27
	v_med3_f32 v28, v28, s59, v189
	v_add_f32_e32 v28, 1.0, v28
	v_add_f32_e32 v29, 1.0, v29
	v_mul_f32_e32 v26, v26, v28
	v_rcp_f32_e32 v29, v29
	v_mul_f32_e32 v26, v26, v27
	v_mul_f32_e32 v0, 4.0, v0
	v_mul_f32_e32 v27, 4.0, v20
	v_mov_b32_e32 v20, v171
	v_cvt_pk_fp8_f32 v20, v0, v27
	v_mul_f32_e32 v0, 4.0, v21
	v_mul_f32_e32 v22, 4.0, v22
	v_mov_b32_e32 v21, v171
	v_cvt_pk_fp8_f32 v21, v0, v22
	v_mul_f32_e32 v25, v25, v29
	v_mul_f32_e32 v23, 4.0, v23
	v_mul_f32_e32 v25, 4.0, v25
	v_mul_f32_e32 v0, 4.0, v24
	v_mul_f32_e32 v22, 4.0, v26
	v_cvt_pk_fp8_f32 v20, v23, v25 op_sel:[0,0,1]
	v_cvt_pk_fp8_f32 v21, v0, v22 op_sel:[0,0,1]
	v_add_co_u32_e32 v22, vcc, s61, v18
	v_fmamk_f32 v0, v62, 0x3a800000, v224
	s_nop 0
	v_addc_co_u32_e32 v23, vcc, 0, v19, vcc
	global_store_dwordx2 v[22:23], v[20:21], off
	v_fmamk_f32 v20, v58, 0x3a800000, v228
	v_min_f32_e32 v20, 0x40e00000, v20
	v_min_f32_e32 v0, 0x40e00000, v0
	v_mul_f32_e32 v24, 0x3fd9db23, v20
	v_mul_f32_e32 v23, 0x3fd9db23, v0
	v_mul_f32_e32 v24, 0xbfb8aa3b, v24
	v_mul_f32_e32 v23, 0xbfb8aa3b, v23
	v_exp_f32_e32 v24, v24
	v_fmamk_f32 v21, v54, 0x3a800000, v232
	v_exp_f32_e32 v23, v23
	v_med3_f32 v21, v21, s59, v189
	v_fmamk_f32 v22, v50, 0x3a800000, v236
	v_med3_f32 v22, v22, s59, v189
	v_add_f32_e32 v21, 1.0, v21
	v_mul_f32_e32 v0, v0, v21
	v_add_f32_e32 v21, 1.0, v24
	v_add_f32_e32 v22, 1.0, v22
	v_add_f32_e32 v23, 1.0, v23
	v_rcp_f32_e32 v21, v21
	v_mul_f32_e32 v20, v20, v22
	v_fmamk_f32 v22, v59, 0x3a800000, v229
	v_rcp_f32_e32 v23, v23
	v_min_f32_e32 v22, 0x40e00000, v22
	v_mul_f32_e32 v26, 0x3fd9db23, v22
	v_mul_f32_e32 v26, 0xbfb8aa3b, v26
	v_mul_f32_e32 v21, v20, v21
	v_fmamk_f32 v20, v63, 0x3a800000, v225
	v_exp_f32_e32 v26, v26
	v_mul_f32_e32 v0, v0, v23
	v_min_f32_e32 v20, 0x40e00000, v20
	v_fmamk_f32 v23, v55, 0x3a800000, v233
	v_med3_f32 v23, v23, s59, v189
	v_mul_f32_e32 v25, 0x3fd9db23, v20
	v_add_f32_e32 v23, 1.0, v23
	v_mul_f32_e32 v25, 0xbfb8aa3b, v25
	v_exp_f32_e32 v25, v25
	v_mul_f32_e32 v20, v20, v23
	v_add_f32_e32 v23, 1.0, v26
	v_fmamk_f32 v24, v51, 0x3a800000, v237
	v_rcp_f32_e32 v23, v23
	v_med3_f32 v24, v24, s59, v189
	v_add_f32_e32 v24, 1.0, v24
	v_add_f32_e32 v25, 1.0, v25
	v_mul_f32_e32 v22, v22, v24
	v_fmamk_f32 v24, v60, 0x3a800000, v230
	v_rcp_f32_e32 v25, v25
	v_mul_f32_e32 v22, v22, v23
	v_fmamk_f32 v23, v64, 0x3a800000, v226
	v_min_f32_e32 v24, 0x40e00000, v24
	v_min_f32_e32 v23, 0x40e00000, v23
	v_mul_f32_e32 v28, 0x3fd9db23, v24
	v_mul_f32_e32 v27, 0x3fd9db23, v23
	v_mul_f32_e32 v28, 0xbfb8aa3b, v28
	v_mul_f32_e32 v27, 0xbfb8aa3b, v27
	v_exp_f32_e32 v28, v28
	v_mul_f32_e32 v20, v20, v25
	v_fmamk_f32 v25, v56, 0x3a800000, v234
	v_exp_f32_e32 v27, v27
	v_med3_f32 v25, v25, s59, v189
	v_fmamk_f32 v26, v52, 0x3a800000, v238
	v_med3_f32 v26, v26, s59, v189
	v_add_f32_e32 v25, 1.0, v25
	v_mul_f32_e32 v23, v23, v25
	v_add_f32_e32 v25, 1.0, v28
	v_add_f32_e32 v26, 1.0, v26
	v_add_f32_e32 v27, 1.0, v27
	v_rcp_f32_e32 v25, v25
	v_mul_f32_e32 v24, v24, v26
	v_fmamk_f32 v26, v61, 0x3a800000, v231
	v_rcp_f32_e32 v27, v27
	v_min_f32_e32 v26, 0x40e00000, v26
	v_mul_f32_e32 v30, 0x3fd9db23, v26
	v_mul_f32_e32 v30, 0xbfb8aa3b, v30
	v_mul_f32_e32 v24, v24, v25
	v_fmamk_f32 v25, v65, 0x3a800000, v227
	v_exp_f32_e32 v30, v30
	v_mul_f32_e32 v23, v23, v27
	v_min_f32_e32 v25, 0x40e00000, v25
	v_fmamk_f32 v27, v57, 0x3a800000, v235
	v_med3_f32 v27, v27, s59, v189
	v_mul_f32_e32 v29, 0x3fd9db23, v25
	v_add_f32_e32 v27, 1.0, v27
	v_mul_f32_e32 v29, 0xbfb8aa3b, v29
	v_exp_f32_e32 v29, v29
	v_mul_f32_e32 v25, v25, v27
	v_add_f32_e32 v27, 1.0, v30
	v_fmamk_f32 v28, v53, 0x3a800000, v239
	v_rcp_f32_e32 v27, v27
	v_med3_f32 v28, v28, s59, v189
	v_add_f32_e32 v28, 1.0, v28
	v_add_f32_e32 v29, 1.0, v29
	v_mul_f32_e32 v26, v26, v28
	v_rcp_f32_e32 v29, v29
	v_mul_f32_e32 v26, v26, v27
	v_mul_f32_e32 v0, 4.0, v0
	v_mul_f32_e32 v27, 4.0, v20
	v_mov_b32_e32 v20, v171
	v_cvt_pk_fp8_f32 v20, v0, v27
	v_mul_f32_e32 v0, 4.0, v21
	v_mul_f32_e32 v22, 4.0, v22
	v_mov_b32_e32 v21, v171
	v_cvt_pk_fp8_f32 v21, v0, v22
	v_mul_f32_e32 v25, v25, v29
	v_mul_f32_e32 v23, 4.0, v23
	v_mul_f32_e32 v25, 4.0, v25
	v_mul_f32_e32 v0, 4.0, v24
	v_mul_f32_e32 v22, 4.0, v26
	v_cvt_pk_fp8_f32 v20, v23, v25 op_sel:[0,0,1]
	v_cvt_pk_fp8_f32 v21, v0, v22 op_sel:[0,0,1]
	v_add_co_u32_e32 v22, vcc, s62, v18
	v_fmamk_f32 v2, v42, 0x3a800000, v228
	s_nop 0
	v_addc_co_u32_e32 v23, vcc, 0, v19, vcc
	v_min_f32_e32 v2, 0x40e00000, v2
	global_store_dwordx2 v[22:23], v[20:21], off
	v_mul_f32_e32 v20, 0x3fd9db23, v2
	v_mul_f32_e32 v20, 0xbfb8aa3b, v20
	v_exp_f32_e32 v20, v20
	v_fmamk_f32 v0, v46, 0x3a800000, v224
	v_fmamk_f32 v10, v38, 0x3a800000, v232
	v_med3_f32 v10, v10, s59, v189
	v_min_f32_e32 v0, 0x40e00000, v0
	v_add_f32_e32 v10, 1.0, v10
	v_mul_f32_e32 v14, 0x3fd9db23, v0
	v_mul_f32_e32 v0, v0, v10
	v_add_f32_e32 v10, 1.0, v20
	v_fmamk_f32 v6, v34, 0x3a800000, v236
	v_rcp_f32_e32 v10, v10
	v_med3_f32 v6, v6, s59, v189
	v_add_f32_e32 v6, 1.0, v6
	v_mul_f32_e32 v14, 0xbfb8aa3b, v14
	v_mul_f32_e32 v2, v2, v6
	v_exp_f32_e32 v14, v14
	v_mul_f32_e32 v6, v2, v10
	v_fmamk_f32 v2, v47, 0x3a800000, v225
	v_min_f32_e32 v2, 0x40e00000, v2
	v_mul_f32_e32 v11, 0x3fd9db23, v2
	v_mul_f32_e32 v11, 0xbfb8aa3b, v11
	v_add_f32_e32 v14, 1.0, v14
	v_exp_f32_e32 v11, v11
	v_rcp_f32_e32 v14, v14
	v_fmamk_f32 v3, v43, 0x3a800000, v229
	v_min_f32_e32 v3, 0x40e00000, v3
	v_fmamk_f32 v7, v35, 0x3a800000, v237
	v_add_f32_e32 v11, 1.0, v11
	v_mul_f32_e32 v0, v0, v14
	v_fmamk_f32 v10, v39, 0x3a800000, v233
	v_med3_f32 v7, v7, s59, v189
	v_mul_f32_e32 v14, 0x3fd9db23, v3
	v_rcp_f32_e32 v11, v11
	v_med3_f32 v10, v10, s59, v189
	v_mul_f32_e32 v14, 0xbfb8aa3b, v14
	v_add_f32_e32 v7, 1.0, v7
	v_add_f32_e32 v10, 1.0, v10
	v_exp_f32_e32 v14, v14
	v_mul_f32_e32 v3, v3, v7
	v_fmamk_f32 v7, v48, 0x3a800000, v226
	v_mul_f32_e32 v2, v2, v10
	v_min_f32_e32 v7, 0x40e00000, v7
	v_mul_f32_e32 v2, v2, v11
	v_mul_f32_e32 v11, 0x3fd9db23, v7
	v_mul_f32_e32 v11, 0xbfb8aa3b, v11
	v_add_f32_e32 v10, 1.0, v14
	v_fmamk_f32 v4, v44, 0x3a800000, v230
	v_exp_f32_e32 v11, v11
	v_rcp_f32_e32 v10, v10
	v_min_f32_e32 v4, 0x40e00000, v4
	v_mul_f32_e32 v12, 0x3fd9db23, v4
	v_mul_f32_e32 v12, 0xbfb8aa3b, v12
	v_exp_f32_e32 v12, v12
	v_add_f32_e32 v11, 1.0, v11
	v_mul_f32_e32 v3, v3, v10
	v_fmamk_f32 v10, v40, 0x3a800000, v234
	v_fmamk_f32 v8, v36, 0x3a800000, v238
	v_rcp_f32_e32 v11, v11
	v_med3_f32 v10, v10, s59, v189
	v_med3_f32 v8, v8, s59, v189
	v_add_f32_e32 v10, 1.0, v10
	v_add_f32_e32 v8, 1.0, v8
	v_fmamk_f32 v13, v49, 0x3a800000, v227
	v_fmamk_f32 v5, v45, 0x3a800000, v231
	v_mul_f32_e32 v7, v7, v10
	v_add_f32_e32 v10, 1.0, v12
	v_mul_f32_e32 v4, v4, v8
	v_min_f32_e32 v8, 0x40e00000, v13
	v_min_f32_e32 v5, 0x40e00000, v5
	v_rcp_f32_e32 v10, v10
	v_mul_f32_e32 v7, v7, v11
	v_mul_f32_e32 v11, 0x3fd9db23, v8
	v_mul_f32_e32 v12, 0x3fd9db23, v5
	v_mul_f32_e32 v11, 0xbfb8aa3b, v11
	v_mul_f32_e32 v12, 0xbfb8aa3b, v12
	v_exp_f32_e32 v11, v11
	v_exp_f32_e32 v12, v12
	v_fmamk_f32 v17, v41, 0x3a800000, v235
	v_mul_f32_e32 v4, v4, v10
	v_med3_f32 v10, v17, s59, v189
	v_fmamk_f32 v9, v37, 0x3a800000, v239
	v_med3_f32 v9, v9, s59, v189
	v_add_f32_e32 v10, 1.0, v10
	v_add_f32_e32 v11, 1.0, v11
	v_mul_f32_e32 v8, v8, v10
	v_add_f32_e32 v10, 1.0, v12
	v_add_f32_e32 v9, 1.0, v9
	v_rcp_f32_e32 v11, v11
	v_rcp_f32_e32 v10, v10
	v_mul_f32_e32 v5, v5, v9
	v_mul_f32_e32 v0, 4.0, v0
	v_mul_f32_e32 v9, 4.0, v2
	v_mov_b32_e32 v2, v171
	v_cvt_pk_fp8_f32 v2, v0, v9
	v_mul_f32_e32 v0, 4.0, v6
	v_mul_f32_e32 v6, 4.0, v3
	v_mov_b32_e32 v3, v171
	v_cvt_pk_fp8_f32 v3, v0, v6
	v_mul_f32_e32 v8, v8, v11
	v_mul_f32_e32 v5, v5, v10
	v_mul_f32_e32 v7, 4.0, v7
	v_mul_f32_e32 v8, 4.0, v8
	v_mul_f32_e32 v0, 4.0, v4
	v_mul_f32_e32 v4, 4.0, v5
	v_cvt_pk_fp8_f32 v2, v7, v8 op_sel:[0,0,1]
	v_cvt_pk_fp8_f32 v3, v0, v4 op_sel:[0,0,1]
	v_add_co_u32_e32 v4, vcc, 0x58000, v18
	s_nop 1
	v_addc_co_u32_e32 v5, vcc, 0, v19, vcc
	s_andn2_b64 vcc, exec, s[4:5]
	s_mov_b64 s[4:5], -1
	global_store_dwordx2 v[4:5], v[2:3], off
	s_cbranch_vccnz .LBB0_1470
	s_andn2_b64 vcc, exec, s[12:13]
	s_cbranch_vccnz .LBB0_1469
	s_barrier
	s_branch .LBB0_1469

.LBB0_1571:
	s_ashr_i32 s0, s28, 3
	s_add_i32 s26, s30, s0
	v_and_b32_e32 v0, 63, v254
	v_lshlrev_b32_e32 v0, 2, v0
	v_add_u32_e32 v0, 0x23a00, v0
	ds_read_b32 v0, v0
	s_waitcnt lgkmcnt(0)
	v_cmp_ge_i32_e32 vcc, s26, v0
	s_nop 1
	s_and_b32 s0, vcc_lo, 0xfffffffe
	s_bcnt1_i32_b32 s27, s0
	s_lshl_b32 s0, s27, 2
	s_add_i32 s0, s0, 0
	s_add_i32 s0, s0, 0x23a00
	v_mov_b32_e32 v0, s0
	ds_read2st64_b32 v[2:3], v0 offset1:1
	ds_read_b32 v0, v0 offset:512
	s_waitcnt lgkmcnt(0)
	v_readfirstlane_b32 s0, v3
	s_abs_i32 s1, s0
	v_cvt_f32_u32_e32 v3, s1
	v_readfirstlane_b32 s2, v2
	v_readfirstlane_b32 s3, v0
	s_sub_i32 s29, 0, s1
	v_rcp_iflag_f32_e32 v2, v3
	s_sub_i32 s2, s26, s2
	s_abs_i32 s28, s2
	s_xor_b32 s26, s2, s0
	v_mul_f32_e32 v0, 0x4f7ffffe, v2
	v_cvt_u32_f32_e32 v0, v0
	s_ashr_i32 s26, s26, 31
	v_readfirstlane_b32 s30, v0
	s_mul_i32 s29, s29, s30
	s_mul_hi_u32 s29, s30, s29
	s_add_i32 s30, s30, s29
	s_mul_hi_u32 s29, s28, s30
	s_mul_i32 s30, s29, s1
	s_sub_i32 s28, s28, s30
	s_add_i32 s31, s29, 1
	s_sub_i32 s30, s28, s1
	s_cmp_ge_u32 s28, s1
	s_cselect_b32 s29, s31, s29
	s_cselect_b32 s28, s30, s28
	s_add_i32 s30, s29, 1
	s_cmp_ge_u32 s28, s1
	s_cselect_b32 s1, s30, s29
	s_xor_b32 s1, s1, s26
	s_sub_i32 s1, s1, s26
	s_mul_i32 s0, s1, s0
	s_lshl_b32 s27, s27, 3
	s_sub_i32 s0, s2, s0
	s_add_i32 s26, s0, s3
	s_add_i32 s28, s1, s27
.LBB0_1576:
	s_lshl_b32 s1, s38, 8
	s_ashr_i32 s0, s38, 3
	s_and_b32 s1, s1, 0x700
	v_or_b32_e32 v240, s1, v183
	s_ashr_i32 s1, s0, 31
	s_lshl_b64 s[0:1], s[0:1], 13
	s_add_u32 s2, s6, s0
	s_addc_u32 s3, s7, s1
	v_lshlrev_b32_e32 v240, 2, v240
	global_load_dwordx4 v[224:227], v240, s[2:3]
	global_load_dwordx4 v[228:231], v240, s[2:3] offset:16
	global_load_dwordx4 v[232:235], v240, s[2:3] offset:512
	global_load_dwordx4 v[236:239], v240, s[2:3] offset:528
	s_ashr_i32 s27, s26, 31
	s_lshl_b64 s[0:1], s[26:27], 19
	s_add_u32 s30, s49, s0
	s_addc_u32 s31, s50, s1
	s_and_b64 s[0:1], s[4:5], exec
	s_cselect_b32 s27, s31, s43
	s_cselect_b32 s39, s30, s42
	s_ashr_i32 s29, s28, 31
	s_lshl_b64 s[0:1], s[28:29], 19
	s_add_u32 s34, s51, s0
	s_addc_u32 s35, s52, s1
	s_and_b64 s[0:1], s[4:5], exec
	s_cselect_b32 s29, s35, s41
	s_cselect_b32 s68, s34, s40
	s_add_u32 s69, s40, 0x4000
	s_addc_u32 s70, s41, 0
	s_add_u32 s40, s42, 0x40080
	v_mov_b32_e32 v34, 0
	s_addc_u32 s41, s43, 0
	s_mov_b32 s71, -2
	v_mov_b32_e32 v35, v34
	v_mov_b32_e32 v36, v34
	v_mov_b32_e32 v37, v34
	v_mov_b32_e32 v38, v34
	v_mov_b32_e32 v39, v34
	v_mov_b32_e32 v40, v34
	v_mov_b32_e32 v41, v34
	v_mov_b32_e32 v42, v34
	v_mov_b32_e32 v43, v34
	v_mov_b32_e32 v44, v34
	v_mov_b32_e32 v45, v34
	v_mov_b32_e32 v46, v34
	v_mov_b32_e32 v47, v34
	v_mov_b32_e32 v48, v34
	v_mov_b32_e32 v49, v34
	v_mov_b32_e32 v50, v34
	v_mov_b32_e32 v51, v34
	v_mov_b32_e32 v52, v34
	v_mov_b32_e32 v53, v34
	v_mov_b32_e32 v54, v34
	v_mov_b32_e32 v55, v34
	v_mov_b32_e32 v56, v34
	v_mov_b32_e32 v57, v34
	v_mov_b32_e32 v58, v34
	v_mov_b32_e32 v59, v34
	v_mov_b32_e32 v60, v34
	v_mov_b32_e32 v61, v34
	v_mov_b32_e32 v62, v34
	v_mov_b32_e32 v63, v34
	v_mov_b32_e32 v64, v34
	v_mov_b32_e32 v65, v34
	v_mov_b32_e32 v90, v34
	v_mov_b32_e32 v91, v34
	v_mov_b32_e32 v92, v34
	v_mov_b32_e32 v93, v34
	v_mov_b32_e32 v94, v34
	v_mov_b32_e32 v95, v34
	v_mov_b32_e32 v96, v34
	v_mov_b32_e32 v97, v34
	v_mov_b32_e32 v106, v34
	v_mov_b32_e32 v107, v34
	v_mov_b32_e32 v108, v34
	v_mov_b32_e32 v109, v34
	v_mov_b32_e32 v110, v34
	v_mov_b32_e32 v111, v34
	v_mov_b32_e32 v112, v34
	v_mov_b32_e32 v113, v34
	v_mov_b32_e32 v114, v34
	v_mov_b32_e32 v115, v34
	v_mov_b32_e32 v116, v34
	v_mov_b32_e32 v117, v34
	v_mov_b32_e32 v118, v34
	v_mov_b32_e32 v119, v34
	v_mov_b32_e32 v120, v34
	v_mov_b32_e32 v121, v34
	v_mov_b32_e32 v122, v34
	v_mov_b32_e32 v123, v34
	v_mov_b32_e32 v124, v34
	v_mov_b32_e32 v125, v34
	v_mov_b32_e32 v126, v34
	v_mov_b32_e32 v127, v34
	v_mov_b32_e32 v128, v34
	v_mov_b32_e32 v129, v34
	v_mov_b32_e32 v66, v34
	v_mov_b32_e32 v67, v34
	v_mov_b32_e32 v68, v34
	v_mov_b32_e32 v69, v34
	v_mov_b32_e32 v70, v34
	v_mov_b32_e32 v71, v34
	v_mov_b32_e32 v72, v34
	v_mov_b32_e32 v73, v34
	v_mov_b32_e32 v74, v34
	v_mov_b32_e32 v75, v34
	v_mov_b32_e32 v76, v34
	v_mov_b32_e32 v77, v34
	v_mov_b32_e32 v78, v34
	v_mov_b32_e32 v79, v34
	v_mov_b32_e32 v80, v34
	v_mov_b32_e32 v81, v34
	v_mov_b32_e32 v82, v34
	v_mov_b32_e32 v83, v34
	v_mov_b32_e32 v84, v34
	v_mov_b32_e32 v85, v34
	v_mov_b32_e32 v86, v34
	v_mov_b32_e32 v87, v34
	v_mov_b32_e32 v88, v34
	v_mov_b32_e32 v89, v34
	v_mov_b32_e32 v98, v34
	v_mov_b32_e32 v99, v34
	v_mov_b32_e32 v100, v34
	v_mov_b32_e32 v101, v34
	v_mov_b32_e32 v102, v34
	v_mov_b32_e32 v103, v34
	v_mov_b32_e32 v104, v34
	v_mov_b32_e32 v105, v34
	v_mov_b32_e32 v130, v34
	v_mov_b32_e32 v131, v34
	v_mov_b32_e32 v132, v34
	v_mov_b32_e32 v133, v34
	v_mov_b32_e32 v134, v34
	v_mov_b32_e32 v135, v34
	v_mov_b32_e32 v136, v34
	v_mov_b32_e32 v137, v34
	v_mov_b32_e32 v138, v34
	v_mov_b32_e32 v139, v34
	v_mov_b32_e32 v140, v34
	v_mov_b32_e32 v141, v34
	v_mov_b32_e32 v142, v34
	v_mov_b32_e32 v143, v34
	v_mov_b32_e32 v144, v34
	v_mov_b32_e32 v145, v34
	v_mov_b32_e32 v146, v34
	v_mov_b32_e32 v147, v34
	v_mov_b32_e32 v148, v34
	v_mov_b32_e32 v149, v34
	v_mov_b32_e32 v150, v34
	v_mov_b32_e32 v151, v34
	v_mov_b32_e32 v152, v34
	v_mov_b32_e32 v153, v34
	v_mov_b32_e32 v154, v34
	v_mov_b32_e32 v155, v34
	v_mov_b32_e32 v156, v34
	v_mov_b32_e32 v157, v34
	v_mov_b32_e32 v158, v34
	v_mov_b32_e32 v159, v34
	v_mov_b32_e32 v160, v34
	v_mov_b32_e32 v161, v34

.LBB0_1580:
	s_lshl_b32 s1, s38, 8
	s_ashr_i32 s0, s38, 3
	s_and_b32 s1, s1, 0x700
	v_or_b32_e32 v170, s1, v183
	s_nop 15
	s_nop 15
	s_nop 15
	s_nop 15
	s_nop 15
	v_mov_b32_e32 v16, v171
	v_mov_b32_e32 v17, v171
	v_mov_b32_e32 v18, v171
	v_mov_b32_e32 v19, v171
	v_mov_b32_e32 v20, v171
	v_mov_b32_e32 v21, v171
	v_lshl_add_u32 v10, s36, 8, v1
	v_ashrrev_i32_e32 v11, 31, v10
	v_or_b32_e32 v12, 16, v10
	v_or_b32_e32 v14, 32, v10
	v_or_b32_e32 v24, 48, v10
	v_lshlrev_b64 v[10:11], 11, v[10:11]
	v_ashrrev_i32_e32 v13, 31, v12
	v_ashrrev_i32_e32 v15, 31, v14
	v_lshl_add_u64 v[10:11], s[12:13], 0, v[10:11]
	v_lshlrev_b64 v[12:13], 11, v[12:13]
	v_lshlrev_b64 v[14:15], 11, v[14:15]
	v_lshl_add_u64 v[10:11], v[10:11], 0, v[170:171]
	v_lshl_add_u64 v[12:13], s[12:13], 0, v[12:13]
	v_lshl_add_u64 v[14:15], s[12:13], 0, v[14:15]
	v_mov_b32_e32 v22, v171
	v_lshl_add_u64 v[12:13], v[12:13], 0, v[170:171]
	v_lshl_add_u64 v[14:15], v[14:15], 0, v[170:171]
	v_pk_fma_f32 v[28:29], v[158:159], s[18:19], v[224:225] op_sel_hi:[1,0,1]
	v_pk_fma_f32 v[32:33], v[154:155], s[18:19], v[228:229] op_sel_hi:[1,0,1]
	v_pk_fma_f32 v[150:151], v[150:151], s[18:19], v[224:225] op_sel_hi:[1,0,1]
	v_pk_fma_f32 v[146:147], v[146:147], s[18:19], v[228:229] op_sel_hi:[1,0,1]
	v_mul_f32_e32 v23, 0x41800000, v28
	v_mul_f32_e32 v25, 0x41800000, v29
	v_mul_f32_e32 v28, 0x41800000, v32
	v_mul_f32_e32 v29, 0x41800000, v33
	v_pk_fma_f32 v[142:143], v[142:143], s[18:19], v[224:225] op_sel_hi:[1,0,1]
	v_pk_fma_f32 v[138:139], v[138:139], s[18:19], v[228:229] op_sel_hi:[1,0,1]
	v_mul_f32_e32 v32, 0x41800000, v150
	v_mul_f32_e32 v33, 0x41800000, v151
	v_mul_f32_e32 v146, 0x41800000, v146
	v_mul_f32_e32 v147, 0x41800000, v147
	v_cvt_pk_fp8_f32 v16, v23, v25
	v_cvt_pk_fp8_f32 v17, v28, v29
	v_mul_f32_e32 v142, 0x41800000, v142
	v_mul_f32_e32 v143, 0x41800000, v143
	v_mul_f32_e32 v138, 0x41800000, v138
	v_mul_f32_e32 v139, 0x41800000, v139
	v_cvt_pk_fp8_f32 v18, v32, v33
	v_cvt_pk_fp8_f32 v19, v146, v147
	v_pk_fma_f32 v[26:27], v[160:161], s[18:19], v[226:227] op_sel_hi:[1,0,1]
	v_pk_fma_f32 v[30:31], v[156:157], s[18:19], v[230:231] op_sel_hi:[1,0,1]
	v_cvt_pk_fp8_f32 v20, v142, v143
	v_cvt_pk_fp8_f32 v21, v138, v139
	v_pk_fma_f32 v[152:153], v[152:153], s[18:19], v[226:227] op_sel_hi:[1,0,1]
	v_pk_fma_f32 v[148:149], v[148:149], s[18:19], v[230:231] op_sel_hi:[1,0,1]
	v_mul_f32_e32 v26, 0x41800000, v26
	v_mul_f32_e32 v27, 0x41800000, v27
	v_mul_f32_e32 v30, 0x41800000, v30
	v_mul_f32_e32 v31, 0x41800000, v31
	v_pk_fma_f32 v[144:145], v[144:145], s[18:19], v[226:227] op_sel_hi:[1,0,1]
	v_pk_fma_f32 v[140:141], v[140:141], s[18:19], v[230:231] op_sel_hi:[1,0,1]
	v_mul_f32_e32 v150, 0x41800000, v152
	v_mul_f32_e32 v151, 0x41800000, v153
	v_mul_f32_e32 v148, 0x41800000, v148
	v_mul_f32_e32 v149, 0x41800000, v149
	v_cvt_pk_fp8_f32 v16, v26, v27 op_sel:[0,0,1]
	v_cvt_pk_fp8_f32 v17, v30, v31 op_sel:[0,0,1]
	v_mul_f32_e32 v144, 0x41800000, v144
	v_mul_f32_e32 v145, 0x41800000, v145
	v_mul_f32_e32 v140, 0x41800000, v140
	v_mul_f32_e32 v141, 0x41800000, v141
	v_cvt_pk_fp8_f32 v18, v150, v151 op_sel:[0,0,1]
	v_cvt_pk_fp8_f32 v19, v148, v149 op_sel:[0,0,1]
	v_cvt_pk_fp8_f32 v20, v144, v145 op_sel:[0,0,1]
	v_cvt_pk_fp8_f32 v21, v140, v141 op_sel:[0,0,1]
	v_pk_fma_f32 v[134:135], v[134:135], s[18:19], v[224:225] op_sel_hi:[1,0,1]
	v_pk_fma_f32 v[130:131], v[130:131], s[18:19], v[228:229] op_sel_hi:[1,0,1]
	v_mul_f32_e32 v134, 0x41800000, v134
	v_mul_f32_e32 v135, 0x41800000, v135
	v_mul_f32_e32 v130, 0x41800000, v130
	global_store_dwordx2 v[10:11], v[16:17], off
	global_store_dwordx2 v[12:13], v[18:19], off
	global_store_dwordx2 v[14:15], v[20:21], off
	v_mul_f32_e32 v16, 0x41800000, v131
	v_mov_b32_e32 v23, v171
	v_cvt_pk_fp8_f32 v22, v134, v135
	v_cvt_pk_fp8_f32 v23, v130, v16
	v_pk_fma_f32 v[136:137], v[136:137], s[18:19], v[226:227] op_sel_hi:[1,0,1]
	v_pk_fma_f32 v[132:133], v[132:133], s[18:19], v[230:231] op_sel_hi:[1,0,1]
	v_mul_f32_e32 v136, 0x41800000, v136
	v_mul_f32_e32 v137, 0x41800000, v137
	v_mul_f32_e32 v16, 0x41800000, v132
	v_mul_f32_e32 v17, 0x41800000, v133
	v_ashrrev_i32_e32 v25, 31, v24
	v_pk_fma_f32 v[18:19], v[128:129], s[18:19], v[226:227] op_sel_hi:[1,0,1]
	v_pk_fma_f32 v[20:21], v[126:127], s[18:19], v[224:225] op_sel_hi:[1,0,1]
	v_cvt_pk_fp8_f32 v22, v136, v137 op_sel:[0,0,1]
	v_cvt_pk_fp8_f32 v23, v16, v17 op_sel:[0,0,1]
	v_lshlrev_b64 v[16:17], 11, v[24:25]
	v_pk_fma_f32 v[24:25], v[122:123], s[18:19], v[228:229] op_sel_hi:[1,0,1]
	v_mul_f32_e32 v20, 0x41800000, v20
	v_mul_f32_e32 v21, 0x41800000, v21
	v_mul_f32_e32 v26, 0x41800000, v18
	v_mov_b32_e32 v18, v171
	v_mul_f32_e32 v27, 0x41800000, v19
	v_cvt_pk_fp8_f32 v18, v20, v21
	v_mul_f32_e32 v20, 0x41800000, v24
	v_mul_f32_e32 v21, 0x41800000, v25
	v_mov_b32_e32 v19, v171
	v_lshl_add_u64 v[16:17], s[12:13], 0, v[16:17]
	v_cvt_pk_fp8_f32 v19, v20, v21
	v_lshl_add_u64 v[16:17], v[16:17], 0, v[170:171]
	global_store_dwordx2 v[16:17], v[22:23], off
	v_pk_fma_f32 v[22:23], v[124:125], s[18:19], v[230:231] op_sel_hi:[1,0,1]
	v_cvt_pk_fp8_f32 v18, v26, v27 op_sel:[0,0,1]
	v_mul_f32_e32 v20, 0x41800000, v22
	v_mul_f32_e32 v21, 0x41800000, v23
	v_cvt_pk_fp8_f32 v19, v20, v21 op_sel:[0,0,1]
	v_add_co_u32_e32 v20, vcc, s64, v10
	v_pk_fma_f32 v[24:25], v[114:115], s[18:19], v[228:229] op_sel_hi:[1,0,1]
	s_nop 0
	v_addc_co_u32_e32 v21, vcc, 0, v11, vcc
	global_store_dwordx2 v[20:21], v[18:19], off
	v_pk_fma_f32 v[18:19], v[120:121], s[18:19], v[226:227] op_sel_hi:[1,0,1]
	v_pk_fma_f32 v[20:21], v[118:119], s[18:19], v[224:225] op_sel_hi:[1,0,1]
	v_mul_f32_e32 v26, 0x41800000, v18
	v_mul_f32_e32 v20, 0x41800000, v20
	v_mul_f32_e32 v21, 0x41800000, v21
	v_mov_b32_e32 v18, v171
	v_mul_f32_e32 v27, 0x41800000, v19
	v_cvt_pk_fp8_f32 v18, v20, v21
	v_mul_f32_e32 v20, 0x41800000, v24
	v_mul_f32_e32 v21, 0x41800000, v25
	v_mov_b32_e32 v19, v171
	v_cvt_pk_fp8_f32 v19, v20, v21
	v_pk_fma_f32 v[22:23], v[116:117], s[18:19], v[230:231] op_sel_hi:[1,0,1]
	v_cvt_pk_fp8_f32 v18, v26, v27 op_sel:[0,0,1]
	v_mul_f32_e32 v20, 0x41800000, v22
	v_mul_f32_e32 v21, 0x41800000, v23
	v_cvt_pk_fp8_f32 v19, v20, v21 op_sel:[0,0,1]
	v_add_co_u32_e32 v20, vcc, s65, v10
	v_pk_fma_f32 v[24:25], v[106:107], s[18:19], v[228:229] op_sel_hi:[1,0,1]
	s_nop 0
	v_addc_co_u32_e32 v21, vcc, 0, v11, vcc
	global_store_dwordx2 v[20:21], v[18:19], off
	v_pk_fma_f32 v[18:19], v[112:113], s[18:19], v[226:227] op_sel_hi:[1,0,1]
	v_pk_fma_f32 v[20:21], v[110:111], s[18:19], v[224:225] op_sel_hi:[1,0,1]
	v_mul_f32_e32 v26, 0x41800000, v18
	v_mul_f32_e32 v20, 0x41800000, v20
	v_mul_f32_e32 v21, 0x41800000, v21
	v_mov_b32_e32 v18, v171
	v_mul_f32_e32 v27, 0x41800000, v19
	v_cvt_pk_fp8_f32 v18, v20, v21
	v_mul_f32_e32 v20, 0x41800000, v24
	v_mul_f32_e32 v21, 0x41800000, v25
	v_mov_b32_e32 v19, v171
	v_cvt_pk_fp8_f32 v19, v20, v21
	v_pk_fma_f32 v[22:23], v[108:109], s[18:19], v[230:231] op_sel_hi:[1,0,1]
	v_cvt_pk_fp8_f32 v18, v26, v27 op_sel:[0,0,1]
	v_mul_f32_e32 v20, 0x41800000, v22
	v_mul_f32_e32 v21, 0x41800000, v23
	v_cvt_pk_fp8_f32 v19, v20, v21 op_sel:[0,0,1]
	v_add_co_u32_e32 v20, vcc, s66, v10
	v_pk_fma_f32 v[6:7], v[94:95], s[18:19], v[224:225] op_sel_hi:[1,0,1]
	s_nop 0
	v_addc_co_u32_e32 v21, vcc, 0, v11, vcc
	global_store_dwordx2 v[20:21], v[18:19], off
	v_pk_fma_f32 v[2:3], v[90:91], s[18:19], v[228:229] op_sel_hi:[1,0,1]
	v_mul_f32_e32 v18, 0x41800000, v6
	v_mul_f32_e32 v7, 0x41800000, v7
	v_mov_b32_e32 v6, v171
	v_cvt_pk_fp8_f32 v6, v18, v7
	v_mul_f32_e32 v2, 0x41800000, v2
	v_mul_f32_e32 v3, 0x41800000, v3
	v_mov_b32_e32 v7, v171
	v_cvt_pk_fp8_f32 v7, v2, v3
	v_pk_fma_f32 v[8:9], v[96:97], s[18:19], v[226:227] op_sel_hi:[1,0,1]
	v_pk_fma_f32 v[4:5], v[92:93], s[18:19], v[230:231] op_sel_hi:[1,0,1]
	v_mul_f32_e32 v8, 0x41800000, v8
	v_mul_f32_e32 v9, 0x41800000, v9
	v_mul_f32_e32 v2, 0x41800000, v4
	v_mul_f32_e32 v3, 0x41800000, v5
	v_cvt_pk_fp8_f32 v6, v8, v9 op_sel:[0,0,1]
	v_cvt_pk_fp8_f32 v7, v2, v3 op_sel:[0,0,1]
	v_add_co_u32_e32 v2, vcc, s67, v10
	v_lshl_add_u64 v[18:19], v[10:11], 0, s[8:9]
	s_nop 0
	v_addc_co_u32_e32 v3, vcc, 0, v11, vcc
	global_store_dwordx2 v[2:3], v[6:7], off
	s_nop 0
	v_lshl_add_u64 v[20:21], v[10:11], 0, s[20:21]
	v_lshl_add_u64 v[22:23], v[10:11], 0, s[22:23]
	v_lshl_add_u64 v[24:25], v[10:11], 0, s[24:25]
	s_andn2_b64 vcc, exec, s[4:5]
	s_mov_b64 s[4:5], -1
	v_pk_fma_f32 v[26:27], v[104:105], s[18:19], v[234:235] op_sel_hi:[1,0,1]
	v_pk_fma_f32 v[28:29], v[102:103], s[18:19], v[232:233] op_sel_hi:[1,0,1]
	v_pk_fma_f32 v[32:33], v[98:99], s[18:19], v[236:237] op_sel_hi:[1,0,1]
	v_mul_f32_e32 v0, 0x41800000, v28
	v_mul_f32_e32 v28, 0x41800000, v29
	v_mul_f32_e32 v29, 0x41800000, v26
	v_mov_b32_e32 v26, v171
	v_mul_f32_e32 v90, 0x41800000, v27
	v_cvt_pk_fp8_f32 v26, v0, v28
	v_mul_f32_e32 v0, 0x41800000, v32
	v_mul_f32_e32 v28, 0x41800000, v33
	v_mov_b32_e32 v27, v171
	v_cvt_pk_fp8_f32 v27, v0, v28
	v_pk_fma_f32 v[30:31], v[100:101], s[18:19], v[238:239] op_sel_hi:[1,0,1]
	v_cvt_pk_fp8_f32 v26, v29, v90 op_sel:[0,0,1]
	v_mul_f32_e32 v0, 0x41800000, v30
	v_mul_f32_e32 v28, 0x41800000, v31
	v_cvt_pk_fp8_f32 v27, v0, v28 op_sel:[0,0,1]
	v_pk_fma_f32 v[28:29], v[88:89], s[18:19], v[234:235] op_sel_hi:[1,0,1]
	v_pk_fma_f32 v[30:31], v[86:87], s[18:19], v[232:233] op_sel_hi:[1,0,1]
	v_pk_fma_f32 v[82:83], v[82:83], s[18:19], v[236:237] op_sel_hi:[1,0,1]
	v_mul_f32_e32 v0, 0x41800000, v30
	v_mul_f32_e32 v30, 0x41800000, v31
	v_mul_f32_e32 v31, 0x41800000, v28
	v_mov_b32_e32 v28, v171
	v_pk_fma_f32 v[32:33], v[84:85], s[18:19], v[238:239] op_sel_hi:[1,0,1]
	v_mul_f32_e32 v84, 0x41800000, v29
	v_cvt_pk_fp8_f32 v28, v0, v30
	v_mul_f32_e32 v0, 0x41800000, v82
	v_mul_f32_e32 v30, 0x41800000, v83
	v_mov_b32_e32 v29, v171
	v_cvt_pk_fp8_f32 v29, v0, v30
	v_mul_f32_e32 v0, 0x41800000, v32
	v_mul_f32_e32 v30, 0x41800000, v33
	v_cvt_pk_fp8_f32 v28, v31, v84 op_sel:[0,0,1]
	v_cvt_pk_fp8_f32 v29, v0, v30 op_sel:[0,0,1]
	v_pk_fma_f32 v[30:31], v[80:81], s[18:19], v[234:235] op_sel_hi:[1,0,1]
	v_pk_fma_f32 v[32:33], v[78:79], s[18:19], v[232:233] op_sel_hi:[1,0,1]
	v_pk_fma_f32 v[74:75], v[74:75], s[18:19], v[236:237] op_sel_hi:[1,0,1]
	v_mul_f32_e32 v0, 0x41800000, v32
	v_mul_f32_e32 v32, 0x41800000, v33
	v_mul_f32_e32 v33, 0x41800000, v30
	v_mov_b32_e32 v30, v171
	v_mul_f32_e32 v78, 0x41800000, v31
	v_cvt_pk_fp8_f32 v30, v0, v32
	v_mul_f32_e32 v0, 0x41800000, v74
	v_mul_f32_e32 v32, 0x41800000, v75
	v_mov_b32_e32 v31, v171
	v_cvt_pk_fp8_f32 v31, v0, v32
	v_pk_fma_f32 v[76:77], v[76:77], s[18:19], v[238:239] op_sel_hi:[1,0,1]
	v_cvt_pk_fp8_f32 v30, v33, v78 op_sel:[0,0,1]
	v_mul_f32_e32 v0, 0x41800000, v76
	v_mul_f32_e32 v32, 0x41800000, v77
	v_cvt_pk_fp8_f32 v31, v0, v32 op_sel:[0,0,1]
	v_pk_fma_f32 v[32:33], v[72:73], s[18:19], v[234:235] op_sel_hi:[1,0,1]
	v_pk_fma_f32 v[70:71], v[70:71], s[18:19], v[232:233] op_sel_hi:[1,0,1]
	v_pk_fma_f32 v[66:67], v[66:67], s[18:19], v[236:237] op_sel_hi:[1,0,1]
	v_mul_f32_e32 v0, 0x41800000, v70
	v_mul_f32_e32 v70, 0x41800000, v71
	v_mul_f32_e32 v71, 0x41800000, v32
	v_mov_b32_e32 v32, v171
	v_mul_f32_e32 v72, 0x41800000, v33
	v_cvt_pk_fp8_f32 v32, v0, v70
	v_mul_f32_e32 v0, 0x41800000, v66
	v_mul_f32_e32 v66, 0x41800000, v67
	v_mov_b32_e32 v33, v171
	v_cvt_pk_fp8_f32 v33, v0, v66
	v_pk_fma_f32 v[68:69], v[68:69], s[18:19], v[238:239] op_sel_hi:[1,0,1]
	v_cvt_pk_fp8_f32 v32, v71, v72 op_sel:[0,0,1]
	v_mul_f32_e32 v0, 0x41800000, v68
	v_mul_f32_e32 v66, 0x41800000, v69
	v_cvt_pk_fp8_f32 v33, v0, v66 op_sel:[0,0,1]
	global_store_dwordx2 v[10:11], v[26:27], off offset:128
	global_store_dwordx2 v[12:13], v[28:29], off offset:128
	global_store_dwordx2 v[14:15], v[30:31], off offset:128
	global_store_dwordx2 v[16:17], v[32:33], off offset:128
	v_pk_fma_f32 v[10:11], v[64:65], s[18:19], v[234:235] op_sel_hi:[1,0,1]
	v_pk_fma_f32 v[12:13], v[62:63], s[18:19], v[232:233] op_sel_hi:[1,0,1]
	v_pk_fma_f32 v[16:17], v[58:59], s[18:19], v[236:237] op_sel_hi:[1,0,1]
	v_mul_f32_e32 v0, 0x41800000, v12
	v_mul_f32_e32 v12, 0x41800000, v13
	v_mul_f32_e32 v13, 0x41800000, v10
	v_mov_b32_e32 v10, v171
	v_mul_f32_e32 v26, 0x41800000, v11
	v_cvt_pk_fp8_f32 v10, v0, v12
	v_mul_f32_e32 v0, 0x41800000, v16
	v_mul_f32_e32 v12, 0x41800000, v17
	v_mov_b32_e32 v11, v171
	v_cvt_pk_fp8_f32 v11, v0, v12
	v_pk_fma_f32 v[14:15], v[60:61], s[18:19], v[238:239] op_sel_hi:[1,0,1]
	v_cvt_pk_fp8_f32 v10, v13, v26 op_sel:[0,0,1]
	v_mul_f32_e32 v0, 0x41800000, v14
	v_mul_f32_e32 v12, 0x41800000, v15
	v_cvt_pk_fp8_f32 v11, v0, v12 op_sel:[0,0,1]
	v_pk_fma_f32 v[12:13], v[56:57], s[18:19], v[234:235] op_sel_hi:[1,0,1]
	v_pk_fma_f32 v[14:15], v[54:55], s[18:19], v[232:233] op_sel_hi:[1,0,1]
	v_pk_fma_f32 v[26:27], v[50:51], s[18:19], v[236:237] op_sel_hi:[1,0,1]
	v_mul_f32_e32 v0, 0x41800000, v14
	v_mul_f32_e32 v14, 0x41800000, v15
	v_mul_f32_e32 v15, 0x41800000, v12
	v_mov_b32_e32 v12, v171
	v_mul_f32_e32 v28, 0x41800000, v13
	v_cvt_pk_fp8_f32 v12, v0, v14
	v_mul_f32_e32 v0, 0x41800000, v26
	v_mul_f32_e32 v14, 0x41800000, v27
	v_mov_b32_e32 v13, v171
	v_cvt_pk_fp8_f32 v13, v0, v14
	v_pk_fma_f32 v[16:17], v[52:53], s[18:19], v[238:239] op_sel_hi:[1,0,1]
	v_cvt_pk_fp8_f32 v12, v15, v28 op_sel:[0,0,1]
	v_mul_f32_e32 v0, 0x41800000, v16
	v_mul_f32_e32 v14, 0x41800000, v17
	v_cvt_pk_fp8_f32 v13, v0, v14 op_sel:[0,0,1]
	v_pk_fma_f32 v[14:15], v[48:49], s[18:19], v[234:235] op_sel_hi:[1,0,1]
	v_pk_fma_f32 v[16:17], v[46:47], s[18:19], v[232:233] op_sel_hi:[1,0,1]
	v_pk_fma_f32 v[28:29], v[42:43], s[18:19], v[236:237] op_sel_hi:[1,0,1]
	v_mul_f32_e32 v0, 0x41800000, v16
	v_mul_f32_e32 v16, 0x41800000, v17
	v_mul_f32_e32 v17, 0x41800000, v14
	v_mov_b32_e32 v14, v171
	v_mul_f32_e32 v30, 0x41800000, v15
	v_cvt_pk_fp8_f32 v14, v0, v16
	v_mul_f32_e32 v0, 0x41800000, v28
	v_mul_f32_e32 v16, 0x41800000, v29
	v_mov_b32_e32 v15, v171
	v_cvt_pk_fp8_f32 v15, v0, v16
	v_pk_fma_f32 v[26:27], v[44:45], s[18:19], v[238:239] op_sel_hi:[1,0,1]
	v_pk_fma_f32 v[2:3], v[38:39], s[18:19], v[232:233] op_sel_hi:[1,0,1]
	v_mul_f32_e32 v0, 0x41800000, v26
	v_mul_f32_e32 v16, 0x41800000, v27
	v_cvt_pk_fp8_f32 v15, v0, v16 op_sel:[0,0,1]
	v_pk_fma_f32 v[6:7], v[34:35], s[18:19], v[236:237] op_sel_hi:[1,0,1]
	v_mul_f32_e32 v0, 0x41800000, v2
	v_mul_f32_e32 v3, 0x41800000, v3
	v_mov_b32_e32 v2, v171
	v_cvt_pk_fp8_f32 v2, v0, v3
	v_mul_f32_e32 v0, 0x41800000, v6
	v_mul_f32_e32 v6, 0x41800000, v7
	v_mov_b32_e32 v3, v171
	v_cvt_pk_fp8_f32 v3, v0, v6
	v_pk_fma_f32 v[4:5], v[40:41], s[18:19], v[234:235] op_sel_hi:[1,0,1]
	v_pk_fma_f32 v[8:9], v[36:37], s[18:19], v[238:239] op_sel_hi:[1,0,1]
	v_mul_f32_e32 v4, 0x41800000, v4
	v_mul_f32_e32 v5, 0x41800000, v5
	v_cvt_pk_fp8_f32 v14, v17, v30 op_sel:[0,0,1]
	v_cvt_pk_fp8_f32 v2, v4, v5 op_sel:[0,0,1]
	v_mul_f32_e32 v0, 0x41800000, v8
	v_mul_f32_e32 v4, 0x41800000, v9
	v_cvt_pk_fp8_f32 v3, v0, v4 op_sel:[0,0,1]
	global_store_dwordx2 v[18:19], v[10:11], off offset:128
	global_store_dwordx2 v[20:21], v[12:13], off offset:128
	global_store_dwordx2 v[22:23], v[14:15], off offset:128
	global_store_dwordx2 v[24:25], v[2:3], off offset:128
	s_cbranch_vccnz .LBB0_1565
	s_andn2_b64 vcc, exec, s[10:11]
	s_cbranch_vccnz .LBB0_1564
	s_barrier
	s_branch .LBB0_1564
